# bf16 RNE pack -> v_cvt_pk_bf16_f32 in all row/scan/prep phases (191 sites), scan waves 4-7 prio 2
# speedup vs baseline: 1.0059x; 1.0036x over previous
.LBB0_307:
	s_waitcnt vmcnt(0)
	v_lshlrev_b32_e32 v76, 16, v9
	v_lshlrev_b32_e32 v75, 16, v5
	v_mul_f32_e32 v79, v71, v76
	v_lshlrev_b32_e32 v78, 16, v17
	v_fma_f32 v79, v70, v75, -v79
	v_mul_f32_e32 v70, v70, v76
	v_lshlrev_b32_e32 v77, 16, v13
	v_fmac_f32_e32 v70, v71, v75
	v_mul_f32_e32 v71, v69, v78
	v_fma_f32 v71, v68, v77, -v71
	v_mul_f32_e32 v68, v68, v78
	v_lshlrev_b32_e32 v75, 16, v8
	v_fmac_f32_e32 v68, v69, v77
	v_lshlrev_b32_e32 v69, 16, v4
	v_mul_f32_e32 v78, v65, v75
	v_lshlrev_b32_e32 v77, 16, v16
	v_fma_f32 v78, v64, v69, -v78
	v_mul_f32_e32 v64, v64, v75
	v_lshlrev_b32_e32 v76, 16, v12
	v_fmac_f32_e32 v64, v65, v69
	v_mul_f32_e32 v65, v63, v77
	v_fma_f32 v65, v62, v76, -v65
	v_mul_f32_e32 v62, v62, v77
	v_and_b32_e32 v8, 0xffff0000, v8
	v_fmac_f32_e32 v62, v63, v76
	v_and_b32_e32 v4, 0xffff0000, v4
	v_and_b32_e32 v16, 0xffff0000, v16
	v_mul_f32_e32 v63, v67, v8
	v_mul_f32_e32 v8, v66, v8
	v_and_b32_e32 v12, 0xffff0000, v12
	v_fma_f32 v63, v66, v4, -v63
	v_fmac_f32_e32 v8, v67, v4
	v_mul_f32_e32 v4, v61, v16
	v_fma_f32 v4, v60, v12, -v4
	v_mul_f32_e32 v66, 0x3d800000, v4
	v_mul_f32_e32 v4, v60, v16
	v_mul_f32_e32 v78, 0x3d800000, v78
	v_fmac_f32_e32 v4, v61, v12
	v_mul_f32_e32 v63, 0x3d800000, v63
	v_mul_f32_e32 v16, 0x3d800000, v4
	v_mul_f32_e32 v64, 0x3d800000, v64
	v_mul_f32_e32 v8, 0x3d800000, v8
	v_cvt_pk_bf16_f32 v4, v78, v63
	v_bfe_u32 v12, v64, 16, 1
	v_add3_u32 v12, v64, v12, s44
	v_bfe_u32 v60, v8, 16, 1
	v_mul_f32_e32 v65, 0x3d800000, v65
	v_lshrrev_b32_e32 v12, 16, v12
	v_add3_u32 v8, v8, v60, s44
	v_and_or_b32 v8, v8, s43, v12
	v_mul_f32_e32 v62, 0x3d800000, v62
	v_cvt_pk_bf16_f32 v12, v65, v66
	v_bfe_u32 v60, v62, 16, 1
	v_add3_u32 v60, v62, v60, s44
	v_bfe_u32 v61, v16, 16, 1
	v_lshrrev_b32_e32 v60, 16, v60
	v_add3_u32 v16, v16, v61, s44
	v_and_b32_e32 v61, 0xffff0000, v9
	v_lshlrev_b32_e32 v9, 16, v7
	v_and_or_b32 v16, v16, s43, v60
	v_and_b32_e32 v60, 0xffff0000, v5
	v_lshlrev_b32_e32 v5, 16, v3
	v_mul_f32_e32 v64, v33, v9
	v_mul_f32_e32 v9, v32, v9
	v_and_b32_e32 v63, 0xffff0000, v17
	v_lshlrev_b32_e32 v17, 16, v15
	v_fmac_f32_e32 v9, v33, v5
	v_and_b32_e32 v62, 0xffff0000, v13
	v_lshlrev_b32_e32 v13, 16, v11
	v_fma_f32 v64, v32, v5, -v64
	v_mul_f32_e32 v5, 0x3d800000, v9
	v_mul_f32_e32 v9, v31, v17
	v_mul_f32_e32 v17, v30, v17
	v_fmac_f32_e32 v17, v31, v13
	v_and_b32_e32 v7, 0xffff0000, v7
	v_fma_f32 v9, v30, v13, -v9
	v_mul_f32_e32 v13, 0x3d800000, v17
	v_and_b32_e32 v3, 0xffff0000, v3
	v_and_b32_e32 v15, 0xffff0000, v15
	v_mul_f32_e32 v17, v57, v7
	v_mul_f32_e32 v7, v56, v7
	v_and_b32_e32 v11, 0xffff0000, v11
	v_fma_f32 v17, v56, v3, -v17
	v_fmac_f32_e32 v7, v57, v3
	v_mul_f32_e32 v3, v27, v15
	v_fma_f32 v3, v26, v11, -v3
	v_mul_f32_e32 v30, 0x3d800000, v3
	v_mul_f32_e32 v3, v26, v15
	v_mul_f32_e32 v64, 0x3d800000, v64
	v_fmac_f32_e32 v3, v27, v11
	v_mul_f32_e32 v17, 0x3d800000, v17
	v_mul_f32_e32 v15, 0x3d800000, v3
	v_mul_f32_e32 v7, 0x3d800000, v7
	v_cvt_pk_bf16_f32 v3, v64, v17
	v_bfe_u32 v11, v5, 16, 1
	v_add3_u32 v5, v5, v11, s44
	v_bfe_u32 v11, v7, 16, 1
	v_mul_f32_e32 v9, 0x3d800000, v9
	v_lshrrev_b32_e32 v5, 16, v5
	v_add3_u32 v7, v7, v11, s44
	v_and_or_b32 v7, v7, s43, v5
	v_bfe_u32 v5, v9, 16, 1
	v_add3_u32 v5, v9, v5, s44
	v_bfe_u32 v9, v30, 16, 1
	v_lshrrev_b32_e32 v5, 16, v5
	v_add3_u32 v9, v30, v9, s44
	v_and_or_b32 v11, v9, s43, v5
	v_cvt_pk_bf16_f32 v15, v13, v15
	v_lshlrev_b32_e32 v9, 16, v6
	v_lshlrev_b32_e32 v5, 16, v2
	v_mul_f32_e32 v26, v23, v9
	v_mul_f32_e32 v9, v22, v9
	v_lshlrev_b32_e32 v17, 16, v14
	v_fmac_f32_e32 v9, v23, v5
	v_lshlrev_b32_e32 v13, 16, v10
	v_fma_f32 v26, v22, v5, -v26
	v_mul_f32_e32 v5, 0x3d800000, v9
	v_mul_f32_e32 v9, v21, v17
	v_mul_f32_e32 v17, v20, v17
	v_fmac_f32_e32 v17, v21, v13
	v_and_b32_e32 v6, 0xffff0000, v6
	v_fma_f32 v9, v20, v13, -v9
	v_mul_f32_e32 v13, 0x3d800000, v17
	v_and_b32_e32 v2, 0xffff0000, v2
	v_and_b32_e32 v14, 0xffff0000, v14
	v_mul_f32_e32 v17, v25, v6
	v_mul_f32_e32 v6, v24, v6
	v_and_b32_e32 v10, 0xffff0000, v10
	v_fma_f32 v17, v24, v2, -v17
	v_fmac_f32_e32 v6, v25, v2
	v_mul_f32_e32 v2, v19, v14
	v_fma_f32 v2, v18, v10, -v2
	v_mul_f32_e32 v20, 0x3d800000, v2
	v_mul_f32_e32 v2, v18, v14
	v_mul_f32_e32 v26, 0x3d800000, v26
	v_fmac_f32_e32 v2, v19, v10
	v_mul_f32_e32 v17, 0x3d800000, v17
	v_mul_f32_e32 v14, 0x3d800000, v2
	v_mul_f32_e32 v6, 0x3d800000, v6
	v_cvt_pk_bf16_f32 v2, v26, v17
	v_bfe_u32 v10, v5, 16, 1
	v_add3_u32 v5, v5, v10, s44
	v_bfe_u32 v10, v6, 16, 1
	v_mul_f32_e32 v9, 0x3d800000, v9
	v_lshrrev_b32_e32 v5, 16, v5
	v_add3_u32 v6, v6, v10, s44
	v_and_or_b32 v6, v6, s43, v5
	v_bfe_u32 v5, v9, 16, 1
	v_add3_u32 v5, v9, v5, s44
	v_bfe_u32 v9, v20, 16, 1
	v_lshrrev_b32_e32 v5, 16, v5
	v_add3_u32 v9, v20, v9, s44
	v_and_or_b32 v10, v9, s43, v5
	v_pk_mul_f32 v[18:19], v[58:59], v[60:61]
	v_cvt_pk_bf16_f32 v14, v13, v14
	v_sub_f32_e32 v5, v18, v19
	v_pk_mul_f32 v[18:19], v[58:59], v[60:61] op_sel:[1,0] op_sel_hi:[0,1]
	v_add_f32_e32 v9, v18, v19
	v_pk_mul_f32 v[18:19], v[28:29], v[62:63]
	v_mul_f32_e32 v79, 0x3d800000, v79
	v_sub_f32_e32 v13, v18, v19
	v_pk_mul_f32 v[18:19], v[28:29], v[62:63] op_sel:[1,0] op_sel_hi:[0,1]
	v_mul_f32_e32 v5, 0x3d800000, v5
	v_add_f32_e32 v17, v18, v19
	v_bfe_u32 v18, v79, 16, 1
	v_add3_u32 v18, v79, v18, s44
	v_bfe_u32 v19, v5, 16, 1
	v_mul_f32_e32 v70, 0x3d800000, v70
	v_lshrrev_b32_e32 v18, 16, v18
	v_add3_u32 v5, v5, v19, s44
	v_mul_f32_e32 v9, 0x3d800000, v9
	v_and_or_b32 v5, v5, s43, v18
	v_bfe_u32 v18, v70, 16, 1
	v_add3_u32 v18, v70, v18, s44
	v_bfe_u32 v19, v9, 16, 1
	v_mul_f32_e32 v71, 0x3d800000, v71
	v_lshrrev_b32_e32 v18, 16, v18
	v_add3_u32 v9, v9, v19, s44
	v_mul_f32_e32 v13, 0x3d800000, v13
	v_and_or_b32 v9, v9, s43, v18
	v_bfe_u32 v18, v71, 16, 1
	v_add3_u32 v18, v71, v18, s44
	v_bfe_u32 v19, v13, 16, 1
	v_mul_f32_e32 v68, 0x3d800000, v68
	v_lshrrev_b32_e32 v18, 16, v18
	v_add3_u32 v13, v13, v19, s44
	v_mul_f32_e32 v17, 0x3d800000, v17
	v_and_or_b32 v13, v13, s43, v18
	v_bfe_u32 v18, v68, 16, 1
	v_add3_u32 v18, v68, v18, s44
	v_bfe_u32 v19, v17, 16, 1
	v_lshrrev_b32_e32 v18, 16, v18
	v_add3_u32 v17, v17, v19, s44
	v_and_or_b32 v17, v17, s43, v18
	v_mul_lo_u32 v18, v74, s42
	v_add3_u32 v18, 0, v18, v54
	ds_write_b128 v18, v[2:5]
	ds_write_b128 v18, v[6:9] offset:128
	ds_write_b128 v18, v[10:13] offset:256
	ds_write_b128 v18, v[14:17] offset:384
	v_add_u32_e32 v2, 0x200, v73
	v_cmp_lt_i32_e32 vcc, s45, v73
	v_add_u32_e32 v72, 0x1000, v72
	s_or_b64 s[20:21], vcc, s[20:21]
	v_mov_b32_e32 v73, v2
	s_andn2_b64 exec, exec, s[20:21]
	s_cbranch_execz .LBB0_324

.LBB0_388:
	s_waitcnt vmcnt(0)
	v_lshlrev_b32_e32 v96, 16, v33
	v_lshlrev_b32_e32 v54, 16, v29
	v_mul_f32_e32 v97, v121, v96
	v_fma_f32 v125, v120, v54, -v97
	v_mul_f32_e32 v54, v121, v54
	v_fmac_f32_e32 v54, v120, v96
	v_lshlrev_b32_e32 v96, 16, v28
	v_lshlrev_b32_e32 v97, 16, v32
	v_mul_f32_e32 v120, v119, v97
	v_mul_f32_e32 v119, v119, v96
	v_fma_f32 v120, v118, v96, -v120
	v_fmac_f32_e32 v119, v118, v97
	v_lshlrev_b32_e32 v96, 16, v27
	v_lshlrev_b32_e32 v97, 16, v31
	v_mul_f32_e32 v118, v117, v97
	v_mul_f32_e32 v117, v117, v96
	v_fmac_f32_e32 v117, v116, v97
	v_lshlrev_b32_e32 v97, 16, v30
	v_fma_f32 v118, v116, v96, -v118
	v_lshlrev_b32_e32 v96, 16, v26
	v_mul_f32_e32 v116, v113, v97
	v_fma_f32 v116, v112, v96, -v116
	v_mul_f32_e32 v121, v113, v96
	v_and_b32_e32 v96, 0xffff0000, v30
	v_fmac_f32_e32 v121, v112, v97
	v_and_b32_e32 v97, 0xffff0000, v26
	v_mul_f32_e32 v26, v109, v96
	v_pk_fma_f32 v[112:113], v[108:109], v[96:97], v[26:27] op_sel:[0,1,0] op_sel_hi:[1,0,0] neg_lo:[0,0,1] neg_hi:[0,0,1]
	v_mul_f32_e32 v26, v109, v97
	v_pk_fma_f32 v[96:97], v[108:109], v[96:97], v[26:27] op_sel_hi:[1,1,0]
	v_cvt_pk_bf16_f32 v30, v116, v112
	v_bfe_u32 v26, v121, 16, 1
	v_add3_u32 v26, v121, v26, s44
	v_bfe_u32 v97, v96, 16, 1
	v_lshrrev_b32_e32 v26, 16, v26
	v_add3_u32 v96, v96, v97, s44
	v_and_or_b32 v26, v96, s43, v26
	v_and_b32_e32 v96, 0xffff0000, v31
	v_and_b32_e32 v97, 0xffff0000, v27
	v_mul_f32_e32 v108, v111, v96
	v_pk_fma_f32 v[108:109], v[110:111], v[96:97], v[108:109] op_sel:[0,1,0] op_sel_hi:[1,0,0] neg_lo:[0,0,1] neg_hi:[0,0,1]
	v_mul_f32_e32 v112, v111, v97
	v_pk_fma_f32 v[96:97], v[110:111], v[96:97], v[112:113] op_sel_hi:[1,1,0]
	v_cvt_pk_bf16_f32 v31, v118, v108
	v_bfe_u32 v27, v117, 16, 1
	v_add3_u32 v27, v117, v27, s44
	v_bfe_u32 v97, v96, 16, 1
	v_lshrrev_b32_e32 v27, 16, v27
	v_add3_u32 v96, v96, v97, s44
	v_and_or_b32 v27, v96, s43, v27
	v_and_b32_e32 v96, 0xffff0000, v32
	v_and_b32_e32 v97, 0xffff0000, v28
	v_mul_f32_e32 v28, v115, v96
	v_pk_fma_f32 v[108:109], v[114:115], v[96:97], v[28:29] op_sel:[0,1,0] op_sel_hi:[1,0,0] neg_lo:[0,0,1] neg_hi:[0,0,1]
	v_mul_f32_e32 v28, v115, v97
	v_pk_fma_f32 v[96:97], v[114:115], v[96:97], v[28:29] op_sel_hi:[1,1,0]
	v_cvt_pk_bf16_f32 v32, v120, v108
	v_bfe_u32 v28, v119, 16, 1
	v_add3_u32 v28, v119, v28, s44
	v_bfe_u32 v97, v96, 16, 1
	v_lshrrev_b32_e32 v28, 16, v28
	v_add3_u32 v96, v96, v97, s44
	v_and_or_b32 v28, v96, s43, v28
	v_and_b32_e32 v96, 0xffff0000, v33
	v_lshlrev_b32_e32 v33, 16, v25
	v_and_b32_e32 v97, 0xffff0000, v29
	v_lshlrev_b32_e32 v29, 16, v21
	v_mul_f32_e32 v108, v107, v33
	v_fma_f32 v108, v106, v29, -v108
	v_mul_f32_e32 v29, v107, v29
	v_fmac_f32_e32 v29, v106, v33
	v_lshlrev_b32_e32 v106, 16, v24
	v_lshlrev_b32_e32 v33, 16, v20
	v_mul_f32_e32 v107, v105, v106
	v_fma_f32 v107, v104, v33, -v107
	v_mul_f32_e32 v33, v105, v33
	v_lshlrev_b32_e32 v105, 16, v23
	v_fmac_f32_e32 v33, v104, v106
	v_lshlrev_b32_e32 v104, 16, v19
	v_mul_f32_e32 v106, v103, v105
	v_fma_f32 v106, v102, v104, -v106
	v_mul_f32_e32 v104, v103, v104
	v_fmac_f32_e32 v104, v102, v105
	v_lshlrev_b32_e32 v102, 16, v18
	v_lshlrev_b32_e32 v103, 16, v22
	v_mul_f32_e32 v105, v95, v103
	v_mul_f32_e32 v109, v95, v102
	v_fma_f32 v105, v94, v102, -v105
	v_fmac_f32_e32 v109, v94, v103
	v_and_b32_e32 v94, 0xffff0000, v22
	v_and_b32_e32 v95, 0xffff0000, v18
	v_mul_f32_e32 v18, v91, v94
	v_pk_fma_f32 v[102:103], v[90:91], v[94:95], v[18:19] op_sel:[0,1,0] op_sel_hi:[1,0,0] neg_lo:[0,0,1] neg_hi:[0,0,1]
	v_mul_f32_e32 v18, v91, v95
	v_pk_fma_f32 v[90:91], v[90:91], v[94:95], v[18:19] op_sel_hi:[1,1,0]
	v_cvt_pk_bf16_f32 v22, v105, v102
	v_bfe_u32 v18, v109, 16, 1
	v_add3_u32 v18, v109, v18, s44
	v_bfe_u32 v91, v90, 16, 1
	v_lshrrev_b32_e32 v18, 16, v18
	v_add3_u32 v90, v90, v91, s44
	v_and_or_b32 v18, v90, s43, v18
	v_and_b32_e32 v90, 0xffff0000, v23
	v_and_b32_e32 v91, 0xffff0000, v19
	v_mul_f32_e32 v94, v93, v90
	v_pk_fma_f32 v[94:95], v[92:93], v[90:91], v[94:95] op_sel:[0,1,0] op_sel_hi:[1,0,0] neg_lo:[0,0,1] neg_hi:[0,0,1]
	v_mul_f32_e32 v102, v93, v91
	v_pk_fma_f32 v[90:91], v[92:93], v[90:91], v[102:103] op_sel_hi:[1,1,0]
	v_cvt_pk_bf16_f32 v23, v106, v94
	v_bfe_u32 v19, v104, 16, 1
	v_add3_u32 v19, v104, v19, s44
	v_bfe_u32 v91, v90, 16, 1
	v_lshrrev_b32_e32 v19, 16, v19
	v_add3_u32 v90, v90, v91, s44
	v_and_or_b32 v19, v90, s43, v19
	v_and_b32_e32 v90, 0xffff0000, v24
	v_and_b32_e32 v91, 0xffff0000, v20
	v_mul_f32_e32 v20, v99, v90
	v_pk_fma_f32 v[92:93], v[98:99], v[90:91], v[20:21] op_sel:[0,1,0] op_sel_hi:[1,0,0] neg_lo:[0,0,1] neg_hi:[0,0,1]
	v_mul_f32_e32 v20, v99, v91
	v_pk_fma_f32 v[90:91], v[98:99], v[90:91], v[20:21] op_sel_hi:[1,1,0]
	v_cvt_pk_bf16_f32 v24, v107, v92
	v_bfe_u32 v20, v33, 16, 1
	v_add3_u32 v20, v33, v20, s44
	v_bfe_u32 v33, v90, 16, 1
	v_add3_u32 v33, v90, v33, s44
	v_and_b32_e32 v90, 0xffff0000, v25
	v_and_b32_e32 v91, 0xffff0000, v21
	v_mul_f32_e32 v92, v101, v90
	v_pk_fma_f32 v[92:93], v[100:101], v[90:91], v[92:93] op_sel:[0,1,0] op_sel_hi:[1,0,0] neg_lo:[0,0,1] neg_hi:[0,0,1]
	v_mul_f32_e32 v94, v101, v91
	v_pk_fma_f32 v[90:91], v[100:101], v[90:91], v[94:95] op_sel_hi:[1,1,0]
	v_cvt_pk_bf16_f32 v25, v108, v92
	v_bfe_u32 v21, v29, 16, 1
	v_lshrrev_b32_e32 v20, 16, v20
	v_add3_u32 v21, v29, v21, s44
	v_bfe_u32 v29, v90, 16, 1
	v_and_or_b32 v20, v33, s43, v20
	v_lshrrev_b32_e32 v21, 16, v21
	v_add3_u32 v29, v90, v29, s44
	v_lshlrev_b32_e32 v33, 16, v17
	v_and_or_b32 v21, v29, s43, v21
	v_lshlrev_b32_e32 v29, 16, v13
	v_mul_f32_e32 v90, v87, v33
	v_fma_f32 v90, v86, v29, -v90
	v_mul_f32_e32 v29, v87, v29
	v_fmac_f32_e32 v29, v86, v33
	v_lshlrev_b32_e32 v86, 16, v16
	v_lshlrev_b32_e32 v33, 16, v12
	v_mul_f32_e32 v87, v85, v86
	v_fma_f32 v87, v84, v33, -v87
	v_mul_f32_e32 v33, v85, v33
	v_lshlrev_b32_e32 v85, 16, v15
	v_fmac_f32_e32 v33, v84, v86
	v_lshlrev_b32_e32 v84, 16, v11
	v_mul_f32_e32 v86, v83, v85
	v_fma_f32 v86, v82, v84, -v86
	v_mul_f32_e32 v84, v83, v84
	v_fmac_f32_e32 v84, v82, v85
	v_lshlrev_b32_e32 v82, 16, v10
	v_lshlrev_b32_e32 v83, 16, v14
	v_mul_f32_e32 v85, v77, v83
	v_mul_f32_e32 v91, v77, v82
	v_fma_f32 v85, v76, v82, -v85
	v_fmac_f32_e32 v91, v76, v83
	v_and_b32_e32 v76, 0xffff0000, v14
	v_and_b32_e32 v77, 0xffff0000, v10
	v_mul_f32_e32 v10, v73, v76
	v_pk_fma_f32 v[82:83], v[72:73], v[76:77], v[10:11] op_sel:[0,1,0] op_sel_hi:[1,0,0] neg_lo:[0,0,1] neg_hi:[0,0,1]
	v_mul_f32_e32 v10, v73, v77
	v_pk_fma_f32 v[72:73], v[72:73], v[76:77], v[10:11] op_sel_hi:[1,1,0]
	v_cvt_pk_bf16_f32 v14, v85, v82
	v_bfe_u32 v10, v91, 16, 1
	v_add3_u32 v10, v91, v10, s44
	v_bfe_u32 v73, v72, 16, 1
	v_lshrrev_b32_e32 v10, 16, v10
	v_add3_u32 v72, v72, v73, s44
	v_and_or_b32 v10, v72, s43, v10
	v_and_b32_e32 v72, 0xffff0000, v15
	v_and_b32_e32 v73, 0xffff0000, v11
	v_mul_f32_e32 v76, v75, v72
	v_pk_fma_f32 v[76:77], v[74:75], v[72:73], v[76:77] op_sel:[0,1,0] op_sel_hi:[1,0,0] neg_lo:[0,0,1] neg_hi:[0,0,1]
	v_mul_f32_e32 v82, v75, v73
	v_pk_fma_f32 v[72:73], v[74:75], v[72:73], v[82:83] op_sel_hi:[1,1,0]
	v_cvt_pk_bf16_f32 v15, v86, v76
	v_bfe_u32 v11, v84, 16, 1
	v_add3_u32 v11, v84, v11, s44
	v_bfe_u32 v73, v72, 16, 1
	v_lshrrev_b32_e32 v11, 16, v11
	v_add3_u32 v72, v72, v73, s44
	v_and_or_b32 v11, v72, s43, v11
	v_and_b32_e32 v72, 0xffff0000, v16
	v_and_b32_e32 v73, 0xffff0000, v12
	v_mul_f32_e32 v12, v79, v72
	v_pk_fma_f32 v[74:75], v[78:79], v[72:73], v[12:13] op_sel:[0,1,0] op_sel_hi:[1,0,0] neg_lo:[0,0,1] neg_hi:[0,0,1]
	v_mul_f32_e32 v12, v79, v73
	v_pk_fma_f32 v[72:73], v[78:79], v[72:73], v[12:13] op_sel_hi:[1,1,0]
	v_cvt_pk_bf16_f32 v16, v87, v74
	v_bfe_u32 v12, v33, 16, 1
	v_add3_u32 v12, v33, v12, s44
	v_bfe_u32 v33, v72, 16, 1
	v_add3_u32 v33, v72, v33, s44
	v_and_b32_e32 v72, 0xffff0000, v17
	v_and_b32_e32 v73, 0xffff0000, v13
	v_mul_f32_e32 v74, v81, v72
	v_pk_fma_f32 v[74:75], v[80:81], v[72:73], v[74:75] op_sel:[0,1,0] op_sel_hi:[1,0,0] neg_lo:[0,0,1] neg_hi:[0,0,1]
	v_mul_f32_e32 v76, v81, v73
	v_pk_fma_f32 v[72:73], v[80:81], v[72:73], v[76:77] op_sel_hi:[1,1,0]
	v_cvt_pk_bf16_f32 v17, v90, v74
	v_bfe_u32 v13, v29, 16, 1
	v_lshrrev_b32_e32 v12, 16, v12
	v_add3_u32 v13, v29, v13, s44
	v_bfe_u32 v29, v72, 16, 1
	v_and_or_b32 v12, v33, s43, v12
	v_lshrrev_b32_e32 v13, 16, v13
	v_add3_u32 v29, v72, v29, s44
	v_lshlrev_b32_e32 v33, 16, v9
	v_and_or_b32 v13, v29, s43, v13
	v_lshlrev_b32_e32 v29, 16, v5
	v_mul_f32_e32 v72, v71, v33
	v_fma_f32 v72, v70, v29, -v72
	v_mul_f32_e32 v29, v71, v29
	v_fmac_f32_e32 v29, v70, v33
	v_lshlrev_b32_e32 v70, 16, v8
	v_lshlrev_b32_e32 v33, 16, v4
	v_mul_f32_e32 v71, v69, v70
	v_fma_f32 v71, v68, v33, -v71
	v_mul_f32_e32 v33, v69, v33
	v_lshlrev_b32_e32 v69, 16, v7
	v_fmac_f32_e32 v33, v68, v70
	v_lshlrev_b32_e32 v68, 16, v3
	v_mul_f32_e32 v70, v67, v69
	v_fma_f32 v70, v66, v68, -v70
	v_mul_f32_e32 v68, v67, v68
	v_fmac_f32_e32 v68, v66, v69
	v_lshlrev_b32_e32 v66, 16, v2
	v_lshlrev_b32_e32 v67, 16, v6
	v_mul_f32_e32 v69, v61, v67
	v_mul_f32_e32 v73, v61, v66
	v_fma_f32 v69, v60, v66, -v69
	v_fmac_f32_e32 v73, v60, v67
	v_and_b32_e32 v60, 0xffff0000, v6
	v_and_b32_e32 v61, 0xffff0000, v2
	v_mul_f32_e32 v2, v57, v60
	v_pk_fma_f32 v[66:67], v[56:57], v[60:61], v[2:3] op_sel:[0,1,0] op_sel_hi:[1,0,0] neg_lo:[0,0,1] neg_hi:[0,0,1]
	v_mul_f32_e32 v2, v57, v61
	v_pk_fma_f32 v[56:57], v[56:57], v[60:61], v[2:3] op_sel_hi:[1,1,0]
	v_cvt_pk_bf16_f32 v2, v69, v66
	v_bfe_u32 v6, v73, 16, 1
	v_add3_u32 v6, v73, v6, s44
	v_bfe_u32 v57, v56, 16, 1
	v_lshrrev_b32_e32 v6, 16, v6
	v_add3_u32 v56, v56, v57, s44
	v_and_or_b32 v6, v56, s43, v6
	v_and_b32_e32 v56, 0xffff0000, v7
	v_and_b32_e32 v57, 0xffff0000, v3
	v_mul_f32_e32 v60, v59, v56
	v_pk_fma_f32 v[60:61], v[58:59], v[56:57], v[60:61] op_sel:[0,1,0] op_sel_hi:[1,0,0] neg_lo:[0,0,1] neg_hi:[0,0,1]
	v_mul_f32_e32 v66, v59, v57
	v_pk_fma_f32 v[56:57], v[58:59], v[56:57], v[66:67] op_sel_hi:[1,1,0]
	v_cvt_pk_bf16_f32 v3, v70, v60
	v_bfe_u32 v7, v68, 16, 1
	v_add3_u32 v7, v68, v7, s44
	v_bfe_u32 v57, v56, 16, 1
	v_lshrrev_b32_e32 v7, 16, v7
	v_add3_u32 v56, v56, v57, s44
	v_and_or_b32 v7, v56, s43, v7
	v_and_b32_e32 v56, 0xffff0000, v8
	v_and_b32_e32 v57, 0xffff0000, v4
	v_mul_f32_e32 v4, v63, v56
	v_pk_fma_f32 v[58:59], v[62:63], v[56:57], v[4:5] op_sel:[0,1,0] op_sel_hi:[1,0,0] neg_lo:[0,0,1] neg_hi:[0,0,1]
	v_mul_f32_e32 v4, v63, v57
	v_pk_fma_f32 v[56:57], v[62:63], v[56:57], v[4:5] op_sel_hi:[1,1,0]
	v_cvt_pk_bf16_f32 v4, v71, v58
	v_bfe_u32 v8, v33, 16, 1
	v_add3_u32 v8, v33, v8, s44
	v_bfe_u32 v33, v56, 16, 1
	v_add3_u32 v33, v56, v33, s44
	v_and_b32_e32 v56, 0xffff0000, v9
	v_and_b32_e32 v57, 0xffff0000, v5
	v_mul_f32_e32 v58, v65, v56
	v_pk_fma_f32 v[58:59], v[64:65], v[56:57], v[58:59] op_sel:[0,1,0] op_sel_hi:[1,0,0] neg_lo:[0,0,1] neg_hi:[0,0,1]
	v_mul_f32_e32 v60, v65, v57
	v_pk_fma_f32 v[56:57], v[64:65], v[56:57], v[60:61] op_sel_hi:[1,1,0]
	v_cvt_pk_bf16_f32 v5, v72, v58
	v_bfe_u32 v9, v29, 16, 1
	v_add3_u32 v9, v29, v9, s44
	v_bfe_u32 v29, v56, 16, 1
	v_lshrrev_b32_e32 v9, 16, v9
	v_add3_u32 v29, v56, v29, s44
	v_mul_f32_e32 v56, v89, v96
	v_lshrrev_b32_e32 v8, 16, v8
	v_and_or_b32 v9, v29, s43, v9
	v_pk_fma_f32 v[56:57], v[88:89], v[96:97], v[56:57] op_sel:[0,1,0] op_sel_hi:[1,0,0] neg_lo:[0,0,1] neg_hi:[0,0,1]
	v_and_or_b32 v8, v33, s43, v8
	s_ashr_i32 s13, s12, 31
	v_mul_f32_e32 v58, v89, v97
	s_lshl_b64 s[8:9], s[12:13], 16
	v_pk_fma_f32 v[58:59], v[88:89], v[96:97], v[58:59] op_sel_hi:[1,1,0]
	v_cvt_pk_bf16_f32 v33, v125, v56
	v_bfe_u32 v29, v54, 16, 1
	v_lshl_add_u64 v[56:57], v[52:53], 0, s[8:9]
	v_add3_u32 v29, v54, v29, s44
	v_bfe_u32 v54, v58, 16, 1
	global_store_dwordx4 v[56:57], v[2:5], off
	global_store_dwordx4 v[56:57], v[14:17], off offset:1024
	global_store_dwordx4 v[56:57], v[6:9], off offset:2048
	global_store_dwordx4 v[56:57], v[10:13], off offset:3072
	v_add_co_u32_e32 v56, vcc, s41, v56
	v_lshrrev_b32_e32 v29, 16, v29
	v_add3_u32 v54, v58, v54, s44
	v_addc_co_u32_e32 v57, vcc, 0, v57, vcc
	v_and_or_b32 v29, v54, s43, v29
	global_store_dwordx4 v[56:57], v[22:25], off
	global_store_dwordx4 v[56:57], v[30:33], off offset:1024
	global_store_dwordx4 v[56:57], v[18:21], off offset:2048
	global_store_dwordx4 v[56:57], v[26:29], off offset:3072
	s_waitcnt lgkmcnt(0)
	s_barrier
	ds_read_b128 v[56:59], v123
	ds_read_b128 v[60:63], v123 offset:64
	ds_read_b128 v[64:67], v123 offset:8448
	ds_read_b128 v[68:71], v123 offset:8512
	ds_read_b128 v[72:75], v123 offset:16896
	ds_read_b128 v[76:79], v123 offset:16960
	ds_read_b128 v[80:83], v123 offset:25344
	ds_read_b128 v[84:87], v123 offset:25408
	ds_read_b128 v[88:91], v123 offset:33792
	ds_read_b128 v[92:95], v123 offset:33856
	ds_read_b128 v[96:99], v123 offset:42240
	ds_read_b128 v[100:103], v123 offset:42304
	ds_read_b128 v[104:107], v123 offset:50688
	ds_read_b128 v[108:111], v123 offset:50752
	ds_read_b128 v[112:115], v123 offset:59136
	ds_read_b128 v[116:119], v123 offset:59200
	s_waitcnt lgkmcnt(14)
	v_mfma_f32_16x16x32_bf16 v[56:59], v[56:59], v[2:5], 0
	s_lshl_b64 s[8:9], s[12:13], 15
	s_add_u32 s14, s35, s8
	s_addc_u32 s15, s36, s9
	s_waitcnt lgkmcnt(13)
	v_mfma_f32_16x16x32_bf16 v[64:67], v[64:67], v[2:5], 0
	s_waitcnt lgkmcnt(11)
	v_mfma_f32_16x16x32_bf16 v[72:75], v[72:75], v[2:5], 0
	s_waitcnt lgkmcnt(9)
	v_mfma_f32_16x16x32_bf16 v[80:83], v[80:83], v[2:5], 0
	s_waitcnt lgkmcnt(7)
	v_mfma_f32_16x16x32_bf16 v[88:91], v[88:91], v[2:5], 0
	s_waitcnt lgkmcnt(5)
	v_mfma_f32_16x16x32_bf16 v[96:99], v[96:99], v[2:5], 0
	s_waitcnt lgkmcnt(3)
	v_mfma_f32_16x16x32_bf16 v[104:107], v[104:107], v[2:5], 0
	s_waitcnt lgkmcnt(1)
	v_mfma_f32_16x16x32_bf16 v[2:5], v[112:115], v[2:5], 0
	v_mfma_f32_16x16x32_bf16 v[56:59], v[60:63], v[14:17], v[56:59]
	v_mfma_f32_16x16x32_bf16 v[60:63], v[68:71], v[14:17], v[64:67]
	v_mfma_f32_16x16x32_bf16 v[64:67], v[76:79], v[14:17], v[72:75]
	v_mfma_f32_16x16x32_bf16 v[68:71], v[84:87], v[14:17], v[80:83]
	v_mfma_f32_16x16x32_bf16 v[72:75], v[92:95], v[14:17], v[88:91]
	v_mfma_f32_16x16x32_bf16 v[76:79], v[100:103], v[14:17], v[96:99]
	v_mfma_f32_16x16x32_bf16 v[80:83], v[108:111], v[14:17], v[104:107]
	s_waitcnt lgkmcnt(0)
	v_mfma_f32_16x16x32_bf16 v[2:5], v[116:119], v[14:17], v[2:5]
	ds_read_b128 v[14:17], v123 offset:128
	ds_read_b128 v[84:87], v123 offset:192
	s_waitcnt lgkmcnt(1)
	v_mfma_f32_16x16x32_bf16 v[14:17], v[14:17], v[6:9], v[56:59]
	s_nop 2
	ds_read_b128 v[56:59], v123 offset:8576
	ds_read_b128 v[88:91], v123 offset:8640
	s_waitcnt lgkmcnt(1)
	v_mfma_f32_16x16x32_bf16 v[56:59], v[56:59], v[6:9], v[60:63]
	s_nop 2
	ds_read_b128 v[60:63], v123 offset:17024
	ds_read_b128 v[92:95], v123 offset:17088
	s_waitcnt lgkmcnt(1)
	v_mfma_f32_16x16x32_bf16 v[60:63], v[60:63], v[6:9], v[64:67]
	s_nop 2
	ds_read_b128 v[64:67], v123 offset:25472
	ds_read_b128 v[96:99], v123 offset:25536
	s_waitcnt lgkmcnt(1)
	v_mfma_f32_16x16x32_bf16 v[64:67], v[64:67], v[6:9], v[68:71]
	s_nop 2
	ds_read_b128 v[68:71], v123 offset:33920
	ds_read_b128 v[100:103], v123 offset:33984
	s_waitcnt lgkmcnt(1)
	v_mfma_f32_16x16x32_bf16 v[68:71], v[68:71], v[6:9], v[72:75]
	s_nop 2
	ds_read_b128 v[72:75], v123 offset:42368
	ds_read_b128 v[104:107], v123 offset:42432
	s_waitcnt lgkmcnt(1)
	v_mfma_f32_16x16x32_bf16 v[72:75], v[72:75], v[6:9], v[76:79]
	s_nop 2
	ds_read_b128 v[76:79], v123 offset:50816
	ds_read_b128 v[108:111], v123 offset:50880
	s_waitcnt lgkmcnt(1)
	v_mfma_f32_16x16x32_bf16 v[76:79], v[76:79], v[6:9], v[80:83]
	s_nop 2
	ds_read_b128 v[80:83], v123 offset:59264
	ds_read_b128 v[112:115], v123 offset:59328
	s_waitcnt lgkmcnt(1)
	v_mfma_f32_16x16x32_bf16 v[2:5], v[80:83], v[6:9], v[2:5]
	v_mfma_f32_16x16x32_bf16 v[6:9], v[84:87], v[10:13], v[14:17]
	v_mfma_f32_16x16x32_bf16 v[14:17], v[88:91], v[10:13], v[56:59]
	v_mfma_f32_16x16x32_bf16 v[56:59], v[92:95], v[10:13], v[60:63]
	v_mfma_f32_16x16x32_bf16 v[60:63], v[96:99], v[10:13], v[64:67]
	v_mfma_f32_16x16x32_bf16 v[64:67], v[100:103], v[10:13], v[68:71]
	v_mfma_f32_16x16x32_bf16 v[68:71], v[104:107], v[10:13], v[72:75]
	v_mfma_f32_16x16x32_bf16 v[72:75], v[108:111], v[10:13], v[76:79]
	s_waitcnt lgkmcnt(0)
	v_mfma_f32_16x16x32_bf16 v[2:5], v[112:115], v[10:13], v[2:5]
	ds_read_b128 v[10:13], v123 offset:256
	ds_read_b128 v[76:79], v123 offset:320
	s_waitcnt lgkmcnt(1)
	v_mfma_f32_16x16x32_bf16 v[6:9], v[10:13], v[22:25], v[6:9]
	ds_read_b128 v[10:13], v123 offset:8704
	ds_read_b128 v[80:83], v123 offset:8768
	s_waitcnt lgkmcnt(1)
	v_mfma_f32_16x16x32_bf16 v[10:13], v[10:13], v[22:25], v[14:17]
	s_nop 2
	ds_read_b128 v[14:17], v123 offset:17152
	ds_read_b128 v[84:87], v123 offset:17216
	s_waitcnt lgkmcnt(1)
	v_mfma_f32_16x16x32_bf16 v[14:17], v[14:17], v[22:25], v[56:59]
	s_nop 2
	ds_read_b128 v[56:59], v123 offset:25600
	ds_read_b128 v[88:91], v123 offset:25664
	s_waitcnt lgkmcnt(1)
	v_mfma_f32_16x16x32_bf16 v[56:59], v[56:59], v[22:25], v[60:63]
	s_nop 2
	ds_read_b128 v[60:63], v123 offset:34048
	ds_read_b128 v[92:95], v123 offset:34112
	s_waitcnt lgkmcnt(1)
	v_mfma_f32_16x16x32_bf16 v[60:63], v[60:63], v[22:25], v[64:67]
	s_nop 2
	ds_read_b128 v[64:67], v123 offset:42496
	ds_read_b128 v[96:99], v123 offset:42560
	s_waitcnt lgkmcnt(1)
	v_mfma_f32_16x16x32_bf16 v[64:67], v[64:67], v[22:25], v[68:71]
	s_nop 2
	ds_read_b128 v[68:71], v123 offset:50944
	ds_read_b128 v[100:103], v123 offset:51008
	s_waitcnt lgkmcnt(1)
	v_mfma_f32_16x16x32_bf16 v[68:71], v[68:71], v[22:25], v[72:75]
	s_nop 2
	ds_read_b128 v[72:75], v123 offset:59392
	ds_read_b128 v[104:107], v123 offset:59456
	s_waitcnt lgkmcnt(1)
	v_mfma_f32_16x16x32_bf16 v[2:5], v[72:75], v[22:25], v[2:5]
	v_mfma_f32_16x16x32_bf16 v[6:9], v[76:79], v[30:33], v[6:9]
	v_mfma_f32_16x16x32_bf16 v[10:13], v[80:83], v[30:33], v[10:13]
	v_mfma_f32_16x16x32_bf16 v[14:17], v[84:87], v[30:33], v[14:17]
	v_mfma_f32_16x16x32_bf16 v[22:25], v[88:91], v[30:33], v[56:59]
	v_mfma_f32_16x16x32_bf16 v[56:59], v[92:95], v[30:33], v[60:63]
	v_mfma_f32_16x16x32_bf16 v[60:63], v[96:99], v[30:33], v[64:67]
	v_mfma_f32_16x16x32_bf16 v[64:67], v[100:103], v[30:33], v[68:71]
	s_waitcnt lgkmcnt(0)
	v_mfma_f32_16x16x32_bf16 v[2:5], v[104:107], v[30:33], v[2:5]
	ds_read_b128 v[30:33], v123 offset:384
	ds_read_b128 v[68:71], v123 offset:448
	s_waitcnt lgkmcnt(1)
	v_mfma_f32_16x16x32_bf16 v[6:9], v[30:33], v[18:21], v[6:9]
	ds_read_b128 v[30:33], v123 offset:8832
	ds_read_b128 v[72:75], v123 offset:8896
	s_waitcnt lgkmcnt(1)
	v_mfma_f32_16x16x32_bf16 v[10:13], v[30:33], v[18:21], v[10:13]
	ds_read_b128 v[30:33], v123 offset:17280
	ds_read_b128 v[76:79], v123 offset:17344
	s_waitcnt lgkmcnt(1)
	v_mfma_f32_16x16x32_bf16 v[14:17], v[30:33], v[18:21], v[14:17]
	ds_read_b128 v[30:33], v123 offset:25728
	ds_read_b128 v[80:83], v123 offset:25792
	s_waitcnt lgkmcnt(1)
	v_mfma_f32_16x16x32_bf16 v[22:25], v[30:33], v[18:21], v[22:25]
	ds_read_b128 v[30:33], v123 offset:34176
	ds_read_b128 v[84:87], v123 offset:34240
	s_waitcnt lgkmcnt(1)
	v_mfma_f32_16x16x32_bf16 v[30:33], v[30:33], v[18:21], v[56:59]
	s_nop 2
	ds_read_b128 v[56:59], v123 offset:42624
	ds_read_b128 v[88:91], v123 offset:42688
	s_waitcnt lgkmcnt(1)
	v_mfma_f32_16x16x32_bf16 v[56:59], v[56:59], v[18:21], v[60:63]
	s_nop 2
	ds_read_b128 v[60:63], v123 offset:51072
	ds_read_b128 v[92:95], v123 offset:51136
	s_waitcnt lgkmcnt(1)
	v_mfma_f32_16x16x32_bf16 v[60:63], v[60:63], v[18:21], v[64:67]
	s_nop 2
	ds_read_b128 v[64:67], v123 offset:59520
	ds_read_b128 v[96:99], v123 offset:59584
	s_waitcnt lgkmcnt(1)
	v_mfma_f32_16x16x32_bf16 v[2:5], v[64:67], v[18:21], v[2:5]
	v_mfma_f32_16x16x32_bf16 v[6:9], v[68:71], v[26:29], v[6:9]
	v_mfma_f32_16x16x32_bf16 v[10:13], v[72:75], v[26:29], v[10:13]
	v_mfma_f32_16x16x32_bf16 v[14:17], v[76:79], v[26:29], v[14:17]
	v_mfma_f32_16x16x32_bf16 v[18:21], v[80:83], v[26:29], v[22:25]
	v_mfma_f32_16x16x32_bf16 v[22:25], v[84:87], v[26:29], v[30:33]
	v_mfma_f32_16x16x32_bf16 v[30:33], v[88:91], v[26:29], v[56:59]
	v_mfma_f32_16x16x32_bf16 v[56:59], v[92:95], v[26:29], v[60:63]
	s_waitcnt lgkmcnt(0)
	v_mfma_f32_16x16x32_bf16 v[2:5], v[96:99], v[26:29], v[2:5]
	v_bfe_u32 v26, v6, 16, 1
	v_add3_u32 v6, v6, v26, s44
	v_bfe_u32 v26, v7, 16, 1
	v_lshrrev_b32_e32 v6, 16, v6
	v_add3_u32 v7, v7, v26, s44
	v_and_or_b32 v6, v7, s43, v6
	v_bfe_u32 v7, v8, 16, 1
	v_add3_u32 v7, v8, v7, s44
	v_bfe_u32 v8, v9, 16, 1
	v_lshrrev_b32_e32 v7, 16, v7
	v_add3_u32 v8, v9, v8, s44
	v_and_or_b32 v7, v8, s43, v7
	v_lshl_add_u64 v[8:9], v[36:37], 1, s[14:15]
	global_store_dwordx2 v[8:9], v[6:7], off
	v_cvt_pk_bf16_f32 v6, v10, v11
	v_cvt_pk_bf16_f32 v7, v12, v13
	v_lshl_add_u64 v[8:9], v[38:39], 1, s[14:15]
	global_store_dwordx2 v[8:9], v[6:7], off
	v_cvt_pk_bf16_f32 v6, v14, v15
	v_cvt_pk_bf16_f32 v7, v16, v17
	v_lshl_add_u64 v[8:9], v[40:41], 1, s[14:15]
	global_store_dwordx2 v[8:9], v[6:7], off
	v_cvt_pk_bf16_f32 v6, v18, v19
	v_cvt_pk_bf16_f32 v7, v20, v21
	v_lshl_add_u64 v[8:9], v[42:43], 1, s[14:15]
	global_store_dwordx2 v[8:9], v[6:7], off
	v_cvt_pk_bf16_f32 v6, v22, v23
	v_cvt_pk_bf16_f32 v7, v24, v25
	v_lshl_add_u64 v[8:9], v[44:45], 1, s[14:15]
	global_store_dwordx2 v[8:9], v[6:7], off
	v_cvt_pk_bf16_f32 v6, v30, v31
	v_cvt_pk_bf16_f32 v7, v32, v33
	v_lshl_add_u64 v[8:9], v[46:47], 1, s[14:15]
	global_store_dwordx2 v[8:9], v[6:7], off
	v_cvt_pk_bf16_f32 v6, v56, v57
	v_cvt_pk_bf16_f32 v7, v58, v59
	v_lshl_add_u64 v[8:9], v[48:49], 1, s[14:15]
	global_store_dwordx2 v[8:9], v[6:7], off
	v_bfe_u32 v6, v2, 16, 1
	v_add3_u32 v2, v2, v6, s44
	v_bfe_u32 v6, v3, 16, 1
	v_lshrrev_b32_e32 v2, 16, v2
	v_add3_u32 v3, v3, v6, s44
	v_and_or_b32 v2, v3, s43, v2
	v_bfe_u32 v3, v4, 16, 1
	v_add3_u32 v3, v4, v3, s44
	v_bfe_u32 v4, v5, 16, 1
	v_lshrrev_b32_e32 v3, 16, v3
	v_add3_u32 v4, v5, v4, s44
	v_and_or_b32 v3, v4, s43, v3
	v_lshl_add_u64 v[4:5], v[50:51], 1, s[14:15]
	global_store_dwordx2 v[4:5], v[2:3], off
	s_and_saveexec_b64 s[14:15], s[6:7]
	s_cbranch_execz .LBB0_304
	s_lshl_b64 s[8:9], s[8:9], 1
	s_add_u32 s8, s37, s8
	s_addc_u32 s9, s40, s9
	s_mov_b64 s[16:17], 0
	v_mov_b32_e32 v2, v170

.LBB0_441:
	s_cmp_lt_i32 s92, 5
	s_cselect_b64 s[4:5], -1, 0
	s_cmp_gt_i32 s93, 4
	s_cselect_b64 s[6:7], -1, 0
	s_and_b64 s[4:5], s[4:5], s[6:7]
	s_andn2_b64 vcc, exec, s[4:5]
	s_cbranch_vccnz .LBB0_527
	s_cmp_lt_u32 s88, 4
	s_cbranch_scc1 .Lmy_prio_skip4
	s_setprio 2
.Lmy_prio_skip4:
	s_cmpk_gt_i32 s89, 0xff
	s_mov_b32 s6, 11
	s_mov_b32 s4, 12
	s_cbranch_scc1 .LBB0_477
	s_lshr_b32 s3, s90, 7
	s_add_u32 s18, s26, 0x32d00000
	s_addc_u32 s19, s27, 0
	s_add_u32 s35, s26, 0x21d00000
	s_addc_u32 s69, s27, 0
	s_add_u32 s74, s26, 0x3d700000
	s_addc_u32 s75, s27, 0
	s_ashr_i32 s7, s6, 31
	s_lshl_b64 s[6:7], s[6:7], 3
	v_and_b32_e32 v2, 15, v250
	s_add_u32 s6, s0, s6
	v_lshl_or_b32 v1, s88, 4, v2
	s_addc_u32 s7, s1, s7
	s_ashr_i32 s5, s4, 31
	v_add_u32_e32 v3, 0xffffff81, v1
	s_lshl_b64 s[4:5], s[4:5], 3
	v_cvt_f32_i32_e32 v176, v3
	v_ashrrev_i32_e32 v3, 1, v250
	s_add_u32 s4, s0, s4
	v_and_b32_e32 v177, -8, v3
	v_bfe_u32 v3, v250, 2, 2
	s_addc_u32 s5, s1, s5
	s_load_dwordx2 s[20:21], s[6:7], 0x0
	s_load_dwordx2 s[22:23], s[4:5], 0x0
	v_or_b32_e32 v3, v177, v3
	s_movk_i32 s6, 0x90
	v_lshlrev_b32_e32 v4, 3, v250
	s_lshl_b32 s5, s88, 12
	v_mul_lo_u32 v3, v3, s6
	v_and_b32_e32 v4, 24, v4
	v_lshl_add_u32 v142, v250, 4, s5
	v_mov_b32_e32 v143, 0
	v_add3_u32 v178, 0, v3, v4
	v_mul_u32_u24_e32 v4, 0x210, v2
	v_ashrrev_i32_e32 v179, 3, v170
	v_lshlrev_b32_e32 v2, 4, v170
	v_add_u32_e32 v144, s5, v142
	v_mov_b32_e32 v145, v143
	v_mul_lo_u32 v8, v1, s6
	v_and_b32_e32 v9, 0x70, v2
	v_mul_lo_u32 v10, v179, s6
	v_lshl_add_u64 v[2:3], s[26:27], 0, v[142:143]
	s_mov_b64 s[6:7], 0x37100000
	v_lshl_add_u64 v[148:149], v[2:3], 0, s[6:7]
	v_lshl_add_u64 v[2:3], s[26:27], 0, v[144:145]
	s_mov_b64 s[6:7], 0x34f00000
	s_and_b32 s4, s90, 0xffffffc0
	v_cvt_f32_u32_e32 v175, v1
	v_lshl_add_u64 v[150:151], v[2:3], 0, s[6:7]
	v_lshlrev_b32_e32 v2, 3, v170
	s_add_i32 s4, s4, 0
	s_add_i32 s8, 0, 0x11400
	v_and_b32_e32 v2, 56, v2
	v_lshlrev_b32_e32 v5, 1, v177
	v_add_u32_e32 v6, s8, v177
	v_add_u32_e32 v7, s4, v177
	s_movk_i32 s4, 0x2100
	v_lshlrev_b32_e32 v3, 1, v2
	s_mov_b32 s41, 0
	v_sub_u32_e32 v171, 0x80, v1
	v_add_u32_e32 v174, 1, v1
	v_cmp_gt_i32_e64 s[4:5], s4, v170
	v_lshl_or_b32 v146, v179, 10, v9
	v_sub_u32_e32 v180, 0x7f, v179
	v_sub_u32_e32 v181, 63, v179
	v_add_u32_e32 v182, 64, v179
	v_mov_b32_e32 v147, v143
	v_lshl_add_u64 v[152:153], s[18:19], 0, v[144:145]
	v_add3_u32 v183, 0, v10, v9
	v_add3_u32 v184, s8, v10, v3
	v_add3_u32 v185, 0, v5, v4
	v_add_u32_e32 v186, 0xfffffe00, v170
	v_lshl_add_u32 v187, v170, 2, 0
	s_mov_b32 s76, 0x800000
	v_mov_b32_e32 v188, 0x42000000
	s_mov_b32 s77, 0xc2fc0000
	v_mov_b32_e32 v189, 0x42800000
	s_movk_i32 s78, 0x1eff
	s_mov_b32 s79, 0xffff0000
	s_mov_b64 s[42:43], 0x1000
	s_movk_i32 s80, 0x7fff
	v_lshlrev_b32_e32 v142, 1, v2
	s_mov_b32 s81, 0x40000
	v_mov_b32_e32 v190, 0xffff
	v_mov_b32_e32 v191, 0xffff0000
	v_not_b32_e32 v192, 63
	v_add_u32_e32 v193, v6, v8
	v_add_u32_e32 v194, v7, v4
	s_mov_b32 s82, s89
	v_lshrrev_b32_e32 v34, 2, v170
	v_lshrrev_b32_e32 v35, 3, v170
	v_xor_b32_e32 v34, v34, v35
	v_and_b32_e32 v34, 1, v34
	v_bfe_u32 v35, v170, 4, 1
	v_lshlrev_b32_e32 v35, 5, v35
	v_sub_u32_e32 v35, 16, v35
	v_mul_lo_u32 v35, v35, v34
	v_add_u32_e32 v185, v185, v35
	v_bfe_u32 v35, v170, 5, 1
	v_lshlrev_b32_e32 v35, 5, v35
	v_sub_u32_e32 v35, 16, v35
	v_mul_lo_u32 v35, v35, v34
	v_add_u32_e32 v194, v194, v35
	s_branch .LBB0_445

.LBB0_527:
	s_setprio 0
	s_cmp_lt_i32 s92, 6
	s_cselect_b64 s[4:5], -1, 0
	s_cmp_gt_i32 s93, 5
	s_cselect_b64 s[6:7], -1, 0
	s_and_b64 s[4:5], s[4:5], s[6:7]
	s_andn2_b64 vcc, exec, s[4:5]
	s_cbranch_vccnz .LBB0_581
	s_lshl_b32 s3, s89, 3
	s_add_i32 s6, s3, s88
	s_cmpk_gt_i32 s6, 0x43ff
	s_mov_b32 s10, 13
	s_mov_b32 s4, 14
	s_cbranch_scc1 .LBB0_531
	s_add_u32 s3, s26, 0x2a500000
	s_addc_u32 s15, s27, 0
	s_ashr_i32 s11, s10, 31
	s_lshl_b32 s8, s34, 3
	s_lshl_b64 s[10:11], s[10:11], 3
	s_add_u32 s12, s0, s10
	s_addc_u32 s13, s1, s11
	s_add_u32 s16, s26, 0x3d700000
	s_addc_u32 s17, s27, 0
	s_ashr_i32 s7, s6, 31
	s_lshl_b64 s[18:19], s[6:7], 12
	s_add_u32 s20, s16, s18
	s_addc_u32 s21, s17, s19
	s_add_u32 s22, s26, 0x41b00000
	s_waitcnt vmcnt(0)
	v_lshlrev_b32_e32 v2, 3, v250
	s_addc_u32 s23, s27, 0
	v_lshlrev_b32_e32 v1, 5, v250
	v_and_b32_e32 v2, 0x78, v2
	s_movk_i32 s5, 0xfe00
	s_add_u32 s28, s22, s18
	v_and_or_b32 v146, v1, s5, v2
	s_addc_u32 s29, s23, s19
	s_lshl_b64 s[10:11], s[6:7], 13
	v_ashrrev_i32_e32 v147, 31, v146
	s_add_u32 s10, s3, s10
	s_addc_u32 s11, s15, s11
	v_lshlrev_b64 v[2:3], 1, v[146:147]
	v_lshl_add_u64 v[4:5], s[10:11], 0, v[2:3]
	s_movk_i32 s7, 0x1000
	s_mov_b64 s[10:11], 0x1000
	v_lshl_add_u64 v[10:11], s[20:21], 0, v[2:3]
	v_add_co_u32_e32 v12, vcc, s7, v4
	v_lshl_add_u64 v[6:7], v[4:5], 0, s[10:11]
	v_lshl_add_u64 v[8:9], s[28:29], 0, v[2:3]
	global_load_dwordx4 v[34:37], v[4:5], off offset:768
	global_load_dwordx4 v[74:77], v[4:5], off offset:512
	global_load_dwordx4 v[78:81], v[6:7], off offset:512
	global_load_dwordx4 v[82:85], v[6:7], off offset:256
	global_load_dwordx4 v[106:109], v[8:9], off offset:512
	global_load_dwordx4 v[122:125], v[8:9], off offset:256
	global_load_dwordx4 v[118:121], v[10:11], off offset:512
	global_load_dwordx4 v[126:129], v[10:11], off offset:256
	v_addc_co_u32_e32 v13, vcc, 0, v5, vcc
	global_load_dwordx4 v[110:113], v[10:11], off offset:768
	global_load_dwordx4 v[94:97], v[12:13], off
	global_load_dwordx4 v[86:89], v[4:5], off offset:256
	global_load_dwordx4 v[90:93], v[4:5], off
	global_load_dwordx4 v[38:41], v[6:7], off offset:768
	global_load_dwordx4 v[130:133], v[8:9], off
	global_load_dwordx4 v[114:117], v[8:9], off offset:768
	global_load_dwordx4 v[134:137], v[10:11], off
	s_ashr_i32 s5, s4, 31
	s_lshl_b64 s[4:5], s[4:5], 3
	s_add_u32 s4, s0, s4
	s_addc_u32 s5, s1, s5
	s_load_dwordx2 s[20:21], s[12:13], 0x0
	s_load_dwordx2 s[28:29], s[4:5], 0x0
	s_add_u32 s4, s26, s18
	s_addc_u32 s5, s27, s19
	v_lshl_add_u64 v[148:149], s[16:17], 0, v[2:3]
	v_lshl_add_u64 v[150:151], s[22:23], 0, v[2:3]
	v_lshlrev_b64 v[4:5], 2, v[146:147]
	v_lshl_add_u64 v[2:3], s[4:5], 0, v[2:3]
	s_mov_b64 s[4:5], 0x45f00000
	s_ashr_i32 s9, s8, 31
	s_waitcnt lgkmcnt(0)
	v_lshl_add_u64 v[152:153], s[20:21], 0, v[4:5]
	v_lshl_add_u64 v[154:155], s[28:29], 0, v[4:5]
	v_lshl_add_u64 v[156:157], v[2:3], 0, s[4:5]
	s_lshl_b64 s[12:13], s[8:9], 12
	s_mov_b32 s14, 0x3b000000
	v_mov_b32_e32 v1, 0x358637bd
	s_mov_b32 s9, 0xf800000
	v_mov_b32_e32 v171, 0x260
	v_lshlrev_b32_e32 v242, 4, v250
	s_lshl_b32 s98, s88, 14
	v_add_u32_e32 v242, s98, v242
	global_load_dwordx4 v[2:5], v[152:153], off
	global_load_dwordx4 v[6:9], v[152:153], off offset:16
	global_load_dwordx4 v[10:13], v[152:153], off offset:512
	global_load_dwordx4 v[14:17], v[152:153], off offset:528
	global_load_dwordx4 v[18:21], v[152:153], off offset:1024
	global_load_dwordx4 v[22:25], v[152:153], off offset:1040
	global_load_dwordx4 v[26:29], v[152:153], off offset:1536
	global_load_dwordx4 v[30:33], v[152:153], off offset:1552
	global_load_dwordx4 v[42:45], v[154:155], off
	global_load_dwordx4 v[46:49], v[154:155], off offset:16
	global_load_dwordx4 v[50:53], v[154:155], off offset:512
	global_load_dwordx4 v[54:57], v[154:155], off offset:528
	global_load_dwordx4 v[58:61], v[154:155], off offset:1024
	global_load_dwordx4 v[62:65], v[154:155], off offset:1040
	global_load_dwordx4 v[66:69], v[154:155], off offset:1536
	global_load_dwordx4 v[70:73], v[154:155], off offset:1552
	s_waitcnt vmcnt(0)
	ds_write_b128 v242, v[2:5]
	ds_write_b128 v242, v[6:9] offset:1024
	ds_write_b128 v242, v[10:13] offset:2048
	ds_write_b128 v242, v[14:17] offset:3072
	ds_write_b128 v242, v[18:21] offset:4096
	ds_write_b128 v242, v[22:25] offset:5120
	ds_write_b128 v242, v[26:29] offset:6144
	ds_write_b128 v242, v[30:33] offset:7168
	ds_write_b128 v242, v[42:45] offset:8192
	ds_write_b128 v242, v[46:49] offset:9216
	ds_write_b128 v242, v[50:53] offset:10240
	ds_write_b128 v242, v[54:57] offset:11264
	ds_write_b128 v242, v[58:61] offset:12288
	ds_write_b128 v242, v[62:65] offset:13312
	ds_write_b128 v242, v[66:69] offset:14336
	ds_write_b128 v242, v[70:73] offset:15360
	s_waitcnt lgkmcnt(0)

.LBB0_676:
	s_add_i32 s10, s6, 0xfffffc00
	s_lshr_b32 s10, s10, 12
	s_mulk_i32 s10, 0x1800
	s_and_b64 s[4:5], s[4:5], exec
	s_cselect_b32 s10, 0x6000, s10
	s_lshl_b64 s[4:5], s[10:11], 2
	v_pk_mul_f32 v[62:63], v[32:33], v[32:33]
	v_pk_mul_f32 v[64:65], v[30:31], v[30:31]
	v_lshl_add_u64 v[66:67], v[24:25], 0, s[4:5]
	v_pk_mul_f32 v[58:59], v[34:35], v[34:35]
	v_pk_mul_f32 v[60:61], v[44:45], v[44:45]
	global_load_dwordx4 v[18:21], v[66:67], off
	global_load_dwordx4 v[46:49], v[66:67], off offset:1024
	global_load_dwordx4 v[50:53], v[66:67], off offset:2048
	global_load_dwordx4 v[54:57], v[66:67], off offset:3072
	v_pk_mov_b32 v[66:67], v[64:65], v[62:63] op_sel:[1,0]
	v_mov_b32_e32 v65, v63
	v_pk_add_f32 v[62:63], v[66:67], v[64:65]
	v_pk_mov_b32 v[64:65], v[60:61], v[58:59] op_sel:[1,0]
	v_mov_b32_e32 v61, v59
	v_pk_add_f32 v[58:59], v[64:65], v[60:61]
	v_pk_add_f32 v[62:63], v[62:63], v[62:63] op_sel_hi:[0,1]
	v_pk_add_f32 v[58:59], v[58:59], v[58:59] op_sel_hi:[0,1]
	v_mul_f32_e32 v58, v42, v42
	v_pk_fma_f32 v[60:61], v[42:43], v[42:43], v[58:59] op_sel_hi:[1,1,0]
	v_mul_f32_e32 v58, v36, v36
	v_pk_fma_f32 v[64:65], v[36:37], v[36:37], v[58:59] op_sel_hi:[1,1,0]
	v_mul_f32_e32 v60, v38, v38
	v_mul_f32_e32 v64, v39, v39
	v_mul_f32_e32 v62, v40, v40
	v_mul_f32_e32 v58, v41, v41
	v_pk_add_f32 v[66:67], v[60:61], v[64:65]
	v_pk_add_f32 v[68:69], v[62:63], v[58:59]
	v_lshl_add_u64 v[74:75], v[22:23], 0, s[4:5]
	v_pk_add_f32 v[66:67], v[66:67], v[68:69]
	global_load_dwordx4 v[58:61], v[74:75], off offset:2048
	global_load_dwordx4 v[62:65], v[74:75], off offset:3072
	v_add_f32_e32 v76, v66, v67
	global_load_dwordx4 v[66:69], v[74:75], off
	global_load_dwordx4 v[70:73], v[74:75], off offset:1024
	v_add_f32_dpp v74, v76, v76 row_ror:8 row_mask:0xf bank_mask:0xf bound_ctrl:1
	s_add_i32 s6, s6, s8
	s_cmpk_lt_i32 s6, 0x4400
	v_add_f32_dpp v74, v74, v74 row_ror:4 row_mask:0xf bank_mask:0xf bound_ctrl:1
	s_waitcnt vmcnt(7)
	v_pk_add_f32 v[18:19], v[18:19], 1.0 op_sel_hi:[1,0]
	v_add_f32_dpp v74, v74, v74 row_ror:2 row_mask:0xf bank_mask:0xf bound_ctrl:1
	v_pk_add_f32 v[20:21], v[20:21], 1.0 op_sel_hi:[1,0]
	s_waitcnt vmcnt(6)
	v_pk_add_f32 v[46:47], v[46:47], 1.0 op_sel_hi:[1,0]
	v_add_f32_dpp v74, v74, v74 row_ror:1 row_mask:0xf bank_mask:0xf bound_ctrl:1
	ds_bpermute_b32 v75, v1, v74
	v_pk_add_f32 v[48:49], v[48:49], 1.0 op_sel_hi:[1,0]
	s_waitcnt vmcnt(5)
	v_pk_add_f32 v[50:51], v[50:51], 1.0 op_sel_hi:[1,0]
	v_pk_add_f32 v[52:53], v[52:53], 1.0 op_sel_hi:[1,0]
	s_waitcnt vmcnt(4)
	v_pk_add_f32 v[54:55], v[54:55], 1.0 op_sel_hi:[1,0]
	s_waitcnt lgkmcnt(0)
	v_add_f32_e32 v74, v74, v75
	ds_bpermute_b32 v75, v92, v74
	v_pk_add_f32 v[56:57], v[56:57], 1.0 op_sel_hi:[1,0]
	s_waitcnt lgkmcnt(0)
	v_add_f32_e32 v74, v74, v75
	v_fmamk_f32 v74, v74, 0x3a800000, v93
	v_mul_f32_e32 v75, 0x4f800000, v74
	v_cmp_gt_f32_e32 vcc, s35, v74
	s_nop 1
	v_cndmask_b32_e32 v74, v74, v75, vcc
	v_sqrt_f32_e32 v75, v74
	s_nop 0
	v_add_u32_e32 v76, -1, v75
	v_add_u32_e32 v77, 1, v75
	v_fma_f32 v78, -v76, v75, v74
	v_fma_f32 v79, -v77, v75, v74
	v_cmp_ge_f32_e64 s[4:5], 0, v78
	s_nop 1
	v_cndmask_b32_e64 v75, v75, v76, s[4:5]
	v_cmp_lt_f32_e64 s[4:5], 0, v79
	s_nop 1
	v_cndmask_b32_e64 v75, v75, v77, s[4:5]
	v_mul_f32_e32 v76, 0x37800000, v75
	v_cndmask_b32_e32 v75, v75, v76, vcc
	v_cmp_class_f32_e32 vcc, v74, v94
	s_nop 1
	v_cndmask_b32_e32 v74, v75, v74, vcc
	v_div_scale_f32 v75, s[4:5], v74, v74, 1.0
	v_rcp_f32_e32 v76, v75
	v_div_scale_f32 v77, vcc, 1.0, v74, 1.0
	v_fma_f32 v78, -v75, v76, 1.0
	v_fmac_f32_e32 v76, v78, v76
	v_mul_f32_e32 v78, v77, v76
	v_fma_f32 v79, -v75, v78, v77
	v_fmac_f32_e32 v78, v79, v76
	v_fma_f32 v75, -v75, v78, v77
	v_div_fmas_f32 v75, v75, v76, v78
	v_div_fixup_f32 v74, v75, v74, 1.0
	v_pk_mul_f32 v[30:31], v[30:31], v[74:75] op_sel_hi:[1,0]
	v_pk_mul_f32 v[32:33], v[32:33], v[74:75] op_sel_hi:[1,0]
	v_pk_mul_f32 v[30:31], v[2:3], v[30:31]
	v_pk_mul_f32 v[32:33], v[4:5], v[32:33]
	s_waitcnt vmcnt(1)
	v_pk_fma_f32 v[18:19], v[18:19], v[30:31], v[66:67]
	v_pk_fma_f32 v[20:21], v[20:21], v[32:33], v[68:69]
	v_bfe_u32 v30, v18, 16, 1
	v_add3_u32 v18, v18, v30, s33
	v_bfe_u32 v30, v19, 16, 1
	v_lshrrev_b32_e32 v18, 16, v18
	v_add3_u32 v19, v19, v30, s33
	v_and_or_b32 v18, v19, s3, v18
	v_bfe_u32 v19, v20, 16, 1
	v_add3_u32 v19, v20, v19, s33
	v_bfe_u32 v20, v21, 16, 1
	v_pk_mul_f32 v[44:45], v[44:45], v[74:75] op_sel_hi:[1,0]
	v_lshrrev_b32_e32 v19, 16, v19
	v_add3_u32 v20, v21, v20, s33
	v_pk_mul_f32 v[44:45], v[6:7], v[44:45]
	v_and_or_b32 v19, v20, s3, v19
	v_add_co_u32_e32 v20, vcc, s36, v28
	s_waitcnt vmcnt(0)
	v_pk_fma_f32 v[44:45], v[46:47], v[44:45], v[70:71]
	v_addc_co_u32_e32 v21, vcc, -1, v29, vcc
	v_pk_mul_f32 v[34:35], v[34:35], v[74:75] op_sel_hi:[1,0]
	global_store_dwordx2 v[20:21], v[18:19], off offset:-1536
	v_pk_mul_f32 v[34:35], v[8:9], v[34:35]
	v_pk_fma_f32 v[34:35], v[48:49], v[34:35], v[72:73]
	v_cvt_pk_bf16_f32 v18, v44, v45
	v_pk_mul_f32 v[42:43], v[42:43], v[74:75] op_sel_hi:[1,0]
	v_pk_mul_f32 v[42:43], v[10:11], v[42:43]
	v_pk_fma_f32 v[42:43], v[50:51], v[42:43], v[58:59]
	v_cvt_pk_bf16_f32 v19, v34, v35
	v_pk_mul_f32 v[36:37], v[36:37], v[74:75] op_sel_hi:[1,0]
	global_store_dwordx2 v[20:21], v[18:19], off offset:-1024
	v_pk_mul_f32 v[36:37], v[12:13], v[36:37]
	v_pk_fma_f32 v[36:37], v[52:53], v[36:37], v[60:61]
	v_cvt_pk_bf16_f32 v18, v42, v43
	v_pk_mul_f32 v[38:39], v[38:39], v[74:75] op_sel_hi:[1,0]
	v_pk_mul_f32 v[38:39], v[14:15], v[38:39]
	v_pk_fma_f32 v[38:39], v[54:55], v[38:39], v[62:63]
	v_cvt_pk_bf16_f32 v19, v36, v37
	v_pk_mul_f32 v[40:41], v[40:41], v[74:75] op_sel_hi:[1,0]
	global_store_dwordx2 v[20:21], v[18:19], off offset:-512
	v_pk_mul_f32 v[40:41], v[16:17], v[40:41]
	v_pk_fma_f32 v[40:41], v[56:57], v[40:41], v[64:65]
	v_cvt_pk_bf16_f32 v18, v38, v39
	v_cvt_pk_bf16_f32 v19, v40, v41
	v_lshl_add_u64 v[28:29], v[28:29], 0, s[12:13]
	global_store_dwordx2 v[20:21], v[18:19], off
	s_cbranch_scc0 .LBB0_679
.LBB0_677:
	v_add_co_u32_e32 v18, vcc, 0xdd200000, v28
	s_cmpk_lt_i32 s6, 0x400
	s_nop 0
	v_addc_co_u32_e32 v19, vcc, -1, v29, vcc
	global_load_dwordx2 v[20:21], v[18:19], off offset:-1536
	global_load_dwordx2 v[34:35], v[18:19], off offset:-1024
	global_load_dwordx2 v[36:37], v[18:19], off offset:-512
	global_load_dwordx2 v[40:41], v[18:19], off
	s_cselect_b64 s[4:5], -1, 0
	s_cmpk_gt_i32 s6, 0x3ff
	s_waitcnt vmcnt(3)
	v_lshlrev_b32_e32 v30, 16, v20
	v_and_b32_e32 v31, 0xffff0000, v20
	v_lshlrev_b32_e32 v32, 16, v21
	v_and_b32_e32 v33, 0xffff0000, v21
	s_waitcnt vmcnt(2)
	v_lshlrev_b32_e32 v44, 16, v34
	v_and_b32_e32 v45, 0xffff0000, v34
	v_lshlrev_b32_e32 v34, 16, v35
	v_and_b32_e32 v35, 0xffff0000, v35
	s_waitcnt vmcnt(1)
	v_lshlrev_b32_e32 v42, 16, v36
	v_and_b32_e32 v43, 0xffff0000, v36
	v_lshlrev_b32_e32 v36, 16, v37
	v_and_b32_e32 v37, 0xffff0000, v37
	s_waitcnt vmcnt(0)
	v_lshlrev_b32_e32 v38, 16, v40
	v_and_b32_e32 v39, 0xffff0000, v40
	v_lshlrev_b32_e32 v40, 16, v41
	v_and_b32_e32 v41, 0xffff0000, v41
	s_cbranch_scc1 .LBB0_676
	v_add_co_u32_e32 v48, vcc, 0xff200000, v28
	v_lshl_add_u64 v[56:57], v[28:29], 0, s[14:15]
	s_nop 0
	v_addc_co_u32_e32 v49, vcc, -1, v29, vcc
	v_add_co_u32_e32 v52, vcc, s7, v28
	global_load_dwordx2 v[46:47], v[48:49], off offset:-1536
	s_nop 0
	v_addc_co_u32_e32 v53, vcc, -1, v29, vcc
	v_add_co_u32_e32 v62, vcc, s9, v28
	global_load_dwordx2 v[50:51], v[52:53], off offset:-1536
	s_nop 0
	v_addc_co_u32_e32 v63, vcc, -1, v29, vcc
	v_add_co_u32_e32 v76, vcc, s22, v28
	global_load_dwordx2 v[54:55], v[62:63], off offset:-1536
	s_nop 0
	v_addc_co_u32_e32 v77, vcc, -1, v29, vcc
	v_add_co_u32_e32 v78, vcc, s23, v28
	global_load_dwordx2 v[60:61], v[76:77], off offset:-1536
	s_nop 0
	v_addc_co_u32_e32 v79, vcc, -1, v29, vcc
	v_add_co_u32_e32 v70, vcc, s30, v28
	global_load_dwordx2 v[74:75], v[78:79], off offset:-1536
	s_nop 0
	v_addc_co_u32_e32 v71, vcc, -1, v29, vcc
	global_load_dwordx2 v[72:73], v[70:71], off offset:-1536
	v_add_co_u32_e32 v64, vcc, s31, v28
	s_nop 1
	v_addc_co_u32_e32 v65, vcc, -1, v29, vcc
	global_load_dwordx2 v[68:69], v[64:65], off offset:-1536
	global_load_dwordx2 v[58:59], v[28:29], off offset:-1536
	global_load_dwordx4 v[18:21], v[26:27], off
	global_load_dwordx2 v[66:67], v[48:49], off offset:-1024
	global_load_dwordx2 v[80:81], v[48:49], off offset:-512
	global_load_dwordx2 v[82:83], v[48:49], off
	global_load_dwordx2 v[96:97], v[52:53], off offset:-1024
	global_load_dwordx2 v[98:99], v[52:53], off offset:-512
	global_load_dwordx2 v[84:85], v[52:53], off
	global_load_dwordx2 v[100:101], v[62:63], off offset:-1024
	global_load_dwordx2 v[102:103], v[62:63], off offset:-512
	global_load_dwordx2 v[86:87], v[62:63], off
	global_load_dwordx2 v[104:105], v[76:77], off offset:-1024
	global_load_dwordx2 v[106:107], v[76:77], off offset:-512
	global_load_dwordx2 v[88:89], v[76:77], off
	global_load_dwordx2 v[108:109], v[78:79], off offset:-1024
	global_load_dwordx2 v[110:111], v[78:79], off offset:-512
	global_load_dwordx2 v[90:91], v[78:79], off
	s_waitcnt vmcnt(23)
	v_lshlrev_b32_e32 v48, 16, v46
	v_and_b32_e32 v49, 0xffff0000, v46
	v_lshlrev_b32_e32 v46, 16, v47
	v_and_b32_e32 v47, 0xffff0000, v47
	v_pk_add_f32 v[48:49], v[48:49], 0 op_sel_hi:[1,0]
	v_pk_add_f32 v[46:47], v[46:47], 0 op_sel_hi:[1,0]
	s_waitcnt vmcnt(22)
	v_lshlrev_b32_e32 v52, 16, v50
	v_and_b32_e32 v53, 0xffff0000, v50
	v_lshlrev_b32_e32 v50, 16, v51
	v_and_b32_e32 v51, 0xffff0000, v51
	v_pk_add_f32 v[46:47], v[46:47], v[50:51]
	v_pk_add_f32 v[48:49], v[48:49], v[52:53]
	s_waitcnt vmcnt(21)
	v_lshlrev_b32_e32 v50, 16, v54
	v_and_b32_e32 v51, 0xffff0000, v54
	v_lshlrev_b32_e32 v52, 16, v55
	v_and_b32_e32 v53, 0xffff0000, v55
	v_pk_add_f32 v[48:49], v[48:49], v[50:51]
	v_pk_add_f32 v[46:47], v[46:47], v[52:53]
	s_waitcnt vmcnt(20)
	v_lshlrev_b32_e32 v50, 16, v60
	v_and_b32_e32 v51, 0xffff0000, v60
	v_lshlrev_b32_e32 v52, 16, v61
	v_and_b32_e32 v53, 0xffff0000, v61
	v_pk_add_f32 v[46:47], v[46:47], v[52:53]
	v_pk_add_f32 v[48:49], v[48:49], v[50:51]
	s_waitcnt vmcnt(19)
	v_lshlrev_b32_e32 v50, 16, v74
	v_and_b32_e32 v51, 0xffff0000, v74
	v_lshlrev_b32_e32 v52, 16, v75
	v_and_b32_e32 v53, 0xffff0000, v75
	v_pk_add_f32 v[48:49], v[48:49], v[50:51]
	v_pk_add_f32 v[46:47], v[46:47], v[52:53]
	s_waitcnt vmcnt(18)
	v_lshlrev_b32_e32 v60, 16, v72
	v_and_b32_e32 v61, 0xffff0000, v72
	v_lshlrev_b32_e32 v62, 16, v73
	v_and_b32_e32 v63, 0xffff0000, v73
	global_load_dwordx2 v[50:51], v[70:71], off offset:-1024
	global_load_dwordx2 v[52:53], v[70:71], off offset:-512
	global_load_dwordx2 v[54:55], v[70:71], off
	v_pk_add_f32 v[46:47], v[46:47], v[62:63]
	v_pk_add_f32 v[48:49], v[48:49], v[60:61]
	global_load_dwordx2 v[60:61], v[64:65], off offset:-1024
	global_load_dwordx2 v[62:63], v[64:65], off offset:-512
	global_load_dwordx2 v[70:71], v[64:65], off
	s_waitcnt vmcnt(23)
	v_lshlrev_b32_e32 v64, 16, v68
	v_and_b32_e32 v65, 0xffff0000, v68
	v_lshlrev_b32_e32 v68, 16, v69
	v_and_b32_e32 v69, 0xffff0000, v69
	v_pk_add_f32 v[48:49], v[48:49], v[64:65]
	s_waitcnt vmcnt(22)
	v_lshlrev_b32_e32 v74, 16, v58
	v_and_b32_e32 v75, 0xffff0000, v58
	v_pk_add_f32 v[46:47], v[46:47], v[68:69]
	v_lshlrev_b32_e32 v58, 16, v59
	v_and_b32_e32 v59, 0xffff0000, v59
	v_pk_add_f32 v[48:49], v[48:49], v[74:75]
	v_pk_add_f32 v[46:47], v[46:47], v[58:59]
	s_waitcnt vmcnt(21)
	v_pk_fma_f32 v[18:19], v[48:49], v[18:19], v[30:31]
	v_pk_fma_f32 v[32:33], v[46:47], v[20:21], v[32:33]
	v_bfe_u32 v20, v18, 16, 1
	v_add3_u32 v30, v18, v20, s33
	v_bfe_u32 v18, v19, 16, 1
	v_and_b32_sdwa v20, v33, v95 dst_sel:DWORD dst_unused:UNUSED_PAD src0_sel:WORD_1 src1_sel:DWORD
	v_add3_u32 v18, v19, v18, s33
	v_bfe_u32 v19, v32, 16, 1
	v_add3_u32 v20, v33, v20, s33
	v_and_b32_e32 v31, 0xffff0000, v18
	v_add3_u32 v19, v32, v19, s33
	v_and_b32_e32 v33, 0xffff0000, v20
	v_or_b32_sdwa v18, v31, v30 dst_sel:DWORD dst_unused:UNUSED_PAD src0_sel:DWORD src1_sel:WORD_1
	v_or_b32_sdwa v19, v33, v19 dst_sel:DWORD dst_unused:UNUSED_PAD src0_sel:DWORD src1_sel:WORD_1
	global_load_dwordx2 v[64:65], v[28:29], off offset:-1024
	global_load_dwordx2 v[68:69], v[28:29], off offset:-512
	global_load_dwordx2 v[72:73], v[28:29], off
	s_waitcnt vmcnt(23)
	v_lshlrev_b32_e32 v48, 16, v66
	global_store_dwordx2 v[56:57], v[18:19], off
	global_load_dwordx4 v[18:21], v[26:27], off offset:1024
	v_and_b32_e32 v49, 0xffff0000, v66
	v_lshlrev_b32_e32 v56, 16, v67
	v_and_b32_e32 v57, 0xffff0000, v67
	v_pk_add_f32 v[56:57], v[56:57], 0 op_sel_hi:[1,0]
	v_pk_add_f32 v[48:49], v[48:49], 0 op_sel_hi:[1,0]
	s_waitcnt vmcnt(22)
	v_lshlrev_b32_e32 v58, 16, v96
	v_and_b32_e32 v59, 0xffff0000, v96
	v_lshlrev_b32_e32 v66, 16, v97
	v_and_b32_e32 v67, 0xffff0000, v97
	v_pk_add_f32 v[48:49], v[48:49], v[58:59]
	v_pk_add_f32 v[56:57], v[56:57], v[66:67]
	s_waitcnt vmcnt(19)
	v_lshlrev_b32_e32 v58, 16, v100
	v_and_b32_e32 v59, 0xffff0000, v100
	v_lshlrev_b32_e32 v66, 16, v101
	v_and_b32_e32 v67, 0xffff0000, v101
	v_pk_add_f32 v[56:57], v[56:57], v[66:67]
	v_pk_add_f32 v[48:49], v[48:49], v[58:59]
	s_waitcnt vmcnt(16)
	v_lshlrev_b32_e32 v58, 16, v104
	v_and_b32_e32 v59, 0xffff0000, v104
	v_lshlrev_b32_e32 v66, 16, v105
	v_and_b32_e32 v67, 0xffff0000, v105
	v_pk_add_f32 v[48:49], v[48:49], v[58:59]
	v_pk_add_f32 v[56:57], v[56:57], v[66:67]
	s_waitcnt vmcnt(13)
	v_lshlrev_b32_e32 v58, 16, v108
	v_and_b32_e32 v59, 0xffff0000, v108
	v_lshlrev_b32_e32 v66, 16, v109
	v_and_b32_e32 v67, 0xffff0000, v109
	v_pk_add_f32 v[56:57], v[56:57], v[66:67]
	v_pk_add_f32 v[48:49], v[48:49], v[58:59]
	v_lshl_add_u64 v[46:47], v[28:29], 0, s[16:17]
	v_and_b32_e32 v30, 0xffff0000, v30
	s_waitcnt vmcnt(10)
	v_lshlrev_b32_e32 v58, 16, v50
	v_and_b32_e32 v59, 0xffff0000, v50
	v_lshlrev_b32_e32 v50, 16, v51
	v_and_b32_e32 v51, 0xffff0000, v51
	v_pk_add_f32 v[48:49], v[48:49], v[58:59]
	v_pk_add_f32 v[50:51], v[56:57], v[50:51]
	s_waitcnt vmcnt(7)
	v_lshlrev_b32_e32 v56, 16, v60
	v_and_b32_e32 v57, 0xffff0000, v60
	v_pk_add_f32 v[48:49], v[48:49], v[56:57]
	v_lshlrev_b32_e32 v58, 16, v61
	v_and_b32_e32 v59, 0xffff0000, v61
	v_pk_add_f32 v[50:51], v[50:51], v[58:59]
	v_lshlrev_b32_e32 v60, 16, v98
	v_and_b32_e32 v61, 0xffff0000, v98
	s_waitcnt vmcnt(4)
	v_lshlrev_b32_e32 v56, 16, v64
	v_and_b32_e32 v57, 0xffff0000, v64
	v_pk_add_f32 v[48:49], v[48:49], v[56:57]
	v_lshlrev_b32_e32 v58, 16, v65
	v_and_b32_e32 v59, 0xffff0000, v65
	s_waitcnt vmcnt(0)
	v_pk_fma_f32 v[44:45], v[48:49], v[18:19], v[44:45]
	v_pk_add_f32 v[50:51], v[50:51], v[58:59]
	v_pk_fma_f32 v[34:35], v[50:51], v[20:21], v[34:35]
	v_and_b32_sdwa v20, v35, v95 dst_sel:DWORD dst_unused:UNUSED_PAD src0_sel:WORD_1 src1_sel:DWORD
	v_cvt_pk_bf16_f32 v18, v44, v45
	v_bfe_u32 v19, v34, 16, 1
	v_add3_u32 v20, v35, v20, s33
	v_add3_u32 v19, v34, v19, s33
	v_and_b32_e32 v35, 0xffff0000, v20
	v_or_b32_sdwa v19, v35, v19 dst_sel:DWORD dst_unused:UNUSED_PAD src0_sel:DWORD src1_sel:WORD_1
	global_store_dwordx2 v[46:47], v[18:19], off
	global_load_dwordx4 v[18:21], v[26:27], off offset:2048
	v_lshlrev_b32_e32 v56, 16, v80
	v_and_b32_e32 v57, 0xffff0000, v80
	v_lshlrev_b32_e32 v58, 16, v81
	v_and_b32_e32 v59, 0xffff0000, v81
	v_pk_add_f32 v[58:59], v[58:59], 0 op_sel_hi:[1,0]
	v_pk_add_f32 v[56:57], v[56:57], 0 op_sel_hi:[1,0]
	v_lshlrev_b32_e32 v64, 16, v99
	v_and_b32_e32 v65, 0xffff0000, v99
	v_pk_add_f32 v[56:57], v[56:57], v[60:61]
	v_pk_add_f32 v[58:59], v[58:59], v[64:65]
	v_lshlrev_b32_e32 v60, 16, v102
	v_and_b32_e32 v61, 0xffff0000, v102
	v_lshlrev_b32_e32 v64, 16, v103
	v_and_b32_e32 v65, 0xffff0000, v103
	v_pk_add_f32 v[58:59], v[58:59], v[64:65]
	v_pk_add_f32 v[56:57], v[56:57], v[60:61]
	v_lshlrev_b32_e32 v60, 16, v106
	v_and_b32_e32 v61, 0xffff0000, v106
	v_lshlrev_b32_e32 v64, 16, v107
	v_and_b32_e32 v65, 0xffff0000, v107
	v_pk_add_f32 v[56:57], v[56:57], v[60:61]
	v_pk_add_f32 v[58:59], v[58:59], v[64:65]
	v_lshlrev_b32_e32 v60, 16, v110
	v_and_b32_e32 v61, 0xffff0000, v110
	v_lshlrev_b32_e32 v64, 16, v111
	v_and_b32_e32 v65, 0xffff0000, v111
	v_pk_add_f32 v[58:59], v[58:59], v[64:65]
	v_pk_add_f32 v[56:57], v[56:57], v[60:61]
	v_lshlrev_b32_e32 v60, 16, v52
	v_and_b32_e32 v61, 0xffff0000, v52
	v_lshlrev_b32_e32 v52, 16, v53
	v_and_b32_e32 v53, 0xffff0000, v53
	v_pk_add_f32 v[56:57], v[56:57], v[60:61]
	v_pk_add_f32 v[52:53], v[58:59], v[52:53]
	v_lshlrev_b32_e32 v58, 16, v62
	v_and_b32_e32 v59, 0xffff0000, v62
	v_lshlrev_b32_e32 v60, 16, v63
	v_and_b32_e32 v61, 0xffff0000, v63
	v_lshlrev_b32_e32 v48, 16, v68
	v_and_b32_e32 v49, 0xffff0000, v68
	v_lshlrev_b32_e32 v50, 16, v69
	v_and_b32_e32 v51, 0xffff0000, v69
	v_pk_add_f32 v[52:53], v[52:53], v[60:61]
	v_pk_add_f32 v[56:57], v[56:57], v[58:59]
	v_pk_add_f32 v[50:51], v[52:53], v[50:51]
	v_pk_add_f32 v[48:49], v[56:57], v[48:49]
	v_lshl_add_u64 v[46:47], v[28:29], 0, s[18:19]
	v_lshlrev_b32_e32 v52, 16, v82
	v_and_b32_e32 v53, 0xffff0000, v82
	v_lshlrev_b32_e32 v56, 16, v83
	v_and_b32_e32 v57, 0xffff0000, v83
	v_pk_add_f32 v[56:57], v[56:57], 0 op_sel_hi:[1,0]
	v_pk_add_f32 v[52:53], v[52:53], 0 op_sel_hi:[1,0]
	v_lshlrev_b32_e32 v58, 16, v84
	v_and_b32_e32 v59, 0xffff0000, v84
	v_lshlrev_b32_e32 v60, 16, v85
	v_and_b32_e32 v61, 0xffff0000, v85
	v_pk_add_f32 v[52:53], v[52:53], v[58:59]
	v_pk_add_f32 v[56:57], v[56:57], v[60:61]
	v_lshlrev_b32_e32 v58, 16, v86
	v_and_b32_e32 v59, 0xffff0000, v86
	v_lshlrev_b32_e32 v60, 16, v87
	v_and_b32_e32 v61, 0xffff0000, v87
	v_pk_add_f32 v[56:57], v[56:57], v[60:61]
	v_pk_add_f32 v[52:53], v[52:53], v[58:59]
	v_lshlrev_b32_e32 v58, 16, v88
	v_and_b32_e32 v59, 0xffff0000, v88
	v_lshlrev_b32_e32 v60, 16, v89
	v_and_b32_e32 v61, 0xffff0000, v89
	v_pk_add_f32 v[52:53], v[52:53], v[58:59]
	v_pk_add_f32 v[56:57], v[56:57], v[60:61]
	v_lshlrev_b32_e32 v58, 16, v90
	v_and_b32_e32 v59, 0xffff0000, v90
	v_lshlrev_b32_e32 v60, 16, v91
	v_and_b32_e32 v61, 0xffff0000, v91
	v_pk_add_f32 v[56:57], v[56:57], v[60:61]
	v_pk_add_f32 v[52:53], v[52:53], v[58:59]
	v_lshlrev_b32_e32 v58, 16, v54
	v_and_b32_e32 v59, 0xffff0000, v54
	s_waitcnt vmcnt(0)
	v_pk_fma_f32 v[36:37], v[50:51], v[20:21], v[36:37]
	v_pk_fma_f32 v[42:43], v[48:49], v[18:19], v[42:43]
	v_and_b32_sdwa v21, v37, v95 dst_sel:DWORD dst_unused:UNUSED_PAD src0_sel:WORD_1 src1_sel:DWORD
	v_bfe_u32 v20, v36, 16, 1
	v_add3_u32 v21, v37, v21, s33
	v_add3_u32 v20, v36, v20, s33
	v_and_b32_e32 v37, 0xffff0000, v21
	v_cvt_pk_bf16_f32 v18, v42, v43
	v_or_b32_sdwa v19, v37, v20 dst_sel:DWORD dst_unused:UNUSED_PAD src0_sel:DWORD src1_sel:WORD_1
	global_store_dwordx2 v[46:47], v[18:19], off
	global_load_dwordx4 v[18:21], v[26:27], off offset:3072
	v_lshlrev_b32_e32 v54, 16, v55
	v_and_b32_e32 v55, 0xffff0000, v55
	v_pk_add_f32 v[52:53], v[52:53], v[58:59]
	v_pk_add_f32 v[54:55], v[56:57], v[54:55]
	v_lshlrev_b32_e32 v56, 16, v70
	v_and_b32_e32 v57, 0xffff0000, v70
	v_lshlrev_b32_e32 v58, 16, v71
	v_and_b32_e32 v59, 0xffff0000, v71
	v_lshlrev_b32_e32 v48, 16, v72
	v_and_b32_e32 v49, 0xffff0000, v72
	v_lshlrev_b32_e32 v50, 16, v73
	v_and_b32_e32 v51, 0xffff0000, v73
	v_pk_add_f32 v[54:55], v[54:55], v[58:59]
	v_pk_add_f32 v[52:53], v[52:53], v[56:57]
	v_pk_add_f32 v[50:51], v[54:55], v[50:51]
	v_pk_add_f32 v[48:49], v[52:53], v[48:49]
	v_and_b32_sdwa v52, v32, v95 dst_sel:DWORD dst_unused:UNUSED_PAD src0_sel:WORD_1 src1_sel:DWORD
	v_add3_u32 v32, v32, v52, s33
	v_and_b32_sdwa v52, v45, v95 dst_sel:DWORD dst_unused:UNUSED_PAD src0_sel:WORD_1 src1_sel:DWORD
	v_and_b32_sdwa v53, v44, v95 dst_sel:DWORD dst_unused:UNUSED_PAD src0_sel:WORD_1 src1_sel:DWORD
	v_and_b32_sdwa v54, v34, v95 dst_sel:DWORD dst_unused:UNUSED_PAD src0_sel:WORD_1 src1_sel:DWORD
	v_add3_u32 v45, v45, v52, s33
	v_add3_u32 v44, v44, v53, s33
	v_add3_u32 v34, v34, v54, s33
	v_and_b32_sdwa v52, v43, v95 dst_sel:DWORD dst_unused:UNUSED_PAD src0_sel:WORD_1 src1_sel:DWORD
	v_and_b32_sdwa v53, v42, v95 dst_sel:DWORD dst_unused:UNUSED_PAD src0_sel:WORD_1 src1_sel:DWORD
	v_and_b32_sdwa v54, v36, v95 dst_sel:DWORD dst_unused:UNUSED_PAD src0_sel:WORD_1 src1_sel:DWORD
	v_add3_u32 v43, v43, v52, s33
	v_add3_u32 v42, v42, v53, s33
	v_add3_u32 v36, v36, v54, s33
	v_lshl_add_u64 v[46:47], v[28:29], 0, s[20:21]
	v_and_b32_e32 v32, 0xffff0000, v32
	v_and_b32_e32 v45, 0xffff0000, v45
	v_and_b32_e32 v44, 0xffff0000, v44
	v_and_b32_e32 v34, 0xffff0000, v34
	v_and_b32_e32 v43, 0xffff0000, v43
	v_and_b32_e32 v42, 0xffff0000, v42
	v_and_b32_e32 v36, 0xffff0000, v36
	s_waitcnt vmcnt(0)
	v_pk_fma_f32 v[20:21], v[50:51], v[20:21], v[40:41]
	v_pk_fma_f32 v[18:19], v[48:49], v[18:19], v[38:39]
	v_and_b32_sdwa v49, v21, v95 dst_sel:DWORD dst_unused:UNUSED_PAD src0_sel:WORD_1 src1_sel:DWORD
	v_bfe_u32 v38, v18, 16, 1
	v_bfe_u32 v39, v19, 16, 1
	v_bfe_u32 v40, v20, 16, 1
	v_and_b32_sdwa v41, v19, v95 dst_sel:DWORD dst_unused:UNUSED_PAD src0_sel:WORD_1 src1_sel:DWORD
	v_and_b32_sdwa v48, v18, v95 dst_sel:DWORD dst_unused:UNUSED_PAD src0_sel:WORD_1 src1_sel:DWORD
	v_and_b32_sdwa v50, v20, v95 dst_sel:DWORD dst_unused:UNUSED_PAD src0_sel:WORD_1 src1_sel:DWORD
	v_add3_u32 v38, v18, v38, s33
	v_add3_u32 v21, v21, v49, s33
	v_add3_u32 v51, v19, v39, s33
	v_add3_u32 v52, v20, v40, s33
	v_add3_u32 v19, v19, v41, s33
	v_add3_u32 v18, v18, v48, s33
	v_add3_u32 v20, v20, v50, s33
	v_lshrrev_b32_e32 v40, 16, v38
	v_and_b32_e32 v41, 0xffff0000, v21
	v_and_b32_e32 v39, 0xffff0000, v19
	v_and_b32_e32 v38, 0xffff0000, v18
	v_and_or_b32 v18, v51, s3, v40
	v_and_b32_e32 v40, 0xffff0000, v20
	v_or_b32_sdwa v19, v41, v52 dst_sel:DWORD dst_unused:UNUSED_PAD src0_sel:DWORD src1_sel:WORD_1
	global_store_dwordx2 v[46:47], v[18:19], off
	s_branch .LBB0_676

.LBB0_891:
	v_pk_mul_f32 v[62:63], v[32:33], v[32:33]
	v_pk_mul_f32 v[64:65], v[30:31], v[30:31]
	v_pk_mul_f32 v[58:59], v[34:35], v[34:35]
	v_pk_mul_f32 v[60:61], v[38:39], v[38:39]
	v_pk_mov_b32 v[66:67], v[64:65], v[62:63] op_sel:[1,0]
	v_mov_b32_e32 v65, v63
	v_pk_add_f32 v[62:63], v[66:67], v[64:65]
	v_pk_mov_b32 v[64:65], v[60:61], v[58:59] op_sel:[1,0]
	v_mov_b32_e32 v61, v59
	v_pk_add_f32 v[58:59], v[64:65], v[60:61]
	s_add_i32 s10, s6, 0xfffffc00
	v_pk_add_f32 v[58:59], v[58:59], v[58:59] op_sel_hi:[0,1]
	v_mul_f32_e32 v58, v44, v44
	s_lshr_b32 s10, s10, 12
	v_pk_fma_f32 v[60:61], v[44:45], v[44:45], v[58:59] op_sel_hi:[1,1,0]
	v_mul_f32_e32 v58, v40, v40
	s_mulk_i32 s10, 0x1800
	s_and_b64 s[4:5], s[4:5], exec
	v_pk_add_f32 v[62:63], v[62:63], v[62:63] op_sel_hi:[0,1]
	v_pk_fma_f32 v[64:65], v[40:41], v[40:41], v[58:59] op_sel_hi:[1,1,0]
	s_cselect_b32 s10, 0x6000, s10
	v_mul_f32_e32 v60, v36, v36
	v_mul_f32_e32 v64, v37, v37
	v_mul_f32_e32 v62, v42, v42
	v_mul_f32_e32 v58, v43, v43
	s_lshl_b64 s[4:5], s[10:11], 2
	v_pk_add_f32 v[66:67], v[60:61], v[64:65]
	v_pk_add_f32 v[68:69], v[62:63], v[58:59]
	v_lshl_add_u64 v[54:55], v[24:25], 0, s[4:5]
	v_lshl_add_u64 v[70:71], v[22:23], 0, s[4:5]
	v_pk_add_f32 v[66:67], v[66:67], v[68:69]
	global_load_dwordx4 v[18:21], v[54:55], off
	global_load_dwordx4 v[46:49], v[54:55], off offset:1024
	global_load_dwordx4 v[50:53], v[54:55], off offset:2048
	s_nop 0
	global_load_dwordx4 v[54:57], v[54:55], off offset:3072
	s_nop 0
	global_load_dwordx4 v[58:61], v[70:71], off offset:2048
	global_load_dwordx4 v[62:65], v[70:71], off offset:3072
	v_add_f32_e32 v74, v66, v67
	global_load_dwordx4 v[66:69], v[70:71], off
	s_nop 0
	global_load_dwordx4 v[70:73], v[70:71], off offset:1024
	v_add_f32_dpp v74, v74, v74 row_ror:8 row_mask:0xf bank_mask:0xf bound_ctrl:1
	s_add_i32 s6, s6, s8
	s_cmpk_lt_i32 s6, 0x4400
	v_add_f32_dpp v74, v74, v74 row_ror:4 row_mask:0xf bank_mask:0xf bound_ctrl:1
	s_waitcnt vmcnt(7)
	v_pk_add_f32 v[18:19], v[18:19], 1.0 op_sel_hi:[1,0]
	v_add_f32_dpp v74, v74, v74 row_ror:2 row_mask:0xf bank_mask:0xf bound_ctrl:1
	v_pk_add_f32 v[20:21], v[20:21], 1.0 op_sel_hi:[1,0]
	s_waitcnt vmcnt(6)
	v_pk_add_f32 v[46:47], v[46:47], 1.0 op_sel_hi:[1,0]
	v_add_f32_dpp v74, v74, v74 row_ror:1 row_mask:0xf bank_mask:0xf bound_ctrl:1
	ds_bpermute_b32 v75, v1, v74
	v_pk_add_f32 v[48:49], v[48:49], 1.0 op_sel_hi:[1,0]
	s_waitcnt vmcnt(5)
	v_pk_add_f32 v[50:51], v[50:51], 1.0 op_sel_hi:[1,0]
	v_pk_add_f32 v[52:53], v[52:53], 1.0 op_sel_hi:[1,0]
	s_waitcnt vmcnt(4)
	v_pk_add_f32 v[54:55], v[54:55], 1.0 op_sel_hi:[1,0]
	s_waitcnt lgkmcnt(0)
	v_add_f32_e32 v74, v74, v75
	ds_bpermute_b32 v75, v94, v74
	v_pk_add_f32 v[56:57], v[56:57], 1.0 op_sel_hi:[1,0]
	s_waitcnt lgkmcnt(0)
	v_add_f32_e32 v74, v74, v75
	v_fmamk_f32 v74, v74, 0x3a800000, v95
	v_mul_f32_e32 v75, 0x4f800000, v74
	v_cmp_gt_f32_e32 vcc, s42, v74
	s_nop 1
	v_cndmask_b32_e32 v74, v74, v75, vcc
	v_sqrt_f32_e32 v75, v74
	s_nop 0
	v_add_u32_e32 v76, -1, v75
	v_add_u32_e32 v77, 1, v75
	v_fma_f32 v78, -v76, v75, v74
	v_fma_f32 v79, -v77, v75, v74
	v_cmp_ge_f32_e64 s[4:5], 0, v78
	s_nop 1
	v_cndmask_b32_e64 v75, v75, v76, s[4:5]
	v_cmp_lt_f32_e64 s[4:5], 0, v79
	s_nop 1
	v_cndmask_b32_e64 v75, v75, v77, s[4:5]
	v_mul_f32_e32 v76, 0x37800000, v75
	v_cndmask_b32_e32 v75, v75, v76, vcc
	v_cmp_class_f32_e32 vcc, v74, v96
	s_nop 1
	v_cndmask_b32_e32 v74, v75, v74, vcc
	v_div_scale_f32 v75, s[4:5], v74, v74, 1.0
	v_rcp_f32_e32 v76, v75
	v_div_scale_f32 v77, vcc, 1.0, v74, 1.0
	v_fma_f32 v78, -v75, v76, 1.0
	v_fmac_f32_e32 v76, v78, v76
	v_mul_f32_e32 v78, v77, v76
	v_fma_f32 v79, -v75, v78, v77
	v_fmac_f32_e32 v78, v79, v76
	v_fma_f32 v75, -v75, v78, v77
	v_div_fmas_f32 v75, v75, v76, v78
	v_div_fixup_f32 v74, v75, v74, 1.0
	v_pk_mul_f32 v[30:31], v[30:31], v[74:75] op_sel_hi:[1,0]
	v_pk_mul_f32 v[32:33], v[32:33], v[74:75] op_sel_hi:[1,0]
	v_pk_mul_f32 v[30:31], v[10:11], v[30:31]
	v_pk_mul_f32 v[32:33], v[12:13], v[32:33]
	s_waitcnt vmcnt(1)
	v_pk_fma_f32 v[18:19], v[18:19], v[30:31], v[66:67]
	v_pk_fma_f32 v[20:21], v[20:21], v[32:33], v[68:69]
	v_bfe_u32 v30, v18, 16, 1
	v_add3_u32 v18, v18, v30, s37
	v_bfe_u32 v30, v19, 16, 1
	v_lshrrev_b32_e32 v18, 16, v18
	v_add3_u32 v19, v19, v30, s37
	v_and_or_b32 v18, v19, s3, v18
	v_bfe_u32 v19, v20, 16, 1
	v_add3_u32 v19, v20, v19, s37
	v_bfe_u32 v20, v21, 16, 1
	v_pk_mul_f32 v[38:39], v[38:39], v[74:75] op_sel_hi:[1,0]
	v_lshrrev_b32_e32 v19, 16, v19
	v_add3_u32 v20, v21, v20, s37
	v_pk_mul_f32 v[38:39], v[2:3], v[38:39]
	v_and_or_b32 v19, v20, s3, v19
	v_add_co_u32_e32 v20, vcc, s43, v28
	s_waitcnt vmcnt(0)
	v_pk_fma_f32 v[38:39], v[46:47], v[38:39], v[70:71]
	v_addc_co_u32_e32 v21, vcc, -1, v29, vcc
	v_pk_mul_f32 v[34:35], v[34:35], v[74:75] op_sel_hi:[1,0]
	global_store_dwordx2 v[20:21], v[18:19], off offset:-1536
	v_pk_mul_f32 v[34:35], v[4:5], v[34:35]
	v_pk_fma_f32 v[34:35], v[48:49], v[34:35], v[72:73]
	v_cvt_pk_bf16_f32 v18, v38, v39
	v_pk_mul_f32 v[44:45], v[44:45], v[74:75] op_sel_hi:[1,0]
	v_pk_mul_f32 v[44:45], v[6:7], v[44:45]
	v_pk_fma_f32 v[44:45], v[50:51], v[44:45], v[58:59]
	v_cvt_pk_bf16_f32 v19, v34, v35
	v_pk_mul_f32 v[40:41], v[40:41], v[74:75] op_sel_hi:[1,0]
	global_store_dwordx2 v[20:21], v[18:19], off offset:-1024
	v_pk_mul_f32 v[40:41], v[8:9], v[40:41]
	v_pk_fma_f32 v[40:41], v[52:53], v[40:41], v[60:61]
	v_cvt_pk_bf16_f32 v18, v44, v45
	v_pk_mul_f32 v[36:37], v[36:37], v[74:75] op_sel_hi:[1,0]
	v_pk_mul_f32 v[36:37], v[14:15], v[36:37]
	v_pk_fma_f32 v[36:37], v[54:55], v[36:37], v[62:63]
	v_cvt_pk_bf16_f32 v19, v40, v41
	v_pk_mul_f32 v[42:43], v[42:43], v[74:75] op_sel_hi:[1,0]
	global_store_dwordx2 v[20:21], v[18:19], off offset:-512
	v_pk_mul_f32 v[42:43], v[16:17], v[42:43]
	v_pk_fma_f32 v[42:43], v[56:57], v[42:43], v[64:65]
	v_cvt_pk_bf16_f32 v18, v36, v37
	v_cvt_pk_bf16_f32 v19, v42, v43
	v_lshl_add_u64 v[28:29], v[28:29], 0, s[12:13]
	global_store_dwordx2 v[20:21], v[18:19], off
	s_cbranch_scc0 .LBB0_894
.LBB0_892:
	v_add_co_u32_e32 v18, vcc, 0xdcc00000, v28
	s_cmpk_lt_i32 s6, 0x400
	s_nop 0
	v_addc_co_u32_e32 v19, vcc, -1, v29, vcc
	global_load_dwordx2 v[20:21], v[18:19], off offset:-1536
	global_load_dwordx2 v[34:35], v[18:19], off offset:-1024
	global_load_dwordx2 v[36:37], v[18:19], off offset:-512
	s_nop 0
	global_load_dwordx2 v[18:19], v[18:19], off
	s_cselect_b64 s[4:5], -1, 0
	s_cmpk_gt_i32 s6, 0x3ff
	s_waitcnt vmcnt(3)
	v_lshlrev_b32_e32 v30, 16, v20
	v_and_b32_e32 v31, 0xffff0000, v20
	v_lshlrev_b32_e32 v32, 16, v21
	v_and_b32_e32 v33, 0xffff0000, v21
	s_waitcnt vmcnt(2)
	v_lshlrev_b32_e32 v38, 16, v34
	v_and_b32_e32 v39, 0xffff0000, v34
	v_lshlrev_b32_e32 v34, 16, v35
	v_and_b32_e32 v35, 0xffff0000, v35
	s_waitcnt vmcnt(1)
	v_lshlrev_b32_e32 v44, 16, v36
	v_and_b32_e32 v45, 0xffff0000, v36
	v_lshlrev_b32_e32 v40, 16, v37
	v_and_b32_e32 v41, 0xffff0000, v37
	s_waitcnt vmcnt(0)
	v_lshlrev_b32_e32 v36, 16, v18
	v_and_b32_e32 v37, 0xffff0000, v18
	v_lshlrev_b32_e32 v42, 16, v19
	v_and_b32_e32 v43, 0xffff0000, v19
	s_cbranch_scc1 .LBB0_891
	v_add_co_u32_e32 v76, vcc, 0xfec00000, v28
	v_lshl_add_u64 v[46:47], v[28:29], 0, s[14:15]
	s_nop 0
	v_addc_co_u32_e32 v77, vcc, -1, v29, vcc
	v_add_co_u32_e32 v74, vcc, s7, v28
	global_load_dwordx2 v[50:51], v[76:77], off offset:-1536
	s_nop 0
	v_addc_co_u32_e32 v75, vcc, -1, v29, vcc
	v_add_co_u32_e32 v78, vcc, s9, v28
	global_load_dwordx2 v[48:49], v[28:29], off offset:-1536
	s_nop 0
	v_addc_co_u32_e32 v79, vcc, -1, v29, vcc
	v_add_co_u32_e32 v66, vcc, s22, v28
	global_load_dwordx2 v[72:73], v[78:79], off offset:-1536
	global_load_dwordx2 v[52:53], v[74:75], off offset:-1536
	v_addc_co_u32_e32 v67, vcc, -1, v29, vcc
	v_add_co_u32_e32 v62, vcc, s23, v28
	global_load_dwordx2 v[70:71], v[66:67], off offset:-1536
	s_nop 0
	v_addc_co_u32_e32 v63, vcc, -1, v29, vcc
	v_add_co_u32_e32 v56, vcc, s30, v28
	global_load_dwordx2 v[68:69], v[62:63], off offset:-1536
	s_nop 0
	v_addc_co_u32_e32 v57, vcc, -1, v29, vcc
	v_add_co_u32_e32 v54, vcc, s31, v28
	global_load_dwordx2 v[64:65], v[56:57], off offset:-1536
	s_nop 0
	v_addc_co_u32_e32 v55, vcc, -1, v29, vcc
	global_load_dwordx2 v[58:59], v[54:55], off offset:-1536
	v_add_co_u32_e32 v84, vcc, s33, v28
	s_waitcnt vmcnt(7)
	v_lshlrev_b32_e32 v106, 16, v50
	v_addc_co_u32_e32 v85, vcc, -1, v29, vcc
	global_load_dwordx2 v[86:87], v[84:85], off offset:-1536
	global_load_dwordx4 v[18:21], v[26:27], off
	v_add_co_u32_e32 v80, vcc, s35, v28
	v_and_b32_e32 v107, 0xffff0000, v50
	s_nop 0
	v_addc_co_u32_e32 v81, vcc, -1, v29, vcc
	global_load_dwordx2 v[82:83], v[80:81], off offset:-1536
	global_load_dwordx2 v[60:61], v[76:77], off offset:-1024
	global_load_dwordx2 v[88:89], v[76:77], off offset:-512
	s_nop 0
	global_load_dwordx2 v[76:77], v[76:77], off
	v_add_co_u32_e32 v98, vcc, s36, v28
	v_lshlrev_b32_e32 v50, 16, v51
	s_nop 0
	v_addc_co_u32_e32 v99, vcc, -1, v29, vcc
	global_load_dwordx2 v[100:101], v[98:99], off offset:-1536
	global_load_dwordx2 v[102:103], v[74:75], off offset:-1024
	global_load_dwordx2 v[90:91], v[74:75], off offset:-512
	s_nop 0
	global_load_dwordx2 v[74:75], v[74:75], off
	s_nop 0
	global_load_dwordx2 v[104:105], v[78:79], off offset:-1024
	global_load_dwordx2 v[92:93], v[78:79], off offset:-512
	s_nop 0
	global_load_dwordx2 v[78:79], v[78:79], off
	v_and_b32_e32 v51, 0xffff0000, v51
	v_pk_add_f32 v[50:51], v[50:51], 0 op_sel_hi:[1,0]
	v_pk_add_f32 v[106:107], v[106:107], 0 op_sel_hi:[1,0]
	s_waitcnt vmcnt(17)
	v_lshlrev_b32_e32 v108, 16, v52
	v_and_b32_e32 v109, 0xffff0000, v52
	v_lshlrev_b32_e32 v52, 16, v53
	v_and_b32_e32 v53, 0xffff0000, v53
	v_pk_add_f32 v[106:107], v[106:107], v[108:109]
	v_pk_add_f32 v[50:51], v[50:51], v[52:53]
	v_lshlrev_b32_e32 v52, 16, v72
	v_and_b32_e32 v53, 0xffff0000, v72
	v_lshlrev_b32_e32 v72, 16, v73
	v_and_b32_e32 v73, 0xffff0000, v73
	v_pk_add_f32 v[108:109], v[50:51], v[72:73]
	v_pk_add_f32 v[52:53], v[106:107], v[52:53]
	global_load_dwordx2 v[106:107], v[66:67], off offset:-1024
	global_load_dwordx2 v[72:73], v[66:67], off offset:-512
	global_load_dwordx2 v[50:51], v[66:67], off
	s_waitcnt vmcnt(19)
	v_lshlrev_b32_e32 v66, 16, v70
	v_and_b32_e32 v67, 0xffff0000, v70
	v_lshlrev_b32_e32 v70, 16, v71
	v_and_b32_e32 v71, 0xffff0000, v71
	v_pk_add_f32 v[66:67], v[52:53], v[66:67]
	v_pk_add_f32 v[108:109], v[108:109], v[70:71]
	global_load_dwordx2 v[110:111], v[62:63], off offset:-1024
	global_load_dwordx2 v[70:71], v[62:63], off offset:-512
	global_load_dwordx2 v[52:53], v[62:63], off
	s_waitcnt vmcnt(21)
	v_lshlrev_b32_e32 v62, 16, v68
	v_and_b32_e32 v63, 0xffff0000, v68
	v_lshlrev_b32_e32 v68, 16, v69
	v_and_b32_e32 v69, 0xffff0000, v69
	v_pk_add_f32 v[108:109], v[108:109], v[68:69]
	v_pk_add_f32 v[62:63], v[66:67], v[62:63]
	s_waitcnt vmcnt(20)
	v_lshlrev_b32_e32 v66, 16, v64
	v_and_b32_e32 v67, 0xffff0000, v64
	v_lshlrev_b32_e32 v64, 16, v65
	v_and_b32_e32 v65, 0xffff0000, v65
	v_pk_add_f32 v[62:63], v[62:63], v[66:67]
	v_pk_add_f32 v[64:65], v[108:109], v[64:65]
	s_waitcnt vmcnt(19)
	v_lshlrev_b32_e32 v66, 16, v58
	v_and_b32_e32 v67, 0xffff0000, v58
	v_lshlrev_b32_e32 v58, 16, v59
	v_and_b32_e32 v59, 0xffff0000, v59
	global_load_dwordx2 v[112:113], v[56:57], off offset:-1024
	global_load_dwordx2 v[68:69], v[56:57], off offset:-512
	s_nop 0
	global_load_dwordx2 v[56:57], v[56:57], off
	s_nop 0
	global_load_dwordx2 v[108:109], v[54:55], off offset:-1024
	global_load_dwordx2 v[114:115], v[54:55], off offset:-512
	s_nop 0
	global_load_dwordx2 v[54:55], v[54:55], off
	v_pk_add_f32 v[64:65], v[64:65], v[58:59]
	v_pk_add_f32 v[62:63], v[62:63], v[66:67]
	global_load_dwordx2 v[116:117], v[84:85], off offset:-1024
	global_load_dwordx2 v[118:119], v[84:85], off offset:-512
	global_load_dwordx2 v[58:59], v[84:85], off
	v_lshlrev_b32_e32 v124, 16, v48
	v_and_b32_e32 v125, 0xffff0000, v48
	v_lshlrev_b32_e32 v48, 16, v49
	v_and_b32_e32 v49, 0xffff0000, v49
	s_waitcnt vmcnt(27)
	v_lshlrev_b32_e32 v66, 16, v86
	v_and_b32_e32 v67, 0xffff0000, v86
	v_lshlrev_b32_e32 v84, 16, v87
	v_and_b32_e32 v85, 0xffff0000, v87
	v_pk_add_f32 v[66:67], v[62:63], v[66:67]
	v_pk_add_f32 v[64:65], v[64:65], v[84:85]
	global_load_dwordx2 v[84:85], v[80:81], off offset:-1024
	global_load_dwordx2 v[86:87], v[80:81], off offset:-512
	global_load_dwordx2 v[62:63], v[80:81], off
	s_waitcnt vmcnt(28)
	v_lshlrev_b32_e32 v80, 16, v82
	v_and_b32_e32 v81, 0xffff0000, v82
	v_lshlrev_b32_e32 v82, 16, v83
	v_and_b32_e32 v83, 0xffff0000, v83
	v_pk_add_f32 v[82:83], v[64:65], v[82:83]
	v_pk_add_f32 v[66:67], v[66:67], v[80:81]
	global_load_dwordx2 v[80:81], v[98:99], off offset:-1024
	global_load_dwordx2 v[120:121], v[98:99], off offset:-512
	global_load_dwordx2 v[64:65], v[98:99], off
	s_waitcnt vmcnt(27)
	v_lshlrev_b32_e32 v98, 16, v100
	v_and_b32_e32 v99, 0xffff0000, v100
	v_lshlrev_b32_e32 v100, 16, v101
	v_and_b32_e32 v101, 0xffff0000, v101
	v_pk_add_f32 v[98:99], v[66:67], v[98:99]
	v_pk_add_f32 v[82:83], v[82:83], v[100:101]
	global_load_dwordx2 v[100:101], v[28:29], off offset:-1024
	global_load_dwordx2 v[122:123], v[28:29], off offset:-512
	global_load_dwordx2 v[66:67], v[28:29], off
	v_pk_add_f32 v[48:49], v[82:83], v[48:49]
	v_pk_add_f32 v[82:83], v[98:99], v[124:125]
	v_pk_fma_f32 v[32:33], v[48:49], v[20:21], v[32:33]
	v_pk_fma_f32 v[18:19], v[82:83], v[18:19], v[30:31]
	v_lshlrev_b32_e32 v48, 16, v60
	v_bfe_u32 v20, v18, 16, 1
	v_add3_u32 v30, v18, v20, s37
	v_bfe_u32 v18, v19, 16, 1
	v_and_b32_sdwa v20, v33, v97 dst_sel:DWORD dst_unused:UNUSED_PAD src0_sel:WORD_1 src1_sel:DWORD
	v_add3_u32 v18, v19, v18, s37
	v_bfe_u32 v19, v32, 16, 1
	v_add3_u32 v20, v33, v20, s37
	v_and_b32_e32 v31, 0xffff0000, v18
	v_add3_u32 v19, v32, v19, s37
	v_and_b32_e32 v33, 0xffff0000, v20
	v_or_b32_sdwa v18, v31, v30 dst_sel:DWORD dst_unused:UNUSED_PAD src0_sel:DWORD src1_sel:WORD_1
	v_or_b32_sdwa v19, v33, v19 dst_sel:DWORD dst_unused:UNUSED_PAD src0_sel:DWORD src1_sel:WORD_1
	global_store_dwordx2 v[46:47], v[18:19], off
	global_load_dwordx4 v[18:21], v[26:27], off offset:1024
	v_and_b32_e32 v49, 0xffff0000, v60
	v_lshlrev_b32_e32 v60, 16, v61
	v_and_b32_e32 v61, 0xffff0000, v61
	v_pk_add_f32 v[48:49], v[48:49], 0 op_sel_hi:[1,0]
	v_pk_add_f32 v[60:61], v[60:61], 0 op_sel_hi:[1,0]
	s_waitcnt vmcnt(31)
	v_lshlrev_b32_e32 v82, 16, v102
	v_and_b32_e32 v83, 0xffff0000, v102
	v_lshlrev_b32_e32 v98, 16, v103
	v_and_b32_e32 v99, 0xffff0000, v103
	v_pk_add_f32 v[60:61], v[60:61], v[98:99]
	v_pk_add_f32 v[48:49], v[48:49], v[82:83]
	s_waitcnt vmcnt(28)
	v_lshlrev_b32_e32 v82, 16, v104
	v_and_b32_e32 v83, 0xffff0000, v104
	v_lshlrev_b32_e32 v98, 16, v105
	v_and_b32_e32 v99, 0xffff0000, v105
	v_pk_add_f32 v[48:49], v[48:49], v[82:83]
	v_pk_add_f32 v[60:61], v[60:61], v[98:99]
	s_waitcnt vmcnt(25)
	v_lshlrev_b32_e32 v82, 16, v106
	v_and_b32_e32 v83, 0xffff0000, v106
	v_lshlrev_b32_e32 v98, 16, v107
	v_and_b32_e32 v99, 0xffff0000, v107
	v_pk_add_f32 v[60:61], v[60:61], v[98:99]
	v_pk_add_f32 v[48:49], v[48:49], v[82:83]
	s_waitcnt vmcnt(22)
	v_lshlrev_b32_e32 v82, 16, v110
	v_and_b32_e32 v83, 0xffff0000, v110
	v_lshlrev_b32_e32 v98, 16, v111
	v_and_b32_e32 v99, 0xffff0000, v111
	v_pk_add_f32 v[48:49], v[48:49], v[82:83]
	v_pk_add_f32 v[60:61], v[60:61], v[98:99]
	s_waitcnt vmcnt(19)
	v_lshlrev_b32_e32 v82, 16, v112
	v_and_b32_e32 v83, 0xffff0000, v112
	v_lshlrev_b32_e32 v98, 16, v113
	v_and_b32_e32 v99, 0xffff0000, v113
	v_pk_add_f32 v[60:61], v[60:61], v[98:99]
	v_pk_add_f32 v[48:49], v[48:49], v[82:83]
	s_waitcnt vmcnt(16)
	v_lshlrev_b32_e32 v82, 16, v108
	v_and_b32_e32 v83, 0xffff0000, v108
	v_lshlrev_b32_e32 v98, 16, v109
	v_and_b32_e32 v99, 0xffff0000, v109
	v_pk_add_f32 v[48:49], v[48:49], v[82:83]
	v_pk_add_f32 v[60:61], v[60:61], v[98:99]
	s_waitcnt vmcnt(13)
	v_lshlrev_b32_e32 v82, 16, v116
	v_and_b32_e32 v83, 0xffff0000, v116
	v_lshlrev_b32_e32 v98, 16, v117
	v_and_b32_e32 v99, 0xffff0000, v117
	v_pk_add_f32 v[60:61], v[60:61], v[98:99]
	v_pk_add_f32 v[48:49], v[48:49], v[82:83]
	s_waitcnt vmcnt(10)
	v_lshlrev_b32_e32 v82, 16, v84
	v_and_b32_e32 v83, 0xffff0000, v84
	v_lshlrev_b32_e32 v84, 16, v85
	v_and_b32_e32 v85, 0xffff0000, v85
	v_pk_add_f32 v[48:49], v[48:49], v[82:83]
	v_pk_add_f32 v[60:61], v[60:61], v[84:85]
	s_waitcnt vmcnt(7)
	v_lshlrev_b32_e32 v82, 16, v80
	v_and_b32_e32 v83, 0xffff0000, v80
	v_lshlrev_b32_e32 v80, 16, v81
	v_and_b32_e32 v81, 0xffff0000, v81
	v_pk_add_f32 v[60:61], v[60:61], v[80:81]
	v_pk_add_f32 v[48:49], v[48:49], v[82:83]
	s_waitcnt vmcnt(4)
	v_lshlrev_b32_e32 v80, 16, v100
	v_and_b32_e32 v81, 0xffff0000, v100
	v_pk_add_f32 v[48:49], v[48:49], v[80:81]
	v_lshlrev_b32_e32 v82, 16, v101
	v_and_b32_e32 v83, 0xffff0000, v101
	v_pk_add_f32 v[60:61], v[60:61], v[82:83]
	v_lshl_add_u64 v[46:47], v[28:29], 0, s[16:17]
	v_lshlrev_b32_e32 v80, 16, v89
	v_and_b32_e32 v81, 0xffff0000, v89
	v_pk_add_f32 v[80:81], v[80:81], 0 op_sel_hi:[1,0]
	v_lshlrev_b32_e32 v82, 16, v90
	v_and_b32_e32 v83, 0xffff0000, v90
	v_lshlrev_b32_e32 v84, 16, v91
	v_and_b32_e32 v85, 0xffff0000, v91
	v_pk_add_f32 v[80:81], v[80:81], v[84:85]
	v_lshlrev_b32_e32 v84, 16, v93
	v_and_b32_e32 v85, 0xffff0000, v93
	v_pk_add_f32 v[80:81], v[80:81], v[84:85]
	v_and_b32_e32 v30, 0xffff0000, v30
	s_waitcnt vmcnt(0)
	v_pk_fma_f32 v[38:39], v[48:49], v[18:19], v[38:39]
	s_nop 0
	v_pk_fma_f32 v[34:35], v[60:61], v[20:21], v[34:35]
	v_and_b32_sdwa v20, v35, v97 dst_sel:DWORD dst_unused:UNUSED_PAD src0_sel:WORD_1 src1_sel:DWORD
	v_cvt_pk_bf16_f32 v18, v38, v39
	v_bfe_u32 v19, v34, 16, 1
	v_add3_u32 v20, v35, v20, s37
	v_add3_u32 v19, v34, v19, s37
	v_and_b32_e32 v35, 0xffff0000, v20
	v_or_b32_sdwa v19, v35, v19 dst_sel:DWORD dst_unused:UNUSED_PAD src0_sel:DWORD src1_sel:WORD_1
	global_store_dwordx2 v[46:47], v[18:19], off
	global_load_dwordx4 v[18:21], v[26:27], off offset:2048
	v_and_b32_sdwa v60, v32, v97 dst_sel:DWORD dst_unused:UNUSED_PAD src0_sel:WORD_1 src1_sel:DWORD
	v_add3_u32 v32, v32, v60, s37
	v_and_b32_sdwa v60, v39, v97 dst_sel:DWORD dst_unused:UNUSED_PAD src0_sel:WORD_1 src1_sel:DWORD
	v_and_b32_sdwa v61, v38, v97 dst_sel:DWORD dst_unused:UNUSED_PAD src0_sel:WORD_1 src1_sel:DWORD
	v_add3_u32 v39, v39, v60, s37
	v_add3_u32 v38, v38, v61, s37
	v_lshlrev_b32_e32 v60, 16, v88
	v_and_b32_e32 v61, 0xffff0000, v88
	v_pk_add_f32 v[60:61], v[60:61], 0 op_sel_hi:[1,0]
	v_lshl_add_u64 v[46:47], v[28:29], 0, s[18:19]
	v_pk_add_f32 v[60:61], v[60:61], v[82:83]
	v_lshlrev_b32_e32 v82, 16, v92
	v_and_b32_e32 v83, 0xffff0000, v92
	v_pk_add_f32 v[60:61], v[60:61], v[82:83]
	v_lshlrev_b32_e32 v82, 16, v72
	v_and_b32_e32 v83, 0xffff0000, v72
	v_lshlrev_b32_e32 v72, 16, v73
	v_and_b32_e32 v73, 0xffff0000, v73
	v_pk_add_f32 v[72:73], v[80:81], v[72:73]
	v_pk_add_f32 v[60:61], v[60:61], v[82:83]
	v_lshlrev_b32_e32 v80, 16, v70
	v_and_b32_e32 v81, 0xffff0000, v70
	v_lshlrev_b32_e32 v70, 16, v71
	v_and_b32_e32 v71, 0xffff0000, v71
	v_pk_add_f32 v[60:61], v[60:61], v[80:81]
	v_pk_add_f32 v[70:71], v[72:73], v[70:71]
	v_lshlrev_b32_e32 v72, 16, v68
	v_and_b32_e32 v73, 0xffff0000, v68
	v_lshlrev_b32_e32 v68, 16, v69
	v_and_b32_e32 v69, 0xffff0000, v69
	v_pk_add_f32 v[68:69], v[70:71], v[68:69]
	v_pk_add_f32 v[60:61], v[60:61], v[72:73]
	v_lshlrev_b32_e32 v70, 16, v114
	v_and_b32_e32 v71, 0xffff0000, v114
	v_pk_add_f32 v[60:61], v[60:61], v[70:71]
	v_lshlrev_b32_e32 v70, 16, v118
	v_and_b32_e32 v71, 0xffff0000, v118
	v_lshlrev_b32_e32 v72, 16, v115
	v_and_b32_e32 v73, 0xffff0000, v115
	v_pk_add_f32 v[60:61], v[60:61], v[70:71]
	v_lshlrev_b32_e32 v70, 16, v86
	v_and_b32_e32 v71, 0xffff0000, v86
	v_pk_add_f32 v[68:69], v[68:69], v[72:73]
	v_lshlrev_b32_e32 v72, 16, v119
	v_and_b32_e32 v73, 0xffff0000, v119
	v_pk_add_f32 v[60:61], v[60:61], v[70:71]
	v_lshlrev_b32_e32 v70, 16, v120
	v_and_b32_e32 v71, 0xffff0000, v120
	v_pk_add_f32 v[68:69], v[68:69], v[72:73]
	v_lshlrev_b32_e32 v72, 16, v87
	v_and_b32_e32 v73, 0xffff0000, v87
	v_pk_add_f32 v[60:61], v[60:61], v[70:71]
	v_lshlrev_b32_e32 v70, 16, v122
	v_and_b32_e32 v71, 0xffff0000, v122
	v_pk_add_f32 v[68:69], v[68:69], v[72:73]
	v_lshlrev_b32_e32 v72, 16, v121
	v_and_b32_e32 v73, 0xffff0000, v121
	v_pk_add_f32 v[60:61], v[60:61], v[70:71]
	v_pk_add_f32 v[68:69], v[68:69], v[72:73]
	v_lshlrev_b32_e32 v72, 16, v123
	v_and_b32_e32 v73, 0xffff0000, v123
	v_pk_add_f32 v[68:69], v[68:69], v[72:73]
	v_lshlrev_b32_e32 v70, 16, v75
	v_and_b32_e32 v71, 0xffff0000, v75
	v_lshl_add_u64 v[48:49], v[28:29], 0, s[20:21]
	v_and_b32_e32 v32, 0xffff0000, v32
	v_and_b32_e32 v39, 0xffff0000, v39
	v_and_b32_e32 v38, 0xffff0000, v38
	s_waitcnt vmcnt(0)
	v_pk_fma_f32 v[44:45], v[60:61], v[18:19], v[44:45]
	s_nop 0
	v_pk_fma_f32 v[40:41], v[68:69], v[20:21], v[40:41]
	v_and_b32_sdwa v20, v41, v97 dst_sel:DWORD dst_unused:UNUSED_PAD src0_sel:WORD_1 src1_sel:DWORD
	v_cvt_pk_bf16_f32 v18, v44, v45
	v_bfe_u32 v19, v40, 16, 1
	v_add3_u32 v20, v41, v20, s37
	v_add3_u32 v19, v40, v19, s37
	v_and_b32_e32 v41, 0xffff0000, v20
	v_or_b32_sdwa v19, v41, v19 dst_sel:DWORD dst_unused:UNUSED_PAD src0_sel:DWORD src1_sel:WORD_1
	global_store_dwordx2 v[46:47], v[18:19], off
	global_load_dwordx4 v[18:21], v[26:27], off offset:3072
	v_and_b32_sdwa v46, v34, v97 dst_sel:DWORD dst_unused:UNUSED_PAD src0_sel:WORD_1 src1_sel:DWORD
	v_add3_u32 v34, v34, v46, s37
	v_and_b32_sdwa v46, v45, v97 dst_sel:DWORD dst_unused:UNUSED_PAD src0_sel:WORD_1 src1_sel:DWORD
	v_and_b32_sdwa v47, v44, v97 dst_sel:DWORD dst_unused:UNUSED_PAD src0_sel:WORD_1 src1_sel:DWORD
	v_add3_u32 v45, v45, v46, s37
	v_add3_u32 v44, v44, v47, s37
	v_lshlrev_b32_e32 v46, 16, v76
	v_and_b32_e32 v47, 0xffff0000, v76
	v_lshlrev_b32_e32 v60, 16, v77
	v_and_b32_e32 v61, 0xffff0000, v77
	v_pk_add_f32 v[46:47], v[46:47], 0 op_sel_hi:[1,0]
	v_pk_add_f32 v[60:61], v[60:61], 0 op_sel_hi:[1,0]
	v_lshlrev_b32_e32 v68, 16, v74
	v_and_b32_e32 v69, 0xffff0000, v74
	v_pk_add_f32 v[60:61], v[60:61], v[70:71]
	v_pk_add_f32 v[46:47], v[46:47], v[68:69]
	v_lshlrev_b32_e32 v68, 16, v78
	v_and_b32_e32 v69, 0xffff0000, v78
	v_lshlrev_b32_e32 v70, 16, v79
	v_and_b32_e32 v71, 0xffff0000, v79
	v_pk_add_f32 v[46:47], v[46:47], v[68:69]
	v_pk_add_f32 v[60:61], v[60:61], v[70:71]
	v_lshlrev_b32_e32 v68, 16, v50
	v_and_b32_e32 v69, 0xffff0000, v50
	v_lshlrev_b32_e32 v50, 16, v51
	v_and_b32_e32 v51, 0xffff0000, v51
	v_pk_add_f32 v[50:51], v[60:61], v[50:51]
	v_pk_add_f32 v[46:47], v[46:47], v[68:69]
	v_lshlrev_b32_e32 v60, 16, v52
	v_and_b32_e32 v61, 0xffff0000, v52
	v_lshlrev_b32_e32 v52, 16, v53
	v_and_b32_e32 v53, 0xffff0000, v53
	v_pk_add_f32 v[46:47], v[46:47], v[60:61]
	v_pk_add_f32 v[50:51], v[50:51], v[52:53]
	v_lshlrev_b32_e32 v52, 16, v56
	v_and_b32_e32 v53, 0xffff0000, v56
	v_pk_add_f32 v[46:47], v[46:47], v[52:53]
	v_lshlrev_b32_e32 v52, 16, v54
	v_and_b32_e32 v53, 0xffff0000, v54
	v_pk_add_f32 v[46:47], v[46:47], v[52:53]
	v_lshlrev_b32_e32 v52, 16, v58
	v_and_b32_e32 v53, 0xffff0000, v58
	v_lshlrev_b32_e32 v56, 16, v57
	v_and_b32_e32 v57, 0xffff0000, v57
	v_pk_add_f32 v[46:47], v[46:47], v[52:53]
	v_lshlrev_b32_e32 v52, 16, v62
	v_and_b32_e32 v53, 0xffff0000, v62
	v_pk_add_f32 v[50:51], v[50:51], v[56:57]
	v_lshlrev_b32_e32 v54, 16, v55
	v_and_b32_e32 v55, 0xffff0000, v55
	v_pk_add_f32 v[46:47], v[46:47], v[52:53]
	v_lshlrev_b32_e32 v52, 16, v64
	v_and_b32_e32 v53, 0xffff0000, v64
	v_pk_add_f32 v[50:51], v[50:51], v[54:55]
	v_lshlrev_b32_e32 v54, 16, v59
	v_and_b32_e32 v55, 0xffff0000, v59
	v_pk_add_f32 v[46:47], v[46:47], v[52:53]
	v_lshlrev_b32_e32 v52, 16, v66
	v_and_b32_e32 v53, 0xffff0000, v66
	v_pk_add_f32 v[50:51], v[50:51], v[54:55]
	v_lshlrev_b32_e32 v54, 16, v63
	v_and_b32_e32 v55, 0xffff0000, v63
	v_pk_add_f32 v[46:47], v[46:47], v[52:53]
	v_pk_add_f32 v[50:51], v[50:51], v[54:55]
	v_lshlrev_b32_e32 v54, 16, v65
	v_and_b32_e32 v55, 0xffff0000, v65
	v_pk_add_f32 v[50:51], v[50:51], v[54:55]
	v_lshlrev_b32_e32 v54, 16, v67
	v_and_b32_e32 v55, 0xffff0000, v67
	v_pk_add_f32 v[50:51], v[50:51], v[54:55]
	v_and_b32_sdwa v52, v40, v97 dst_sel:DWORD dst_unused:UNUSED_PAD src0_sel:WORD_1 src1_sel:DWORD
	v_add3_u32 v40, v40, v52, s37
	v_and_b32_e32 v34, 0xffff0000, v34
	v_and_b32_e32 v45, 0xffff0000, v45
	v_and_b32_e32 v44, 0xffff0000, v44
	v_and_b32_e32 v40, 0xffff0000, v40
	s_waitcnt vmcnt(0)
	v_pk_fma_f32 v[18:19], v[46:47], v[18:19], v[36:37]
	s_nop 0
	v_pk_fma_f32 v[20:21], v[50:51], v[20:21], v[42:43]
	v_cvt_pk_bf16_f32 v46, v18, v19
	v_bfe_u32 v36, v20, 16, 1
	v_and_b32_sdwa v37, v18, v97 dst_sel:DWORD dst_unused:UNUSED_PAD src0_sel:WORD_1 src1_sel:DWORD
	v_add3_u32 v47, v20, v36, s37
	v_and_b32_sdwa v36, v19, v97 dst_sel:DWORD dst_unused:UNUSED_PAD src0_sel:WORD_1 src1_sel:DWORD
	v_add3_u32 v18, v18, v37, s37
	v_add3_u32 v19, v19, v36, s37
	v_and_b32_e32 v36, 0xffff0000, v18
	v_and_b32_sdwa v18, v21, v97 dst_sel:DWORD dst_unused:UNUSED_PAD src0_sel:WORD_1 src1_sel:DWORD
	v_and_b32_e32 v37, 0xffff0000, v19
	v_and_b32_sdwa v19, v20, v97 dst_sel:DWORD dst_unused:UNUSED_PAD src0_sel:WORD_1 src1_sel:DWORD
	v_add3_u32 v18, v21, v18, s37
	v_add3_u32 v19, v20, v19, s37
	v_and_b32_e32 v43, 0xffff0000, v18
	v_and_b32_e32 v42, 0xffff0000, v19
	v_or_b32_sdwa v47, v43, v47 dst_sel:DWORD dst_unused:UNUSED_PAD src0_sel:DWORD src1_sel:WORD_1
	global_store_dwordx2 v[48:49], v[46:47], off
	s_branch .LBB0_891

.LBB0_1337:
	v_add_co_u32_e32 v18, vcc, 0xdda00000, v52
	s_cmpk_lt_i32 s42, 0x400
	s_nop 0
	v_addc_co_u32_e32 v19, vcc, -1, v53, vcc
	s_waitcnt lgkmcnt(5)
	global_load_dwordx2 v[22:23], v[18:19], off offset:-1536
	s_waitcnt lgkmcnt(4)
	global_load_dwordx2 v[24:25], v[18:19], off offset:-1024
	s_waitcnt lgkmcnt(3)
	global_load_dwordx2 v[26:27], v[18:19], off offset:-512
	s_waitcnt lgkmcnt(2)
	global_load_dwordx2 v[28:29], v[18:19], off
	s_cselect_b64 s[8:9], -1, 0
	s_cmpk_gt_i32 s42, 0x3ff
	s_waitcnt vmcnt(3)
	v_lshlrev_b32_e32 v20, 16, v22
	v_and_b32_e32 v21, 0xffff0000, v22
	v_lshlrev_b32_e32 v22, 16, v23
	v_and_b32_e32 v23, 0xffff0000, v23
	s_waitcnt vmcnt(2)
	v_lshlrev_b32_e32 v56, 16, v24
	s_waitcnt lgkmcnt(0)
	v_and_b32_e32 v57, 0xffff0000, v24
	v_lshlrev_b32_e32 v24, 16, v25
	v_and_b32_e32 v25, 0xffff0000, v25
	s_waitcnt vmcnt(1)
	v_lshlrev_b32_e32 v54, 16, v26
	v_and_b32_e32 v55, 0xffff0000, v26
	v_lshlrev_b32_e32 v26, 16, v27
	v_and_b32_e32 v27, 0xffff0000, v27
	s_waitcnt vmcnt(0)
	v_lshlrev_b32_e32 v18, 16, v28
	v_and_b32_e32 v19, 0xffff0000, v28
	v_lshlrev_b32_e32 v28, 16, v29
	v_and_b32_e32 v29, 0xffff0000, v29
	s_cbranch_scc1 .LBB0_1339
	v_add_co_u32_e32 v58, vcc, 0xffa00000, v52
	global_load_dwordx2 v[64:65], v[52:53], off offset:-1536
	s_nop 0
	v_addc_co_u32_e32 v59, vcc, -1, v53, vcc
	v_add_co_u32_e32 v68, vcc, s33, v52
	global_load_dwordx2 v[66:67], v[58:59], off offset:-1536
	s_nop 0
	v_addc_co_u32_e32 v69, vcc, -1, v53, vcc
	global_load_dwordx2 v[76:77], v[68:69], off offset:-1536
	v_add_co_u32_e32 v78, vcc, s36, v52
	v_lshl_add_u64 v[82:83], v[52:53], 0, s[52:53]
	s_nop 0
	v_addc_co_u32_e32 v79, vcc, -1, v53, vcc
	global_load_dwordx2 v[80:81], v[78:79], off offset:-1536
	global_load_dwordx4 v[60:63], v[50:51], off
	global_load_dwordx2 v[84:85], v[52:53], off offset:-1024
	global_load_dwordx2 v[86:87], v[52:53], off offset:-512
	global_load_dwordx2 v[88:89], v[52:53], off
	global_load_dwordx2 v[90:91], v[58:59], off offset:-1024
	global_load_dwordx2 v[92:93], v[58:59], off offset:-512
	global_load_dwordx2 v[94:95], v[58:59], off
	global_load_dwordx2 v[96:97], v[68:69], off offset:-1024
	global_load_dwordx2 v[98:99], v[68:69], off offset:-512
	s_nop 0
	global_load_dwordx2 v[68:69], v[68:69], off
	s_nop 0
	global_load_dwordx2 v[100:101], v[78:79], off offset:-1024
	global_load_dwordx2 v[102:103], v[78:79], off offset:-512
	s_nop 0
	global_load_dwordx2 v[78:79], v[78:79], off
	s_waitcnt vmcnt(16)
	v_lshlrev_b32_e32 v58, 16, v64
	v_and_b32_e32 v59, 0xffff0000, v64
	v_lshlrev_b32_e32 v64, 16, v65
	v_and_b32_e32 v65, 0xffff0000, v65
	s_waitcnt vmcnt(15)
	v_lshlrev_b32_e32 v104, 16, v66
	v_and_b32_e32 v105, 0xffff0000, v66
	v_lshlrev_b32_e32 v66, 16, v67
	v_and_b32_e32 v67, 0xffff0000, v67
	v_pk_add_f32 v[104:105], v[104:105], 0 op_sel_hi:[1,0]
	v_pk_add_f32 v[66:67], v[66:67], 0 op_sel_hi:[1,0]
	s_waitcnt vmcnt(14)
	v_lshlrev_b32_e32 v106, 16, v76
	v_and_b32_e32 v107, 0xffff0000, v76
	v_lshlrev_b32_e32 v76, 16, v77
	v_and_b32_e32 v77, 0xffff0000, v77
	v_pk_add_f32 v[66:67], v[66:67], v[76:77]
	v_pk_add_f32 v[76:77], v[104:105], v[106:107]
	s_waitcnt vmcnt(13)
	v_lshlrev_b32_e32 v104, 16, v80
	v_and_b32_e32 v105, 0xffff0000, v80
	v_lshlrev_b32_e32 v80, 16, v81
	v_and_b32_e32 v81, 0xffff0000, v81
	v_pk_add_f32 v[76:77], v[76:77], v[104:105]
	v_pk_add_f32 v[66:67], v[66:67], v[80:81]
	v_pk_add_f32 v[58:59], v[76:77], v[58:59]
	v_pk_add_f32 v[64:65], v[66:67], v[64:65]
	s_waitcnt vmcnt(12)
	v_pk_fma_f32 v[20:21], v[58:59], v[60:61], v[20:21]
	v_pk_fma_f32 v[22:23], v[64:65], v[62:63], v[22:23]
	v_bfe_u32 v59, v21, 16, 1
	v_and_b32_sdwa v61, v23, v74 dst_sel:DWORD dst_unused:UNUSED_PAD src0_sel:WORD_1 src1_sel:DWORD
	v_bfe_u32 v58, v20, 16, 1
	v_bfe_u32 v60, v22, 16, 1
	v_add3_u32 v21, v21, v59, s37
	v_add3_u32 v23, v23, v61, s37
	v_add3_u32 v20, v20, v58, s37
	v_add3_u32 v59, v22, v60, s37
	v_and_b32_e32 v21, 0xffff0000, v21
	v_and_b32_e32 v23, 0xffff0000, v23
	v_or_b32_sdwa v58, v21, v20 dst_sel:DWORD dst_unused:UNUSED_PAD src0_sel:DWORD src1_sel:WORD_1
	v_or_b32_sdwa v59, v23, v59 dst_sel:DWORD dst_unused:UNUSED_PAD src0_sel:DWORD src1_sel:WORD_1
	global_store_dwordx2 v[82:83], v[58:59], off
	global_load_dwordx4 v[58:61], v[50:51], off offset:1024
	s_waitcnt vmcnt(10)
	v_lshlrev_b32_e32 v76, 16, v90
	v_and_b32_e32 v77, 0xffff0000, v90
	v_lshlrev_b32_e32 v80, 16, v91
	v_and_b32_e32 v81, 0xffff0000, v91
	v_lshlrev_b32_e32 v64, 16, v84
	v_and_b32_e32 v65, 0xffff0000, v84
	v_lshlrev_b32_e32 v66, 16, v85
	v_and_b32_e32 v67, 0xffff0000, v85
	v_pk_add_f32 v[80:81], v[80:81], 0 op_sel_hi:[1,0]
	v_pk_add_f32 v[76:77], v[76:77], 0 op_sel_hi:[1,0]
	s_waitcnt vmcnt(7)
	v_lshlrev_b32_e32 v82, 16, v96
	v_and_b32_e32 v83, 0xffff0000, v96
	v_lshlrev_b32_e32 v84, 16, v97
	v_and_b32_e32 v85, 0xffff0000, v97
	v_pk_add_f32 v[76:77], v[76:77], v[82:83]
	v_pk_add_f32 v[80:81], v[80:81], v[84:85]
	s_waitcnt vmcnt(4)
	v_lshlrev_b32_e32 v82, 16, v100
	v_and_b32_e32 v83, 0xffff0000, v100
	v_lshlrev_b32_e32 v84, 16, v101
	v_and_b32_e32 v85, 0xffff0000, v101
	v_pk_add_f32 v[80:81], v[80:81], v[84:85]
	v_pk_add_f32 v[76:77], v[76:77], v[82:83]
	v_pk_add_f32 v[66:67], v[80:81], v[66:67]
	v_pk_add_f32 v[64:65], v[76:77], v[64:65]
	v_lshl_add_u64 v[62:63], v[52:53], 0, s[54:55]
	v_lshlrev_b32_e32 v76, 16, v92
	v_and_b32_e32 v77, 0xffff0000, v92
	v_lshlrev_b32_e32 v80, 16, v93
	v_and_b32_e32 v81, 0xffff0000, v93
	v_pk_add_f32 v[80:81], v[80:81], 0 op_sel_hi:[1,0]
	v_pk_add_f32 v[76:77], v[76:77], 0 op_sel_hi:[1,0]
	v_lshlrev_b32_e32 v82, 16, v98
	v_and_b32_e32 v83, 0xffff0000, v98
	v_lshlrev_b32_e32 v84, 16, v99
	v_and_b32_e32 v85, 0xffff0000, v99
	v_pk_add_f32 v[76:77], v[76:77], v[82:83]
	v_pk_add_f32 v[80:81], v[80:81], v[84:85]
	s_waitcnt vmcnt(3)
	v_lshlrev_b32_e32 v82, 16, v102
	v_and_b32_e32 v83, 0xffff0000, v102
	v_lshlrev_b32_e32 v84, 16, v103
	v_and_b32_e32 v85, 0xffff0000, v103
	v_pk_add_f32 v[80:81], v[80:81], v[84:85]
	v_pk_add_f32 v[76:77], v[76:77], v[82:83]
	v_lshlrev_b32_e32 v82, 16, v68
	v_and_b32_e32 v83, 0xffff0000, v68
	v_lshlrev_b32_e32 v68, 16, v69
	v_and_b32_e32 v69, 0xffff0000, v69
	v_and_b32_e32 v20, 0xffff0000, v20
	s_waitcnt vmcnt(0)
	v_pk_fma_f32 v[24:25], v[66:67], v[60:61], v[24:25]
	v_pk_fma_f32 v[64:65], v[64:65], v[58:59], v[56:57]
	v_and_b32_sdwa v59, v25, v74 dst_sel:DWORD dst_unused:UNUSED_PAD src0_sel:WORD_1 src1_sel:DWORD
	v_bfe_u32 v58, v24, 16, 1
	v_add3_u32 v25, v25, v59, s37
	v_add3_u32 v58, v24, v58, s37
	v_and_b32_e32 v25, 0xffff0000, v25
	v_cvt_pk_bf16_f32 v56, v64, v65
	v_or_b32_sdwa v57, v25, v58 dst_sel:DWORD dst_unused:UNUSED_PAD src0_sel:DWORD src1_sel:WORD_1
	global_store_dwordx2 v[62:63], v[56:57], off
	global_load_dwordx4 v[56:59], v[50:51], off offset:2048
	v_lshlrev_b32_e32 v62, 16, v86
	v_and_b32_e32 v63, 0xffff0000, v86
	v_lshlrev_b32_e32 v66, 16, v87
	v_and_b32_e32 v67, 0xffff0000, v87
	v_pk_add_f32 v[62:63], v[76:77], v[62:63]
	v_pk_add_f32 v[66:67], v[80:81], v[66:67]
	v_lshl_add_u64 v[60:61], v[52:53], 0, s[56:57]
	v_lshlrev_b32_e32 v76, 16, v94
	v_and_b32_e32 v77, 0xffff0000, v94
	v_lshlrev_b32_e32 v80, 16, v95
	v_and_b32_e32 v81, 0xffff0000, v95
	v_pk_add_f32 v[80:81], v[80:81], 0 op_sel_hi:[1,0]
	v_pk_add_f32 v[76:77], v[76:77], 0 op_sel_hi:[1,0]
	v_pk_add_f32 v[68:69], v[80:81], v[68:69]
	v_pk_add_f32 v[76:77], v[76:77], v[82:83]
	v_lshlrev_b32_e32 v80, 16, v78
	v_and_b32_e32 v81, 0xffff0000, v78
	v_lshlrev_b32_e32 v78, 16, v79
	v_and_b32_e32 v79, 0xffff0000, v79
	v_pk_add_f32 v[76:77], v[76:77], v[80:81]
	v_pk_add_f32 v[68:69], v[68:69], v[78:79]
	s_waitcnt vmcnt(0)
	v_pk_fma_f32 v[26:27], v[66:67], v[58:59], v[26:27]
	v_pk_fma_f32 v[54:55], v[62:63], v[56:57], v[54:55]
	v_and_b32_sdwa v59, v27, v74 dst_sel:DWORD dst_unused:UNUSED_PAD src0_sel:WORD_1 src1_sel:DWORD
	v_bfe_u32 v58, v26, 16, 1
	v_add3_u32 v27, v27, v59, s37
	v_add3_u32 v58, v26, v58, s37
	v_and_b32_e32 v27, 0xffff0000, v27
	v_cvt_pk_bf16_f32 v56, v54, v55
	v_or_b32_sdwa v57, v27, v58 dst_sel:DWORD dst_unused:UNUSED_PAD src0_sel:DWORD src1_sel:WORD_1
	global_store_dwordx2 v[60:61], v[56:57], off
	global_load_dwordx4 v[58:61], v[50:51], off offset:3072
	v_lshlrev_b32_e32 v56, 16, v88
	v_and_b32_e32 v57, 0xffff0000, v88
	v_lshlrev_b32_e32 v66, 16, v89
	v_and_b32_e32 v67, 0xffff0000, v89
	v_pk_add_f32 v[76:77], v[76:77], v[56:57]
	v_and_b32_sdwa v56, v22, v74 dst_sel:DWORD dst_unused:UNUSED_PAD src0_sel:WORD_1 src1_sel:DWORD
	v_pk_add_f32 v[66:67], v[68:69], v[66:67]
	v_add3_u32 v22, v22, v56, s37
	v_and_b32_sdwa v56, v65, v74 dst_sel:DWORD dst_unused:UNUSED_PAD src0_sel:WORD_1 src1_sel:DWORD
	v_and_b32_sdwa v57, v64, v74 dst_sel:DWORD dst_unused:UNUSED_PAD src0_sel:WORD_1 src1_sel:DWORD
	v_add3_u32 v56, v65, v56, s37
	v_add3_u32 v64, v64, v57, s37
	v_and_b32_sdwa v65, v54, v74 dst_sel:DWORD dst_unused:UNUSED_PAD src0_sel:WORD_1 src1_sel:DWORD
	v_and_b32_sdwa v68, v24, v74 dst_sel:DWORD dst_unused:UNUSED_PAD src0_sel:WORD_1 src1_sel:DWORD
	v_and_b32_e32 v57, 0xffff0000, v56
	v_and_b32_e32 v56, 0xffff0000, v64
	v_and_b32_sdwa v64, v55, v74 dst_sel:DWORD dst_unused:UNUSED_PAD src0_sel:WORD_1 src1_sel:DWORD
	v_add3_u32 v54, v54, v65, s37
	v_add3_u32 v24, v24, v68, s37
	v_and_b32_sdwa v68, v26, v74 dst_sel:DWORD dst_unused:UNUSED_PAD src0_sel:WORD_1 src1_sel:DWORD
	v_add3_u32 v55, v55, v64, s37
	v_add3_u32 v26, v26, v68, s37
	v_lshl_add_u64 v[62:63], v[52:53], 0, s[58:59]
	v_and_b32_e32 v22, 0xffff0000, v22
	v_and_b32_e32 v24, 0xffff0000, v24
	v_and_b32_e32 v55, 0xffff0000, v55
	v_and_b32_e32 v54, 0xffff0000, v54
	v_and_b32_e32 v26, 0xffff0000, v26
	s_waitcnt vmcnt(0)
	v_pk_fma_f32 v[28:29], v[66:67], v[60:61], v[28:29]
	v_pk_fma_f32 v[18:19], v[76:77], v[58:59], v[18:19]
	v_and_b32_sdwa v65, v29, v74 dst_sel:DWORD dst_unused:UNUSED_PAD src0_sel:WORD_1 src1_sel:DWORD
	v_bfe_u32 v58, v18, 16, 1
	v_bfe_u32 v59, v19, 16, 1
	v_bfe_u32 v60, v28, 16, 1
	v_and_b32_sdwa v61, v19, v74 dst_sel:DWORD dst_unused:UNUSED_PAD src0_sel:WORD_1 src1_sel:DWORD
	v_and_b32_sdwa v64, v18, v74 dst_sel:DWORD dst_unused:UNUSED_PAD src0_sel:WORD_1 src1_sel:DWORD
	v_and_b32_sdwa v66, v28, v74 dst_sel:DWORD dst_unused:UNUSED_PAD src0_sel:WORD_1 src1_sel:DWORD
	v_add3_u32 v58, v18, v58, s37
	v_add3_u32 v29, v29, v65, s37
	v_add3_u32 v59, v19, v59, s37
	v_add3_u32 v60, v28, v60, s37
	v_add3_u32 v19, v19, v61, s37
	v_add3_u32 v18, v18, v64, s37
	v_add3_u32 v28, v28, v66, s37
	v_lshrrev_b32_e32 v58, 16, v58
	v_and_b32_e32 v29, 0xffff0000, v29
	v_and_b32_e32 v19, 0xffff0000, v19
	v_and_b32_e32 v18, 0xffff0000, v18
	v_and_b32_e32 v28, 0xffff0000, v28
	v_and_or_b32 v58, v59, s31, v58
	v_or_b32_sdwa v59, v29, v60 dst_sel:DWORD dst_unused:UNUSED_PAD src0_sel:DWORD src1_sel:WORD_1
	global_store_dwordx2 v[62:63], v[58:59], off
.LBB0_1339:
	s_add_i32 s10, s42, 0xfffffc00
	s_lshr_b32 s10, s10, 12
	s_mulk_i32 s10, 0x1800
	s_and_b64 s[8:9], s[8:9], exec
	v_pk_mul_f32 v[66:67], v[24:25], v[24:25]
	v_pk_mul_f32 v[68:69], v[56:57], v[56:57]
	v_pk_mul_f32 v[58:59], v[22:23], v[22:23]
	v_pk_mul_f32 v[60:61], v[20:21], v[20:21]
	s_cselect_b32 s44, 0x6000, s10
	v_pk_mov_b32 v[62:63], v[60:61], v[58:59] op_sel:[1,0]
	v_mov_b32_e32 v61, v59
	v_pk_mov_b32 v[76:77], v[68:69], v[66:67] op_sel:[1,0]
	s_lshl_b64 s[8:9], s[44:45], 2
	v_mov_b32_e32 v69, v67
	v_pk_add_f32 v[58:59], v[62:63], v[60:61]
	v_lshl_add_u64 v[90:91], v[32:33], 0, s[8:9]
	v_pk_add_f32 v[66:67], v[76:77], v[68:69]
	v_mul_f32_e32 v76, v54, v54
	v_mul_f32_e32 v80, v26, v26
	v_pk_add_f32 v[88:89], v[58:59], v[58:59] op_sel_hi:[0,1]
	global_load_dwordx4 v[58:61], v[90:91], off
	v_lshl_add_u64 v[92:93], v[30:31], 0, s[8:9]
	v_pk_add_f32 v[94:95], v[66:67], v[66:67] op_sel_hi:[0,1]
	v_pk_fma_f32 v[96:97], v[54:55], v[54:55], v[76:77] op_sel_hi:[1,1,0]
	v_pk_fma_f32 v[98:99], v[26:27], v[26:27], v[80:81] op_sel_hi:[1,1,0]
	global_load_dwordx4 v[62:65], v[92:93], off
	global_load_dwordx4 v[80:83], v[90:91], off offset:2048
	v_mul_f32_e32 v96, v18, v18
	v_mul_f32_e32 v98, v19, v19
	v_mul_f32_e32 v88, v28, v28
	v_mul_f32_e32 v94, v29, v29
	global_load_dwordx4 v[66:69], v[90:91], off offset:1024
	v_pk_add_f32 v[96:97], v[96:97], v[98:99]
	v_pk_add_f32 v[88:89], v[88:89], v[94:95]
	global_load_dwordx4 v[76:79], v[92:93], off offset:1024
	v_pk_add_f32 v[88:89], v[96:97], v[88:89]
	global_load_dwordx4 v[84:87], v[92:93], off offset:2048
	v_add_f32_e32 v88, v88, v89
	s_waitcnt vmcnt(5)
	v_pk_add_f32 v[58:59], v[58:59], 1.0 op_sel_hi:[1,0]
	v_add_f32_dpp v94, v88, v88 row_ror:8 row_mask:0xf bank_mask:0xf bound_ctrl:1
	global_load_dwordx4 v[88:91], v[90:91], off offset:3072
	v_pk_add_f32 v[60:61], v[60:61], 1.0 op_sel_hi:[1,0]
	v_add_f32_dpp v96, v94, v94 row_ror:4 row_mask:0xf bank_mask:0xf bound_ctrl:1
	global_load_dwordx4 v[92:95], v[92:93], off offset:3072
	s_nop 0
	v_add_f32_dpp v96, v96, v96 row_ror:2 row_mask:0xf bank_mask:0xf bound_ctrl:1
	s_nop 1
	v_add_f32_dpp v96, v96, v96 row_ror:1 row_mask:0xf bank_mask:0xf bound_ctrl:1
	ds_bpermute_b32 v97, v1, v96
	s_waitcnt lgkmcnt(0)
	v_add_f32_e32 v96, v96, v97
	ds_bpermute_b32 v97, v70, v96
	s_waitcnt lgkmcnt(0)
	v_add_f32_e32 v96, v96, v97
	v_fmamk_f32 v96, v96, 0x3a800000, v72
	v_mul_f32_e32 v97, 0x4f800000, v96
	v_cmp_gt_f32_e32 vcc, s43, v96
	s_nop 1
	v_cndmask_b32_e32 v96, v96, v97, vcc
	v_sqrt_f32_e32 v97, v96
	s_nop 0
	v_add_u32_e32 v98, -1, v97
	v_add_u32_e32 v99, 1, v97
	v_fma_f32 v100, -v98, v97, v96
	v_fma_f32 v101, -v99, v97, v96
	v_cmp_ge_f32_e64 s[8:9], 0, v100
	s_nop 1
	v_cndmask_b32_e64 v97, v97, v98, s[8:9]
	v_cmp_lt_f32_e64 s[8:9], 0, v101
	s_nop 1
	v_cndmask_b32_e64 v97, v97, v99, s[8:9]
	v_mul_f32_e32 v98, 0x37800000, v97
	v_cndmask_b32_e32 v97, v97, v98, vcc
	v_cmp_class_f32_e32 vcc, v96, v73
	s_nop 1
	v_cndmask_b32_e32 v96, v97, v96, vcc
	v_div_scale_f32 v97, s[8:9], v96, v96, 1.0
	v_rcp_f32_e32 v98, v97
	v_div_scale_f32 v99, vcc, 1.0, v96, 1.0
	v_fma_f32 v100, -v97, v98, 1.0
	v_fmac_f32_e32 v98, v100, v98
	v_mul_f32_e32 v100, v99, v98
	v_fma_f32 v101, -v97, v100, v99
	v_fmac_f32_e32 v100, v101, v98
	v_fma_f32 v97, -v97, v100, v99
	v_div_fmas_f32 v97, v97, v98, v100
	v_div_fixup_f32 v96, v97, v96, 1.0
	v_pk_mul_f32 v[20:21], v[20:21], v[96:97] op_sel_hi:[1,0]
	v_pk_mul_f32 v[22:23], v[22:23], v[96:97] op_sel_hi:[1,0]
	v_pk_mul_f32 v[20:21], v[10:11], v[20:21]
	v_pk_mul_f32 v[24:25], v[24:25], v[96:97] op_sel_hi:[1,0]
	s_waitcnt vmcnt(6)
	v_pk_fma_f32 v[62:63], v[58:59], v[20:21], v[62:63]
	v_pk_mul_f32 v[20:21], v[56:57], v[96:97] op_sel_hi:[1,0]
	v_pk_mul_f32 v[22:23], v[12:13], v[22:23]
	v_pk_mul_f32 v[20:21], v[2:3], v[20:21]
	s_waitcnt vmcnt(4)
	v_pk_add_f32 v[56:57], v[66:67], 1.0 op_sel_hi:[1,0]
	v_pk_fma_f32 v[60:61], v[60:61], v[22:23], v[64:65]
	v_pk_mul_f32 v[22:23], v[4:5], v[24:25]
	v_pk_add_f32 v[24:25], v[68:69], 1.0 op_sel_hi:[1,0]
	s_waitcnt vmcnt(3)
	v_pk_fma_f32 v[68:69], v[56:57], v[20:21], v[76:77]
	v_pk_mul_f32 v[20:21], v[26:27], v[96:97] op_sel_hi:[1,0]
	v_pk_fma_f32 v[64:65], v[24:25], v[22:23], v[78:79]
	v_pk_mul_f32 v[20:21], v[8:9], v[20:21]
	v_pk_add_f32 v[24:25], v[82:83], 1.0 op_sel_hi:[1,0]
	v_pk_mul_f32 v[18:19], v[18:19], v[96:97] op_sel_hi:[1,0]
	s_waitcnt vmcnt(2)
	v_pk_fma_f32 v[56:57], v[24:25], v[20:21], v[86:87]
	v_pk_mul_f32 v[18:19], v[14:15], v[18:19]
	s_waitcnt vmcnt(1)
	v_pk_add_f32 v[24:25], v[88:89], 1.0 op_sel_hi:[1,0]
	v_pk_mul_f32 v[22:23], v[54:55], v[96:97] op_sel_hi:[1,0]
	s_waitcnt vmcnt(0)
	v_pk_fma_f32 v[58:59], v[24:25], v[18:19], v[92:93]
	v_pk_mul_f32 v[22:23], v[6:7], v[22:23]
	v_pk_add_f32 v[26:27], v[80:81], 1.0 op_sel_hi:[1,0]
	v_pk_mul_f32 v[20:21], v[28:29], v[96:97] op_sel_hi:[1,0]
	v_pk_fma_f32 v[66:67], v[26:27], v[22:23], v[84:85]
	v_pk_mul_f32 v[20:21], v[16:17], v[20:21]
	v_pk_add_f32 v[22:23], v[90:91], 1.0 op_sel_hi:[1,0]
	v_cvt_pk_bf16_f32 v18, v62, v63
	v_pk_fma_f32 v[54:55], v[22:23], v[20:21], v[94:95]
	v_cvt_pk_bf16_f32 v19, v60, v61
	v_add_co_u32_e32 v20, vcc, s47, v52
	s_nop 0
	s_nop 0
	v_addc_co_u32_e32 v21, vcc, -1, v53, vcc
	global_store_dwordx2 v[20:21], v[18:19], off offset:-1536
	v_cvt_pk_bf16_f32 v18, v68, v69
	v_cvt_pk_bf16_f32 v19, v64, v65
	global_store_dwordx2 v[20:21], v[18:19], off offset:-1024
	v_cvt_pk_bf16_f32 v18, v66, v67
	v_cvt_pk_bf16_f32 v19, v56, v57
	global_store_dwordx2 v[20:21], v[18:19], off offset:-512
	v_cvt_pk_bf16_f32 v18, v58, v59
	v_cvt_pk_bf16_f32 v19, v54, v55
	global_store_dwordx2 v[20:21], v[18:19], off
	global_load_dwordx4 v[18:21], v[34:35], off
	s_nop 0
	global_load_dwordx4 v[76:79], v[34:35], off offset:16
	global_load_dwordx4 v[22:25], v[34:35], off offset:32
	global_load_dwordx4 v[80:83], v[34:35], off offset:48
	global_load_dwordx4 v[26:29], v[36:37], off
	global_load_dwordx4 v[84:87], v[36:37], off offset:16
	global_load_dwordx4 v[88:91], v[36:37], off offset:32
	global_load_dwordx4 v[92:95], v[36:37], off offset:48
	global_load_dwordx4 v[96:99], v[38:39], off
	global_load_dwordx4 v[100:103], v[38:39], off offset:16
	global_load_dwordx4 v[104:107], v[38:39], off offset:32
	global_load_dwordx4 v[108:111], v[38:39], off offset:48
	global_load_dwordx4 v[112:115], v[40:41], off
	global_load_dwordx4 v[116:119], v[40:41], off offset:16
	global_load_dwordx4 v[120:123], v[40:41], off offset:32
	global_load_dwordx4 v[124:127], v[40:41], off offset:48
	global_load_dwordx4 v[128:131], v[42:43], off
	global_load_dwordx4 v[132:135], v[42:43], off offset:16
	global_load_dwordx4 v[136:139], v[42:43], off offset:32
	global_load_dwordx4 v[140:143], v[42:43], off offset:48
	global_load_dwordx4 v[144:147], v[44:45], off offset:16
	global_load_dwordx4 v[148:151], v[44:45], off
	global_load_dwordx4 v[152:155], v[44:45], off offset:48
	global_load_dwordx4 v[156:159], v[44:45], off offset:32
	s_waitcnt vmcnt(23)
	v_pk_fma_f32 v[18:19], v[18:19], v[62:63], 0 op_sel_hi:[1,0,0]
	s_waitcnt vmcnt(22)
	v_fma_f32 v171, v76, v62, 0
	v_fma_f32 v184, v77, v62, 0
	v_fma_f32 v185, v78, v62, 0
	v_fma_f32 v186, v79, v62, 0
	global_load_dwordx4 v[76:79], v[46:47], off offset:16
	global_load_dwordx4 v[160:163], v[46:47], off
	s_waitcnt vmcnt(22)
	v_fmac_f32_e32 v171, v80, v63
	v_fmac_f32_e32 v184, v81, v63
	v_fmac_f32_e32 v185, v82, v63
	v_fmac_f32_e32 v186, v83, v63
	global_load_dwordx4 v[80:83], v[46:47], off offset:48
	global_load_dwordx4 v[164:167], v[46:47], off offset:32
	global_load_dwordx4 v[172:175], v[48:49], off offset:16
	global_load_dwordx4 v[176:179], v[48:49], off
	s_waitcnt vmcnt(24)
	v_fmac_f32_e32 v171, v60, v84
	v_fmac_f32_e32 v184, v60, v85
	v_fmac_f32_e32 v185, v60, v86
	v_fmac_f32_e32 v186, v60, v87
	global_load_dwordx4 v[84:87], v[48:49], off offset:48
	global_load_dwordx4 v[180:183], v[48:49], off offset:32
	v_pk_fma_f32 v[18:19], v[22:23], v[62:63], v[18:19] op_sel:[0,1,0]
	v_fma_f32 v168, v20, v62, 0
	v_pk_fma_f32 v[18:19], v[60:61], v[26:27], v[18:19] op_sel_hi:[0,1,1]
	s_waitcnt vmcnt(25)
	v_pk_fma_f32 v[18:19], v[60:61], v[88:89], v[18:19] op_sel:[1,0,0]
	v_fma_f32 v169, v21, v62, 0
	s_waitcnt vmcnt(23)
	v_pk_fma_f32 v[18:19], v[68:69], v[96:97], v[18:19] op_sel_hi:[0,1,1]
	v_fmac_f32_e32 v168, v24, v63
	v_fmac_f32_e32 v169, v25, v63
	s_waitcnt vmcnt(21)
	v_pk_fma_f32 v[18:19], v[68:69], v[104:105], v[18:19] op_sel:[1,0,0]
	v_fmac_f32_e32 v168, v60, v28
	v_fmac_f32_e32 v169, v60, v29
	s_waitcnt vmcnt(19)
	v_pk_fma_f32 v[18:19], v[64:65], v[112:113], v[18:19] op_sel_hi:[0,1,1]
	v_fmac_f32_e32 v168, v61, v90
	v_fmac_f32_e32 v169, v61, v91
	v_fmac_f32_e32 v171, v61, v92
	v_fmac_f32_e32 v184, v61, v93
	v_fmac_f32_e32 v185, v61, v94
	v_fmac_f32_e32 v186, v61, v95
	s_waitcnt vmcnt(17)
	v_pk_fma_f32 v[18:19], v[64:65], v[120:121], v[18:19] op_sel:[1,0,0]
	v_fmac_f32_e32 v168, v68, v98
	v_fmac_f32_e32 v169, v68, v99
	v_fmac_f32_e32 v171, v68, v100
	v_fmac_f32_e32 v184, v68, v101
	v_fmac_f32_e32 v185, v68, v102
	v_fmac_f32_e32 v186, v68, v103
	s_waitcnt vmcnt(15)
	v_pk_fma_f32 v[18:19], v[66:67], v[128:129], v[18:19] op_sel_hi:[0,1,1]
	v_fmac_f32_e32 v168, v69, v106
	v_fmac_f32_e32 v169, v69, v107
	v_fmac_f32_e32 v171, v69, v108
	v_fmac_f32_e32 v184, v69, v109
	v_fmac_f32_e32 v185, v69, v110
	v_fmac_f32_e32 v186, v69, v111
	s_waitcnt vmcnt(13)
	v_pk_fma_f32 v[18:19], v[66:67], v[136:137], v[18:19] op_sel:[1,0,0]
	v_fmac_f32_e32 v168, v64, v114
	v_fmac_f32_e32 v169, v64, v115
	v_fmac_f32_e32 v171, v64, v116
	v_fmac_f32_e32 v184, v64, v117
	v_fmac_f32_e32 v185, v64, v118
	v_fmac_f32_e32 v186, v64, v119
	s_waitcnt vmcnt(10)
	v_pk_fma_f32 v[18:19], v[56:57], v[148:149], v[18:19] op_sel_hi:[0,1,1]
	v_fmac_f32_e32 v168, v65, v122
	v_fmac_f32_e32 v169, v65, v123
	v_fmac_f32_e32 v171, v65, v124
	v_fmac_f32_e32 v184, v65, v125
	v_fmac_f32_e32 v185, v65, v126
	v_fmac_f32_e32 v186, v65, v127
	s_waitcnt vmcnt(8)
	v_pk_fma_f32 v[18:19], v[56:57], v[156:157], v[18:19] op_sel:[1,0,0]
	v_fmac_f32_e32 v168, v66, v130
	v_fmac_f32_e32 v169, v66, v131
	v_fmac_f32_e32 v171, v66, v132
	v_fmac_f32_e32 v184, v66, v133
	v_fmac_f32_e32 v185, v66, v134
	v_fmac_f32_e32 v186, v66, v135
	v_fmac_f32_e32 v168, v67, v138
	v_fmac_f32_e32 v169, v67, v139
	v_fmac_f32_e32 v171, v67, v140
	v_fmac_f32_e32 v184, v67, v141
	v_fmac_f32_e32 v185, v67, v142
	v_fmac_f32_e32 v186, v67, v143
	v_fmac_f32_e32 v168, v56, v150
	v_fmac_f32_e32 v169, v56, v151
	v_fmac_f32_e32 v171, v56, v144
	v_fmac_f32_e32 v184, v56, v145
	v_fmac_f32_e32 v185, v56, v146
	v_fmac_f32_e32 v186, v56, v147
	v_fmac_f32_e32 v168, v57, v158
	v_fmac_f32_e32 v169, v57, v159
	v_fmac_f32_e32 v171, v57, v152
	s_waitcnt vmcnt(6)
	v_pk_fma_f32 v[18:19], v[58:59], v[160:161], v[18:19] op_sel_hi:[0,1,1]
	v_fmac_f32_e32 v184, v57, v153
	v_fmac_f32_e32 v185, v57, v154
	v_fmac_f32_e32 v186, v57, v155
	v_mov_b32_e32 v20, 0
	s_waitcnt vmcnt(4)
	v_pk_fma_f32 v[18:19], v[58:59], v[164:165], v[18:19] op_sel:[1,0,0]
	v_mov_b32_e32 v21, 0
	s_waitcnt vmcnt(2)
	v_pk_fma_f32 v[18:19], v[54:55], v[176:177], v[18:19] op_sel_hi:[0,1,1]
	v_fmac_f32_e32 v168, v58, v162
	v_fmac_f32_e32 v169, v58, v163
	v_fmac_f32_e32 v171, v58, v76
	s_waitcnt vmcnt(0)
	v_pk_fma_f32 v[18:19], v[54:55], v[180:181], v[18:19] op_sel:[1,0,0]
	v_fmac_f32_e32 v184, v58, v77
	v_fmac_f32_e32 v185, v58, v78
	v_fmac_f32_e32 v186, v58, v79
	v_mov_b32_dpp v20, v18 row_ror:8 row_mask:0xf bank_mask:0xf
	v_mov_b32_dpp v21, v19 row_ror:8 row_mask:0xf bank_mask:0xf
	v_fmac_f32_e32 v168, v59, v166
	v_fmac_f32_e32 v169, v59, v167
	v_fmac_f32_e32 v171, v59, v80
	v_fmac_f32_e32 v184, v59, v81
	v_fmac_f32_e32 v185, v59, v82
	v_fmac_f32_e32 v186, v59, v83
	v_pk_add_f32 v[18:19], v[18:19], v[20:21]
	v_mov_b32_e32 v20, 0
	v_mov_b32_e32 v21, 0
	v_fmac_f32_e32 v168, v54, v178
	v_fmac_f32_e32 v169, v54, v179
	v_fmac_f32_e32 v171, v54, v172
	v_fmac_f32_e32 v184, v54, v173
	v_fmac_f32_e32 v185, v54, v174
	v_fmac_f32_e32 v186, v54, v175
	v_mov_b32_dpp v20, v18 row_ror:4 row_mask:0xf bank_mask:0xf
	v_mov_b32_dpp v21, v19 row_ror:4 row_mask:0xf bank_mask:0xf
	v_fmac_f32_e32 v168, v55, v182
	v_fmac_f32_e32 v169, v55, v183
	v_pk_add_f32 v[18:19], v[18:19], v[20:21]
	v_mov_b32_e32 v20, 0
	v_mov_b32_e32 v21, 0
	v_fmac_f32_e32 v171, v55, v84
	v_fmac_f32_e32 v184, v55, v85
	v_fmac_f32_e32 v185, v55, v86
	v_fmac_f32_e32 v186, v55, v87
	v_mov_b32_dpp v20, v18 row_ror:2 row_mask:0xf bank_mask:0xf
	v_mov_b32_dpp v21, v19 row_ror:2 row_mask:0xf bank_mask:0xf
	v_add_f32_dpp v22, v168, v168 row_ror:8 row_mask:0xf bank_mask:0xf bound_ctrl:1
	v_add_f32_dpp v24, v169, v169 row_ror:8 row_mask:0xf bank_mask:0xf bound_ctrl:1
	v_add_f32_dpp v26, v171, v171 row_ror:8 row_mask:0xf bank_mask:0xf bound_ctrl:1
	v_add_f32_dpp v28, v184, v184 row_ror:8 row_mask:0xf bank_mask:0xf bound_ctrl:1
	v_add_f32_dpp v54, v185, v185 row_ror:8 row_mask:0xf bank_mask:0xf bound_ctrl:1
	v_add_f32_dpp v56, v186, v186 row_ror:8 row_mask:0xf bank_mask:0xf bound_ctrl:1
	v_pk_add_f32 v[18:19], v[18:19], v[20:21]
	v_mov_b32_e32 v20, 0
	v_mov_b32_e32 v21, 0
	v_add_f32_dpp v22, v22, v22 row_ror:4 row_mask:0xf bank_mask:0xf bound_ctrl:1
	v_add_f32_dpp v24, v24, v24 row_ror:4 row_mask:0xf bank_mask:0xf bound_ctrl:1
	v_add_f32_dpp v26, v26, v26 row_ror:4 row_mask:0xf bank_mask:0xf bound_ctrl:1
	v_add_f32_dpp v28, v28, v28 row_ror:4 row_mask:0xf bank_mask:0xf bound_ctrl:1
	v_add_f32_dpp v54, v54, v54 row_ror:4 row_mask:0xf bank_mask:0xf bound_ctrl:1
	v_add_f32_dpp v56, v56, v56 row_ror:4 row_mask:0xf bank_mask:0xf bound_ctrl:1
	v_mov_b32_dpp v20, v18 row_ror:1 row_mask:0xf bank_mask:0xf
	v_mov_b32_dpp v21, v19 row_ror:1 row_mask:0xf bank_mask:0xf
	v_add_f32_dpp v22, v22, v22 row_ror:2 row_mask:0xf bank_mask:0xf bound_ctrl:1
	v_add_f32_dpp v24, v24, v24 row_ror:2 row_mask:0xf bank_mask:0xf bound_ctrl:1
	v_add_f32_dpp v26, v26, v26 row_ror:2 row_mask:0xf bank_mask:0xf bound_ctrl:1
	v_add_f32_dpp v28, v28, v28 row_ror:2 row_mask:0xf bank_mask:0xf bound_ctrl:1
	v_add_f32_dpp v54, v54, v54 row_ror:2 row_mask:0xf bank_mask:0xf bound_ctrl:1
	v_add_f32_dpp v56, v56, v56 row_ror:2 row_mask:0xf bank_mask:0xf bound_ctrl:1
	v_pk_add_f32 v[18:19], v[18:19], v[20:21]
	v_add_f32_dpp v22, v22, v22 row_ror:1 row_mask:0xf bank_mask:0xf bound_ctrl:1
	v_add_f32_dpp v24, v24, v24 row_ror:1 row_mask:0xf bank_mask:0xf bound_ctrl:1
	v_add_f32_dpp v26, v26, v26 row_ror:1 row_mask:0xf bank_mask:0xf bound_ctrl:1
	v_add_f32_dpp v28, v28, v28 row_ror:1 row_mask:0xf bank_mask:0xf bound_ctrl:1
	v_add_f32_dpp v54, v54, v54 row_ror:1 row_mask:0xf bank_mask:0xf bound_ctrl:1
	v_add_f32_dpp v56, v56, v56 row_ror:1 row_mask:0xf bank_mask:0xf bound_ctrl:1
	ds_bpermute_b32 v20, v1, v18
	ds_bpermute_b32 v21, v1, v19
	ds_bpermute_b32 v23, v1, v22
	ds_bpermute_b32 v25, v1, v24
	ds_bpermute_b32 v27, v1, v26
	ds_bpermute_b32 v29, v1, v28
	ds_bpermute_b32 v55, v1, v54
	ds_bpermute_b32 v57, v1, v56
	s_waitcnt lgkmcnt(6)
	v_pk_add_f32 v[18:19], v[18:19], v[20:21]
	s_waitcnt lgkmcnt(5)
	v_add_f32_e32 v22, v22, v23
	s_waitcnt lgkmcnt(4)
	v_add_f32_e32 v24, v24, v25
	s_waitcnt lgkmcnt(3)
	v_add_f32_e32 v26, v26, v27
	s_waitcnt lgkmcnt(2)
	v_add_f32_e32 v28, v28, v29
	s_waitcnt lgkmcnt(1)
	v_add_f32_e32 v54, v54, v55
	s_waitcnt lgkmcnt(0)
	v_add_f32_e32 v56, v56, v57
	ds_bpermute_b32 v20, v70, v18
	ds_bpermute_b32 v21, v70, v19
	ds_bpermute_b32 v23, v70, v22
	ds_bpermute_b32 v25, v70, v24
	ds_bpermute_b32 v27, v70, v26
	ds_bpermute_b32 v29, v70, v28
	ds_bpermute_b32 v55, v70, v54
	ds_bpermute_b32 v57, v70, v56
	s_and_saveexec_b64 s[60:61], s[6:7]
	s_cbranch_execz .LBB0_1336
	s_waitcnt lgkmcnt(6)
	v_pk_add_f32 v[18:19], v[18:19], v[20:21]
	s_waitcnt lgkmcnt(5)
	v_add_f32_e32 v22, v22, v23
	v_cmp_gt_f32_e32 vcc, v19, v18
	s_waitcnt lgkmcnt(4)
	v_add_f32_e32 v24, v24, v25
	s_waitcnt lgkmcnt(3)
	v_add_f32_e32 v26, v26, v27
	v_cndmask_b32_e32 v20, v18, v19, vcc
	v_cmp_gt_f32_e64 s[8:9], v22, v20
	s_waitcnt lgkmcnt(2)
	v_add_f32_e32 v28, v28, v29
	s_waitcnt lgkmcnt(1)
	v_add_f32_e32 v54, v54, v55
	v_cndmask_b32_e64 v20, v20, v22, s[8:9]
	v_cmp_gt_f32_e64 s[10:11], v24, v20
	s_waitcnt lgkmcnt(0)
	v_add_f32_e32 v56, v56, v57
	v_cmp_nlt_f32_e64 s[20:21], s62, v18
	v_cndmask_b32_e64 v20, v20, v24, s[10:11]
	v_cmp_gt_f32_e64 s[12:13], v26, v20
	s_ashr_i32 s49, s48, 31
	s_nop 0
	v_cndmask_b32_e64 v20, v20, v26, s[12:13]
	v_cmp_gt_f32_e64 s[14:15], v28, v20
	s_nop 1
	v_cndmask_b32_e64 v20, v20, v28, s[14:15]
	v_cmp_gt_f32_e64 s[16:17], v54, v20
	s_nop 1
	v_cndmask_b32_e64 v21, v20, v54, s[16:17]
	v_cndmask_b32_e64 v20, 0, 1, vcc
	v_cndmask_b32_e64 v20, v20, 2, s[8:9]
	v_cndmask_b32_e64 v20, v20, 3, s[10:11]
	v_cndmask_b32_e64 v20, v20, 4, s[12:13]
	v_cndmask_b32_e64 v20, v20, 5, s[14:15]
	v_cndmask_b32_e64 v20, v20, 6, s[16:17]
	v_cmp_ngt_f32_e32 vcc, v56, v21
	s_and_b64 s[22:23], s[16:17], vcc
	s_nop 0
	v_cndmask_b32_e32 v20, 7, v20, vcc
	v_cmp_eq_u32_e64 s[18:19], 0, v20
	s_or_b64 s[18:19], s[18:19], s[20:21]
	v_cmp_ne_u32_e64 s[16:17], 1, v20
	v_cndmask_b32_e64 v18, v18, v75, s[18:19]
	v_cmp_gt_f32_e64 s[20:21], v19, v18
	s_and_b64 s[16:17], s[16:17], s[20:21]
	v_cndmask_b32_e64 v18, v18, v19, s[16:17]
	v_cmp_ne_u32_e64 s[14:15], 2, v20
	v_cmp_gt_f32_e64 s[20:21], v22, v18
	s_and_b64 s[14:15], s[14:15], s[20:21]
	v_cndmask_b32_e64 v18, v18, v22, s[14:15]
	v_cmp_ne_u32_e64 s[12:13], 3, v20
	v_cmp_gt_f32_e64 s[20:21], v24, v18
	s_and_b64 s[12:13], s[12:13], s[20:21]
	v_cndmask_b32_e64 v18, v18, v24, s[12:13]
	v_cmp_ne_u32_e64 s[10:11], 4, v20
	v_cmp_gt_f32_e64 s[20:21], v26, v18
	s_and_b64 s[10:11], s[10:11], s[20:21]
	v_cndmask_b32_e64 v18, v18, v26, s[10:11]
	v_cmp_ne_u32_e64 s[8:9], 5, v20
	v_cmp_gt_f32_e64 s[20:21], v28, v18
	s_and_b64 s[8:9], s[8:9], s[20:21]
	v_cndmask_b32_e64 v18, v18, v28, s[8:9]
	v_cmp_ngt_f32_e64 s[20:21], v54, v18
	s_or_b64 s[20:21], s[22:23], s[20:21]
	v_cndmask_b32_e32 v21, v56, v21, vcc
	v_cndmask_b32_e64 v18, v54, v18, s[20:21]
	v_cmp_gt_f32_e64 s[22:23], v56, v18
	s_and_b64 s[22:23], vcc, s[22:23]
	v_cndmask_b32_e64 v19, 0, -1, s[18:19]
	v_cndmask_b32_e64 v18, v18, v56, s[22:23]
	v_sub_f32_e32 v18, v18, v21
	v_mul_f32_e32 v18, 0x3fb8aa3b, v18
	v_exp_f32_e32 v18, v18
	v_cndmask_b32_e64 v19, v19, 1, s[16:17]
	v_cndmask_b32_e64 v19, v19, 2, s[14:15]
	v_cndmask_b32_e64 v19, v19, 3, s[12:13]
	v_add_f32_e32 v22, 1.0, v18
	v_cndmask_b32_e64 v19, v19, 4, s[10:11]
	v_div_scale_f32 v23, s[10:11], v22, v22, 1.0
	v_rcp_f32_e32 v24, v23
	v_cndmask_b32_e64 v19, v19, 5, s[8:9]
	v_cndmask_b32_e64 v19, 6, v19, s[20:21]
	v_lshl_add_u32 v25, v20, 2, s3
	v_cndmask_b32_e64 v21, v19, 7, s[22:23]
	v_fma_f32 v19, -v23, v24, 1.0
	ds_read_b32 v26, v25
	v_fmac_f32_e32 v24, v19, v24
	v_div_scale_f32 v19, vcc, 1.0, v22, 1.0
	v_mul_f32_e32 v27, v19, v24
	v_fma_f32 v28, -v23, v27, v19
	v_fmac_f32_e32 v27, v28, v24
	v_fma_f32 v19, -v23, v27, v19
	s_waitcnt lgkmcnt(0)
	v_add_u32_e32 v23, 1, v26
	ds_write_b32 v25, v23
	v_lshl_add_u32 v23, v21, 2, s3
	ds_read_b32 v25, v23
	s_lshl_b64 s[8:9], s[48:49], 2
	s_add_u32 s10, s78, s8
	v_readlane_b32 s11, v255, 7
	v_div_fmas_f32 v19, v19, v24, v27
	s_addc_u32 s11, s11, s9
	s_add_i32 s12, s48, 1
	v_div_fixup_f32 v19, v19, v22, 1.0
	s_waitcnt lgkmcnt(0)
	v_add_u32_e32 v22, 1, v25
	s_ashr_i32 s13, s12, 31
	ds_write_b32 v23, v22
	global_store_dwordx2 v71, v[20:21], s[10:11]
	s_add_u32 s10, s35, s8
	s_addc_u32 s11, s74, s9
	global_store_dword v71, v19, s[10:11]
	s_lshl_b64 s[10:11], s[12:13], 2
	s_add_u32 s12, s35, s10
	v_mul_f32_e32 v18, v18, v19
	s_addc_u32 s13, s74, s11
	global_store_dword v71, v18, s[12:13]
	v_readlane_b32 s12, v255, 8
	s_add_u32 s8, s12, s8
	v_readlane_b32 s13, v255, 9
	s_addc_u32 s9, s13, s9
	global_store_dword v71, v26, s[8:9]
	s_add_u32 s8, s12, s10
	s_addc_u32 s9, s13, s11
	global_store_dword v71, v25, s[8:9]
	s_branch .LBB0_1336

.LBB0_1683:
	v_and_b32_sdwa v52, v63, v74 dst_sel:DWORD dst_unused:UNUSED_PAD src0_sel:WORD_1 src1_sel:DWORD
	v_and_b32_sdwa v53, v62, v74 dst_sel:DWORD dst_unused:UNUSED_PAD src0_sel:WORD_1 src1_sel:DWORD
	v_add3_u32 v52, v63, v52, s21
	v_add3_u32 v53, v62, v53, s21
	v_and_b32_e32 v77, 0xffff0000, v52
	v_and_b32_e32 v76, 0xffff0000, v53
	v_and_b32_sdwa v52, v67, v74 dst_sel:DWORD dst_unused:UNUSED_PAD src0_sel:WORD_1 src1_sel:DWORD
	v_and_b32_sdwa v53, v66, v74 dst_sel:DWORD dst_unused:UNUSED_PAD src0_sel:WORD_1 src1_sel:DWORD
	v_add3_u32 v52, v67, v52, s21
	v_add3_u32 v53, v66, v53, s21
	v_and_b32_e32 v79, 0xffff0000, v52
	v_and_b32_e32 v78, 0xffff0000, v53
	v_and_b32_sdwa v52, v69, v74 dst_sel:DWORD dst_unused:UNUSED_PAD src0_sel:WORD_1 src1_sel:DWORD
	v_and_b32_sdwa v53, v68, v74 dst_sel:DWORD dst_unused:UNUSED_PAD src0_sel:WORD_1 src1_sel:DWORD
	v_add3_u32 v52, v69, v52, s21
	v_add3_u32 v53, v68, v53, s21
	v_and_b32_e32 v81, 0xffff0000, v52
	v_and_b32_e32 v80, 0xffff0000, v53
	v_mov_b32_e32 v52, v44
	v_mov_b32_e32 v53, v44
	v_pk_mul_f32 v[26:27], v[44:45], v[26:27]
	v_lshlrev_b32_e32 v50, 16, v46
	v_and_b32_e32 v51, 0xffff0000, v46
	v_pk_mul_f32 v[28:29], v[52:53], v[28:29]
	v_mov_b32_e32 v44, v42
	v_mov_b32_e32 v45, v42
	v_pk_fma_f32 v[22:23], v[42:43], v[22:23], v[26:27]
	v_lshlrev_b32_e32 v46, 16, v47
	v_and_b32_e32 v47, 0xffff0000, v47
	v_pk_fma_f32 v[24:25], v[44:45], v[24:25], v[28:29]
	s_waitcnt vmcnt(0)
	v_pk_fma_f32 v[18:19], v[18:19], v[22:23], v[50:51]
	v_pk_fma_f32 v[20:21], v[20:21], v[24:25], v[46:47]
	v_bfe_u32 v22, v18, 16, 1
	v_bfe_u32 v23, v19, 16, 1
	v_and_b32_sdwa v24, v19, v74 dst_sel:DWORD dst_unused:UNUSED_PAD src0_sel:WORD_1 src1_sel:DWORD
	v_and_b32_sdwa v25, v18, v74 dst_sel:DWORD dst_unused:UNUSED_PAD src0_sel:WORD_1 src1_sel:DWORD
	v_add3_u32 v22, v18, v22, s21
	v_add3_u32 v23, v19, v23, s21
	v_add3_u32 v19, v19, v24, s21
	v_add3_u32 v18, v18, v25, s21
	v_and_b32_e32 v47, 0xffff0000, v19
	v_and_b32_e32 v46, 0xffff0000, v18
	v_and_b32_sdwa v18, v21, v74 dst_sel:DWORD dst_unused:UNUSED_PAD src0_sel:WORD_1 src1_sel:DWORD
	v_and_b32_sdwa v19, v20, v74 dst_sel:DWORD dst_unused:UNUSED_PAD src0_sel:WORD_1 src1_sel:DWORD
	v_lshrrev_b32_e32 v22, 16, v22
	v_add3_u32 v18, v21, v18, s21
	v_add3_u32 v19, v20, v19, s21
	v_and_or_b32 v22, v23, s9, v22
	v_bfe_u32 v23, v20, 16, 1
	v_and_b32_e32 v83, 0xffff0000, v18
	v_and_b32_e32 v82, 0xffff0000, v19
	v_pk_mov_b32 v[18:19], v[76:77], v[48:49] op_sel:[1,0]
	v_add3_u32 v23, v20, v23, s21
	v_pk_mul_f32 v[18:19], v[18:19], v[18:19]
	v_mov_b32_e32 v20, v76
	v_mov_b32_e32 v21, v49
	v_or_b32_sdwa v23, v83, v23 dst_sel:DWORD dst_unused:UNUSED_PAD src0_sel:DWORD src1_sel:WORD_1
	v_pk_fma_f32 v[18:19], v[20:21], v[20:21], v[18:19]
	s_lshl_b64 s[4:5], s[10:11], 2
	global_store_dwordx2 v[40:41], v[22:23], off offset:1536
	v_pk_add_f32 v[50:51], v[18:19], v[18:19] op_sel:[0,1] op_sel_hi:[1,0]
	v_pk_mov_b32 v[18:19], v[78:79], v[64:65] op_sel:[1,0]
	v_lshl_add_u64 v[54:55], v[38:39], 0, s[4:5]
	v_pk_mul_f32 v[52:53], v[18:19], v[18:19]
	global_load_dwordx4 v[18:21], v[54:55], off
	global_load_dwordx4 v[22:25], v[54:55], off offset:1024
	global_load_dwordx4 v[26:29], v[54:55], off offset:2048
	global_load_dwordx4 v[42:45], v[54:55], off offset:3072
	v_mov_b32_e32 v54, v78
	v_mov_b32_e32 v55, v65
	v_pk_fma_f32 v[52:53], v[54:55], v[54:55], v[52:53]
	v_mul_f32_e32 v54, v81, v81
	v_mul_f32_e32 v56, v59, v59
	v_pk_add_f32 v[52:53], v[52:53], v[52:53] op_sel:[0,1] op_sel_hi:[1,0]
	v_pk_fma_f32 v[54:55], v[80:81], v[80:81], v[54:55] op_sel_hi:[1,1,0]
	v_pk_fma_f32 v[56:57], v[58:59], v[58:59], v[56:57] op_sel_hi:[1,1,0]
	v_pk_mul_f32 v[60:61], v[46:47], v[46:47]
	v_pk_mul_f32 v[62:63], v[82:83], v[82:83]
	v_mov_b32_e32 v51, v60
	v_mov_b32_e32 v53, v61
	v_mov_b32_e32 v55, v63
	v_mov_b32_e32 v57, v62
	v_pk_add_f32 v[50:51], v[50:51], v[52:53]
	v_pk_add_f32 v[52:53], v[54:55], v[56:57]
	v_lshl_add_u64 v[84:85], v[36:37], 0, s[4:5]
	v_pk_add_f32 v[50:51], v[50:51], v[52:53]
	s_add_i32 s8, s8, s12
	v_add_f32_e32 v60, v50, v51
	global_load_dwordx4 v[50:53], v[84:85], off offset:2048
	global_load_dwordx4 v[54:57], v[84:85], off offset:3072
	v_add_f32_dpp v60, v60, v60 row_ror:8 row_mask:0xf bank_mask:0xf bound_ctrl:1
	s_add_i32 s14, s14, s3
	s_cmpk_lt_i32 s8, 0x4400
	v_add_f32_dpp v75, v60, v60 row_ror:4 row_mask:0xf bank_mask:0xf bound_ctrl:1
	global_load_dwordx4 v[60:63], v[84:85], off
	global_load_dwordx4 v[66:69], v[84:85], off offset:1024
	v_add_f32_dpp v75, v75, v75 row_ror:2 row_mask:0xf bank_mask:0xf bound_ctrl:1
	s_waitcnt vmcnt(7)
	v_pk_add_f32 v[18:19], v[18:19], 1.0 op_sel_hi:[1,0]
	v_add_f32_dpp v75, v75, v75 row_ror:1 row_mask:0xf bank_mask:0xf bound_ctrl:1
	ds_bpermute_b32 v84, v1, v75
	s_waitcnt vmcnt(4)
	v_pk_add_f32 v[42:43], v[42:43], 1.0 op_sel_hi:[1,0]
	v_pk_add_f32 v[20:21], v[20:21], 1.0 op_sel_hi:[1,0]
	v_pk_add_f32 v[22:23], v[22:23], 1.0 op_sel_hi:[1,0]
	v_pk_add_f32 v[24:25], v[24:25], 1.0 op_sel_hi:[1,0]
	s_waitcnt lgkmcnt(0)
	v_add_f32_e32 v75, v75, v84
	ds_bpermute_b32 v84, v70, v75
	v_pk_add_f32 v[26:27], v[26:27], 1.0 op_sel_hi:[1,0]
	v_pk_add_f32 v[28:29], v[28:29], 1.0 op_sel_hi:[1,0]
	v_pk_add_f32 v[44:45], v[44:45], 1.0 op_sel_hi:[1,0]
	s_waitcnt lgkmcnt(0)
	v_add_f32_e32 v75, v75, v84
	v_fmamk_f32 v75, v75, 0x3a800000, v72
	v_mul_f32_e32 v84, 0x4f800000, v75
	v_cmp_gt_f32_e32 vcc, s22, v75
	s_nop 1
	v_cndmask_b32_e32 v75, v75, v84, vcc
	v_sqrt_f32_e32 v84, v75
	s_nop 0
	v_add_u32_e32 v85, -1, v84
	v_fma_f32 v86, -v85, v84, v75
	v_cmp_ge_f32_e64 s[4:5], 0, v86
	v_add_u32_e32 v86, 1, v84
	s_nop 0
	v_cndmask_b32_e64 v85, v84, v85, s[4:5]
	v_fma_f32 v84, -v86, v84, v75
	v_cmp_lt_f32_e64 s[4:5], 0, v84
	s_nop 1
	v_cndmask_b32_e64 v84, v85, v86, s[4:5]
	v_mul_f32_e32 v85, 0x37800000, v84
	v_cndmask_b32_e32 v84, v84, v85, vcc
	v_cmp_class_f32_e32 vcc, v75, v73
	s_nop 1
	v_cndmask_b32_e32 v75, v84, v75, vcc
	v_div_scale_f32 v84, s[4:5], v75, v75, 1.0
	v_rcp_f32_e32 v85, v84
	s_nop 0
	v_fma_f32 v86, -v84, v85, 1.0
	v_fmac_f32_e32 v85, v86, v85
	v_div_scale_f32 v86, vcc, 1.0, v75, 1.0
	v_mul_f32_e32 v87, v86, v85
	v_fma_f32 v88, -v84, v87, v86
	v_fmac_f32_e32 v87, v88, v85
	v_fma_f32 v84, -v84, v87, v86
	v_div_fmas_f32 v84, v84, v85, v87
	v_div_fixup_f32 v84, v84, v75, 1.0
	v_pk_mul_f32 v[76:77], v[76:77], v[84:85] op_sel_hi:[1,0]
	v_pk_mul_f32 v[46:47], v[46:47], v[84:85] op_sel_hi:[1,0]
	v_pk_mul_f32 v[76:77], v[10:11], v[76:77]
	v_pk_mul_f32 v[46:47], v[14:15], v[46:47]
	s_waitcnt vmcnt(1)
	v_pk_fma_f32 v[18:19], v[18:19], v[76:77], v[60:61]
	v_pk_mul_f32 v[48:49], v[48:49], v[84:85] op_sel_hi:[1,0]
	v_pk_fma_f32 v[42:43], v[42:43], v[46:47], v[54:55]
	v_bfe_u32 v46, v18, 16, 1
	v_pk_mul_f32 v[48:49], v[12:13], v[48:49]
	v_add3_u32 v18, v18, v46, s21
	v_bfe_u32 v46, v19, 16, 1
	v_pk_fma_f32 v[20:21], v[20:21], v[48:49], v[62:63]
	v_lshrrev_b32_e32 v18, 16, v18
	v_add3_u32 v19, v19, v46, s21
	v_and_or_b32 v18, v19, s9, v18
	v_bfe_u32 v19, v20, 16, 1
	v_add3_u32 v19, v20, v19, s21
	v_bfe_u32 v20, v21, 16, 1
	v_pk_mul_f32 v[78:79], v[78:79], v[84:85] op_sel_hi:[1,0]
	v_lshrrev_b32_e32 v19, 16, v19
	v_add3_u32 v20, v21, v20, s21
	v_pk_mul_f32 v[78:79], v[2:3], v[78:79]
	v_and_or_b32 v19, v20, s9, v19
	v_add_co_u32_e32 v20, vcc, s23, v40
	s_waitcnt vmcnt(0)
	v_pk_fma_f32 v[22:23], v[22:23], v[78:79], v[66:67]
	v_addc_co_u32_e32 v21, vcc, 0, v41, vcc
	v_pk_mul_f32 v[64:65], v[64:65], v[84:85] op_sel_hi:[1,0]
	global_store_dwordx2 v[20:21], v[18:19], off
	v_pk_mul_f32 v[64:65], v[4:5], v[64:65]
	v_pk_fma_f32 v[24:25], v[24:25], v[64:65], v[68:69]
	v_cvt_pk_bf16_f32 v18, v22, v23
	v_pk_mul_f32 v[80:81], v[80:81], v[84:85] op_sel_hi:[1,0]
	v_pk_mul_f32 v[80:81], v[6:7], v[80:81]
	v_pk_fma_f32 v[26:27], v[26:27], v[80:81], v[50:51]
	v_cvt_pk_bf16_f32 v19, v24, v25
	v_pk_mul_f32 v[58:59], v[58:59], v[84:85] op_sel_hi:[1,0]
	global_store_dwordx2 v[20:21], v[18:19], off offset:512
	v_pk_mul_f32 v[58:59], v[8:9], v[58:59]
	v_pk_fma_f32 v[28:29], v[28:29], v[58:59], v[52:53]
	v_cvt_pk_bf16_f32 v18, v26, v27
	v_cvt_pk_bf16_f32 v19, v28, v29
	v_pk_mul_f32 v[82:83], v[82:83], v[84:85] op_sel_hi:[1,0]
	global_store_dwordx2 v[20:21], v[18:19], off offset:1024
	v_pk_mul_f32 v[82:83], v[16:17], v[82:83]
	v_pk_fma_f32 v[44:45], v[44:45], v[82:83], v[56:57]
	v_cvt_pk_bf16_f32 v18, v42, v43
	v_cvt_pk_bf16_f32 v19, v44, v45
	v_lshl_add_u64 v[40:41], v[40:41], 0, s[16:17]
	global_store_dwordx2 v[20:21], v[18:19], off offset:1536
	s_cbranch_scc0 .LBB0_1716

.LBB0_1692:
	s_waitcnt vmcnt(1)
	v_pk_mul_f32 v[26:27], v[44:45], v[26:27] op_sel_hi:[0,1]
	v_lshlrev_b32_e32 v62, 16, v48
	v_and_b32_e32 v63, 0xffff0000, v48
	v_pk_fma_f32 v[22:23], v[42:43], v[22:23], v[26:27] op_sel_hi:[0,1,1]
	v_pk_mul_f32 v[28:29], v[44:45], v[28:29] op_sel_hi:[0,1]
	s_waitcnt vmcnt(0)
	v_pk_fma_f32 v[62:63], v[18:19], v[22:23], v[62:63]
	v_lshlrev_b32_e32 v48, 16, v49
	v_and_b32_e32 v49, 0xffff0000, v49
	v_pk_fma_f32 v[24:25], v[42:43], v[24:25], v[28:29] op_sel_hi:[0,1,1]
	v_pk_fma_f32 v[24:25], v[20:21], v[24:25], v[48:49]
	v_and_b32_sdwa v20, v25, v74 dst_sel:DWORD dst_unused:UNUSED_PAD src0_sel:WORD_1 src1_sel:DWORD
	v_cvt_pk_bf16_f32 v18, v62, v63
	v_bfe_u32 v19, v24, 16, 1
	v_add3_u32 v20, v25, v20, s21
	v_add3_u32 v19, v24, v19, s21
	v_and_b32_e32 v49, 0xffff0000, v20
	v_or_b32_sdwa v19, v49, v19 dst_sel:DWORD dst_unused:UNUSED_PAD src0_sel:DWORD src1_sel:WORD_1
	global_store_dwordx2 v[40:41], v[18:19], off
	global_load_dwordx4 v[18:21], v[54:55], off offset:1024
	v_and_b32_sdwa v22, v24, v74 dst_sel:DWORD dst_unused:UNUSED_PAD src0_sel:WORD_1 src1_sel:DWORD
	v_add3_u32 v22, v24, v22, s21
	v_and_b32_e32 v48, 0xffff0000, v22
	v_cndmask_b32_e64 v22, 0, 1, s[6:7]
	v_cmp_ne_u32_e64 s[4:5], 1, v22
	s_andn2_b64 vcc, exec, s[6:7]
	s_mov_b64 s[6:7], -1
	s_cbranch_vccnz .LBB0_1694
	global_load_dwordx2 v[24:25], v[56:57], off offset:512
	s_mov_b64 s[6:7], 0
	s_waitcnt vmcnt(0)
	v_lshlrev_b32_e32 v22, 16, v24
	v_and_b32_e32 v23, 0xffff0000, v24
	v_lshlrev_b32_e32 v24, 16, v25
	v_and_b32_e32 v25, 0xffff0000, v25

.LBB0_1700:
	v_mov_b32_e32 v45, v44
	v_mov_b32_e32 v43, v42
	v_pk_mul_f32 v[26:27], v[44:45], v[26:27]
	v_lshlrev_b32_e32 v66, 16, v64
	v_and_b32_e32 v67, 0xffff0000, v64
	v_mov_b32_e32 v68, v44
	v_mov_b32_e32 v69, v44
	v_pk_fma_f32 v[22:23], v[42:43], v[22:23], v[26:27]
	v_pk_mul_f32 v[28:29], v[68:69], v[28:29]
	v_mov_b32_e32 v68, v42
	v_mov_b32_e32 v69, v42
	s_waitcnt vmcnt(0)
	v_pk_fma_f32 v[66:67], v[18:19], v[22:23], v[66:67]
	v_lshlrev_b32_e32 v64, 16, v65
	v_and_b32_e32 v65, 0xffff0000, v65
	v_pk_fma_f32 v[24:25], v[68:69], v[24:25], v[28:29]
	v_pk_fma_f32 v[24:25], v[20:21], v[24:25], v[64:65]
	v_and_b32_sdwa v20, v25, v74 dst_sel:DWORD dst_unused:UNUSED_PAD src0_sel:WORD_1 src1_sel:DWORD
	v_cvt_pk_bf16_f32 v18, v66, v67
	v_bfe_u32 v19, v24, 16, 1
	v_add3_u32 v20, v25, v20, s21
	v_add3_u32 v19, v24, v19, s21
	v_and_b32_e32 v65, 0xffff0000, v20
	v_or_b32_sdwa v19, v65, v19 dst_sel:DWORD dst_unused:UNUSED_PAD src0_sel:DWORD src1_sel:WORD_1
	global_store_dwordx2 v[40:41], v[18:19], off offset:512
	global_load_dwordx4 v[18:21], v[54:55], off offset:2048
	v_and_b32_sdwa v22, v24, v74 dst_sel:DWORD dst_unused:UNUSED_PAD src0_sel:WORD_1 src1_sel:DWORD
	v_add3_u32 v22, v24, v22, s21
	v_and_b32_e32 v64, 0xffff0000, v22
	s_and_b64 vcc, exec, s[4:5]
	s_mov_b64 s[18:19], -1
	s_cbranch_vccnz .LBB0_1704
	global_load_dwordx2 v[24:25], v[56:57], off offset:1024
	s_waitcnt vmcnt(0)
	v_lshlrev_b32_e32 v22, 16, v24
	v_and_b32_e32 v23, 0xffff0000, v24
	v_lshlrev_b32_e32 v24, 16, v25
	v_and_b32_e32 v25, 0xffff0000, v25
	s_cbranch_execz .LBB0_1705

.LBB0_1708:
	s_nop 0
	v_pk_mul_f32 v[26:27], v[44:45], v[26:27]
	v_lshlrev_b32_e32 v68, 16, v58
	v_and_b32_e32 v69, 0xffff0000, v58
	v_mov_b32_e32 v76, v44
	v_mov_b32_e32 v77, v44
	v_pk_fma_f32 v[22:23], v[42:43], v[22:23], v[26:27]
	v_pk_mul_f32 v[28:29], v[76:77], v[28:29]
	v_mov_b32_e32 v76, v42
	v_mov_b32_e32 v77, v42
	s_waitcnt vmcnt(0)
	v_pk_fma_f32 v[68:69], v[18:19], v[22:23], v[68:69]
	v_lshlrev_b32_e32 v58, 16, v59
	v_and_b32_e32 v59, 0xffff0000, v59
	v_pk_fma_f32 v[24:25], v[76:77], v[24:25], v[28:29]
	v_pk_fma_f32 v[24:25], v[20:21], v[24:25], v[58:59]
	v_and_b32_sdwa v20, v25, v74 dst_sel:DWORD dst_unused:UNUSED_PAD src0_sel:WORD_1 src1_sel:DWORD
	v_cvt_pk_bf16_f32 v18, v68, v69
	v_bfe_u32 v19, v24, 16, 1
	v_add3_u32 v20, v25, v20, s21
	v_add3_u32 v19, v24, v19, s21
	v_and_b32_e32 v59, 0xffff0000, v20
	v_or_b32_sdwa v19, v59, v19 dst_sel:DWORD dst_unused:UNUSED_PAD src0_sel:DWORD src1_sel:WORD_1
	global_store_dwordx2 v[40:41], v[18:19], off offset:1024
	global_load_dwordx4 v[18:21], v[54:55], off offset:3072
	v_and_b32_sdwa v22, v24, v74 dst_sel:DWORD dst_unused:UNUSED_PAD src0_sel:WORD_1 src1_sel:DWORD
	v_add3_u32 v22, v24, v22, s21
	v_and_b32_e32 v58, 0xffff0000, v22
	s_and_b64 vcc, exec, s[4:5]
	s_mov_b64 s[4:5], -1
	s_cbranch_vccnz .LBB0_1712
	global_load_dwordx2 v[24:25], v[56:57], off offset:1536
	s_waitcnt vmcnt(0)
	v_lshlrev_b32_e32 v22, 16, v24
	v_and_b32_e32 v23, 0xffff0000, v24
	v_lshlrev_b32_e32 v24, 16, v25
	v_and_b32_e32 v25, 0xffff0000, v25
	s_cbranch_execz .LBB0_1713

.LBB0_2016:
	v_pk_mul_f32 v[62:63], v[28:29], v[28:29]
	v_pk_mul_f32 v[64:65], v[26:27], v[26:27]
	v_pk_mul_f32 v[58:59], v[30:31], v[30:31]
	v_pk_mul_f32 v[60:61], v[32:33], v[32:33]
	v_pk_mov_b32 v[66:67], v[64:65], v[62:63] op_sel:[1,0]
	v_mov_b32_e32 v65, v63
	v_pk_add_f32 v[62:63], v[66:67], v[64:65]
	v_pk_mov_b32 v[64:65], v[60:61], v[58:59] op_sel:[1,0]
	v_mov_b32_e32 v61, v59
	v_pk_add_f32 v[58:59], v[64:65], v[60:61]
	s_add_i32 s10, s6, 0xfffffc00
	v_pk_add_f32 v[58:59], v[58:59], v[58:59] op_sel_hi:[0,1]
	v_mul_f32_e32 v58, v40, v40
	s_lshr_b32 s10, s10, 12
	v_pk_fma_f32 v[60:61], v[40:41], v[40:41], v[58:59] op_sel_hi:[1,1,0]
	v_mul_f32_e32 v58, v36, v36
	s_mulk_i32 s10, 0x1800
	s_and_b64 s[4:5], s[4:5], exec
	v_pk_add_f32 v[62:63], v[62:63], v[62:63] op_sel_hi:[0,1]
	v_pk_fma_f32 v[64:65], v[36:37], v[36:37], v[58:59] op_sel_hi:[1,1,0]
	s_cselect_b32 s10, 0x6000, s10
	v_mul_f32_e32 v60, v34, v34
	v_mul_f32_e32 v64, v35, v35
	v_mul_f32_e32 v62, v38, v38
	v_mul_f32_e32 v58, v39, v39
	s_lshl_b64 s[4:5], s[10:11], 2
	v_pk_add_f32 v[66:67], v[60:61], v[64:65]
	v_pk_add_f32 v[68:69], v[62:63], v[58:59]
	v_lshl_add_u64 v[54:55], v[20:21], 0, s[4:5]
	v_lshl_add_u64 v[70:71], v[18:19], 0, s[4:5]
	v_pk_add_f32 v[66:67], v[66:67], v[68:69]
	global_load_dwordx4 v[42:45], v[54:55], off
	global_load_dwordx4 v[46:49], v[54:55], off offset:1024
	global_load_dwordx4 v[50:53], v[54:55], off offset:2048
	s_nop 0
	global_load_dwordx4 v[54:57], v[54:55], off offset:3072
	s_nop 0
	global_load_dwordx4 v[58:61], v[70:71], off offset:2048
	global_load_dwordx4 v[62:65], v[70:71], off offset:3072
	v_add_f32_e32 v74, v66, v67
	global_load_dwordx4 v[66:69], v[70:71], off
	s_nop 0
	global_load_dwordx4 v[70:73], v[70:71], off offset:1024
	v_add_f32_dpp v74, v74, v74 row_ror:8 row_mask:0xf bank_mask:0xf bound_ctrl:1
	s_add_i32 s6, s6, s8
	s_cmpk_lt_i32 s6, 0x4400
	v_add_f32_dpp v74, v74, v74 row_ror:4 row_mask:0xf bank_mask:0xf bound_ctrl:1
	s_waitcnt vmcnt(7)
	v_pk_add_f32 v[42:43], v[42:43], 1.0 op_sel_hi:[1,0]
	v_add_f32_dpp v74, v74, v74 row_ror:2 row_mask:0xf bank_mask:0xf bound_ctrl:1
	v_pk_add_f32 v[44:45], v[44:45], 1.0 op_sel_hi:[1,0]
	s_waitcnt vmcnt(6)
	v_pk_add_f32 v[46:47], v[46:47], 1.0 op_sel_hi:[1,0]
	v_add_f32_dpp v74, v74, v74 row_ror:1 row_mask:0xf bank_mask:0xf bound_ctrl:1
	ds_bpermute_b32 v75, v1, v74
	v_pk_add_f32 v[48:49], v[48:49], 1.0 op_sel_hi:[1,0]
	s_waitcnt vmcnt(5)
	v_pk_add_f32 v[50:51], v[50:51], 1.0 op_sel_hi:[1,0]
	v_pk_add_f32 v[52:53], v[52:53], 1.0 op_sel_hi:[1,0]
	s_waitcnt vmcnt(4)
	v_pk_add_f32 v[54:55], v[54:55], 1.0 op_sel_hi:[1,0]
	s_waitcnt lgkmcnt(0)
	v_add_f32_e32 v74, v74, v75
	ds_bpermute_b32 v75, v88, v74
	v_pk_add_f32 v[56:57], v[56:57], 1.0 op_sel_hi:[1,0]
	s_waitcnt lgkmcnt(0)
	v_add_f32_e32 v74, v74, v75
	v_fmamk_f32 v74, v74, 0x3a800000, v89
	v_mul_f32_e32 v75, 0x4f800000, v74
	v_cmp_gt_f32_e32 vcc, s42, v74
	s_nop 1
	v_cndmask_b32_e32 v74, v74, v75, vcc
	v_sqrt_f32_e32 v75, v74
	s_nop 0
	v_add_u32_e32 v76, -1, v75
	v_add_u32_e32 v77, 1, v75
	v_fma_f32 v78, -v76, v75, v74
	v_fma_f32 v79, -v77, v75, v74
	v_cmp_ge_f32_e64 s[4:5], 0, v78
	s_nop 1
	v_cndmask_b32_e64 v75, v75, v76, s[4:5]
	v_cmp_lt_f32_e64 s[4:5], 0, v79
	s_nop 1
	v_cndmask_b32_e64 v75, v75, v77, s[4:5]
	v_mul_f32_e32 v76, 0x37800000, v75
	v_cndmask_b32_e32 v75, v75, v76, vcc
	v_cmp_class_f32_e32 vcc, v74, v90
	s_nop 1
	v_cndmask_b32_e32 v74, v75, v74, vcc
	v_div_scale_f32 v75, s[4:5], v74, v74, 1.0
	v_rcp_f32_e32 v76, v75
	v_div_scale_f32 v77, vcc, 1.0, v74, 1.0
	v_fma_f32 v78, -v75, v76, 1.0
	v_fmac_f32_e32 v76, v78, v76
	v_mul_f32_e32 v78, v77, v76
	v_fma_f32 v79, -v75, v78, v77
	v_fmac_f32_e32 v78, v79, v76
	v_fma_f32 v75, -v75, v78, v77
	v_div_fmas_f32 v75, v75, v76, v78
	v_div_fixup_f32 v74, v75, v74, 1.0
	v_pk_mul_f32 v[26:27], v[26:27], v[74:75] op_sel_hi:[1,0]
	v_pk_mul_f32 v[28:29], v[28:29], v[74:75] op_sel_hi:[1,0]
	v_pk_mul_f32 v[26:27], v[10:11], v[26:27]
	v_pk_mul_f32 v[28:29], v[12:13], v[28:29]
	s_waitcnt vmcnt(1)
	v_pk_fma_f32 v[26:27], v[42:43], v[26:27], v[66:67]
	v_pk_fma_f32 v[28:29], v[44:45], v[28:29], v[68:69]
	v_bfe_u32 v42, v26, 16, 1
	v_add3_u32 v26, v26, v42, s41
	v_bfe_u32 v42, v27, 16, 1
	v_lshrrev_b32_e32 v26, 16, v26
	v_add3_u32 v27, v27, v42, s41
	v_and_or_b32 v26, v27, s3, v26
	v_bfe_u32 v27, v28, 16, 1
	v_add3_u32 v27, v28, v27, s41
	v_bfe_u32 v28, v29, 16, 1
	v_pk_mul_f32 v[32:33], v[32:33], v[74:75] op_sel_hi:[1,0]
	v_lshrrev_b32_e32 v27, 16, v27
	v_add3_u32 v28, v29, v28, s41
	v_pk_mul_f32 v[32:33], v[2:3], v[32:33]
	v_and_or_b32 v27, v28, s3, v27
	v_add_co_u32_e32 v28, vcc, s43, v24
	s_waitcnt vmcnt(0)
	v_pk_fma_f32 v[32:33], v[46:47], v[32:33], v[70:71]
	v_addc_co_u32_e32 v29, vcc, -1, v25, vcc
	v_pk_mul_f32 v[30:31], v[30:31], v[74:75] op_sel_hi:[1,0]
	global_store_dwordx2 v[28:29], v[26:27], off offset:-1536
	v_pk_mul_f32 v[30:31], v[4:5], v[30:31]
	v_pk_fma_f32 v[30:31], v[48:49], v[30:31], v[72:73]
	v_cvt_pk_bf16_f32 v26, v32, v33
	v_bfe_u32 v27, v30, 16, 1
	v_pk_mul_f32 v[40:41], v[40:41], v[74:75] op_sel_hi:[1,0]
	v_add3_u32 v27, v30, v27, s41
	v_bfe_u32 v30, v31, 16, 1
	v_pk_mul_f32 v[40:41], v[6:7], v[40:41]
	v_lshrrev_b32_e32 v27, 16, v27
	v_add3_u32 v30, v31, v30, s41
	v_pk_fma_f32 v[40:41], v[50:51], v[40:41], v[58:59]
	v_and_or_b32 v27, v30, s3, v27
	v_pk_mul_f32 v[36:37], v[36:37], v[74:75] op_sel_hi:[1,0]
	global_store_dwordx2 v[28:29], v[26:27], off offset:-1024
	v_pk_mul_f32 v[36:37], v[8:9], v[36:37]
	v_pk_fma_f32 v[36:37], v[52:53], v[36:37], v[60:61]
	v_cvt_pk_bf16_f32 v26, v40, v41
	v_pk_mul_f32 v[34:35], v[34:35], v[74:75] op_sel_hi:[1,0]
	v_pk_mul_f32 v[34:35], v[14:15], v[34:35]
	v_pk_fma_f32 v[34:35], v[54:55], v[34:35], v[62:63]
	v_cvt_pk_bf16_f32 v27, v36, v37
	v_pk_mul_f32 v[38:39], v[38:39], v[74:75] op_sel_hi:[1,0]
	global_store_dwordx2 v[28:29], v[26:27], off offset:-512
	v_pk_mul_f32 v[38:39], v[16:17], v[38:39]
	v_pk_fma_f32 v[38:39], v[56:57], v[38:39], v[64:65]
	v_cvt_pk_bf16_f32 v26, v34, v35
	v_cvt_pk_bf16_f32 v27, v38, v39
	v_lshl_add_u64 v[24:25], v[24:25], 0, s[12:13]
	global_store_dwordx2 v[28:29], v[26:27], off
	s_cbranch_scc0 .LBB0_2019
.LBB0_2017:
	v_add_co_u32_e32 v26, vcc, 0xdca00000, v24
	s_cmpk_lt_i32 s6, 0x400
	s_nop 0
	v_addc_co_u32_e32 v27, vcc, -1, v25, vcc
	global_load_dwordx2 v[28:29], v[26:27], off offset:-1536
	global_load_dwordx2 v[30:31], v[26:27], off offset:-1024
	global_load_dwordx2 v[34:35], v[26:27], off offset:-512
	global_load_dwordx2 v[38:39], v[26:27], off
	s_cselect_b64 s[4:5], -1, 0
	s_cmpk_gt_i32 s6, 0x3ff
	s_waitcnt vmcnt(3)
	v_lshlrev_b32_e32 v26, 16, v28
	v_and_b32_e32 v27, 0xffff0000, v28
	v_lshlrev_b32_e32 v28, 16, v29
	v_and_b32_e32 v29, 0xffff0000, v29
	s_waitcnt vmcnt(2)
	v_lshlrev_b32_e32 v32, 16, v30
	v_and_b32_e32 v33, 0xffff0000, v30
	v_lshlrev_b32_e32 v30, 16, v31
	v_and_b32_e32 v31, 0xffff0000, v31
	s_waitcnt vmcnt(1)
	v_lshlrev_b32_e32 v40, 16, v34
	v_and_b32_e32 v41, 0xffff0000, v34
	v_lshlrev_b32_e32 v36, 16, v35
	v_and_b32_e32 v37, 0xffff0000, v35
	s_waitcnt vmcnt(0)
	v_lshlrev_b32_e32 v34, 16, v38
	v_and_b32_e32 v35, 0xffff0000, v38
	v_lshlrev_b32_e32 v38, 16, v39
	v_and_b32_e32 v39, 0xffff0000, v39
	s_cbranch_scc1 .LBB0_2016
	v_add_co_u32_e32 v68, vcc, 0xfea00000, v24
	v_lshl_add_u64 v[42:43], v[24:25], 0, s[14:15]
	s_nop 0
	v_addc_co_u32_e32 v69, vcc, -1, v25, vcc
	v_add_co_u32_e32 v66, vcc, s7, v24
	global_load_dwordx2 v[46:47], v[68:69], off offset:-1536
	s_nop 0
	v_addc_co_u32_e32 v67, vcc, -1, v25, vcc
	global_load_dwordx2 v[64:65], v[66:67], off offset:-1536
	v_add_co_u32_e32 v60, vcc, s9, v24
	s_waitcnt vmcnt(1)
	v_lshlrev_b32_e32 v74, 16, v46
	v_addc_co_u32_e32 v61, vcc, -1, v25, vcc
	global_load_dwordx2 v[62:63], v[60:61], off offset:-1536
	v_add_co_u32_e32 v54, vcc, s22, v24
	v_and_b32_e32 v75, 0xffff0000, v46
	s_nop 0
	v_addc_co_u32_e32 v55, vcc, -1, v25, vcc
	v_add_co_u32_e32 v50, vcc, s23, v24
	global_load_dwordx2 v[58:59], v[54:55], off offset:-1536
	s_nop 0
	v_addc_co_u32_e32 v51, vcc, -1, v25, vcc
	v_add_co_u32_e32 v48, vcc, s30, v24
	global_load_dwordx2 v[56:57], v[50:51], off offset:-1536
	s_nop 0
	v_addc_co_u32_e32 v49, vcc, -1, v25, vcc
	v_add_co_u32_e32 v76, vcc, s31, v24
	global_load_dwordx2 v[52:53], v[48:49], off offset:-1536
	global_load_dwordx2 v[44:45], v[68:69], off offset:-1024
	global_load_dwordx2 v[70:71], v[68:69], off offset:-512
	s_nop 0
	global_load_dwordx2 v[68:69], v[68:69], off
	v_addc_co_u32_e32 v77, vcc, -1, v25, vcc
	v_add_co_u32_e32 v96, vcc, s33, v24
	global_load_dwordx2 v[86:87], v[76:77], off offset:-1536
	global_load_dwordx2 v[84:85], v[66:67], off offset:-1024
	global_load_dwordx2 v[72:73], v[66:67], off offset:-512
	s_nop 0
	global_load_dwordx2 v[66:67], v[66:67], off
	v_addc_co_u32_e32 v97, vcc, -1, v25, vcc
	v_add_co_u32_e32 v100, vcc, s36, v24
	global_load_dwordx2 v[98:99], v[96:97], off offset:-1536
	s_nop 0
	v_addc_co_u32_e32 v101, vcc, -1, v25, vcc
	v_add_co_u32_e32 v102, vcc, s37, v24
	global_load_dwordx2 v[104:105], v[100:101], off offset:-1536
	s_nop 0
	v_addc_co_u32_e32 v103, vcc, -1, v25, vcc
	v_add_co_u32_e32 v106, vcc, s40, v24
	global_load_dwordx2 v[108:109], v[102:103], off offset:-1536
	s_nop 0
	v_addc_co_u32_e32 v107, vcc, -1, v25, vcc
	v_lshlrev_b32_e32 v46, 16, v47
	v_and_b32_e32 v47, 0xffff0000, v47
	global_load_dwordx2 v[110:111], v[106:107], off offset:-1536
	v_pk_add_f32 v[46:47], v[46:47], 0 op_sel_hi:[1,0]
	s_waitcnt vmcnt(15)
	v_lshlrev_b32_e32 v78, 16, v64
	v_and_b32_e32 v79, 0xffff0000, v64
	v_lshlrev_b32_e32 v64, 16, v65
	v_and_b32_e32 v65, 0xffff0000, v65
	v_pk_add_f32 v[80:81], v[46:47], v[64:65]
	global_load_dwordx2 v[112:113], v[60:61], off offset:-1024
	global_load_dwordx2 v[64:65], v[60:61], off offset:-512
	global_load_dwordx2 v[46:47], v[60:61], off
	global_load_dwordx2 v[114:115], v[24:25], off offset:-1536
	v_pk_add_f32 v[74:75], v[74:75], 0 op_sel_hi:[1,0]
	s_waitcnt vmcnt(18)
	v_lshlrev_b32_e32 v60, 16, v62
	v_pk_add_f32 v[74:75], v[74:75], v[78:79]
	v_and_b32_e32 v61, 0xffff0000, v62
	v_pk_add_f32 v[60:61], v[74:75], v[60:61]
	global_load_dwordx4 v[92:95], v[22:23], off
	global_load_dwordx2 v[116:117], v[54:55], off offset:-1024
	global_load_dwordx2 v[74:75], v[54:55], off offset:-512
	s_nop 0
	global_load_dwordx2 v[54:55], v[54:55], off
	v_lshlrev_b32_e32 v62, 16, v63
	v_and_b32_e32 v63, 0xffff0000, v63
	v_pk_add_f32 v[62:63], v[80:81], v[62:63]
	s_waitcnt vmcnt(21)
	v_lshlrev_b32_e32 v78, 16, v58
	v_and_b32_e32 v79, 0xffff0000, v58
	v_lshlrev_b32_e32 v58, 16, v59
	v_and_b32_e32 v59, 0xffff0000, v59
	v_pk_add_f32 v[58:59], v[62:63], v[58:59]
	v_pk_add_f32 v[60:61], v[60:61], v[78:79]
	s_waitcnt vmcnt(20)
	v_lshlrev_b32_e32 v62, 16, v56
	v_and_b32_e32 v63, 0xffff0000, v56
	v_lshlrev_b32_e32 v56, 16, v57
	v_and_b32_e32 v57, 0xffff0000, v57
	v_pk_add_f32 v[60:61], v[60:61], v[62:63]
	v_pk_add_f32 v[56:57], v[58:59], v[56:57]
	s_waitcnt vmcnt(19)
	v_lshlrev_b32_e32 v58, 16, v52
	v_and_b32_e32 v59, 0xffff0000, v52
	v_lshlrev_b32_e32 v52, 16, v53
	v_and_b32_e32 v53, 0xffff0000, v53
	v_pk_add_f32 v[56:57], v[56:57], v[52:53]
	v_pk_add_f32 v[58:59], v[60:61], v[58:59]
	s_waitcnt vmcnt(15)
	v_lshlrev_b32_e32 v60, 16, v86
	v_and_b32_e32 v61, 0xffff0000, v86
	v_lshlrev_b32_e32 v62, 16, v87
	v_and_b32_e32 v63, 0xffff0000, v87
	global_load_dwordx2 v[118:119], v[50:51], off offset:-1024
	global_load_dwordx2 v[78:79], v[50:51], off offset:-512
	s_nop 0
	global_load_dwordx2 v[50:51], v[50:51], off
	s_nop 0
	global_load_dwordx2 v[120:121], v[48:49], off offset:-1024
	global_load_dwordx2 v[80:81], v[48:49], off offset:-512
	s_nop 0
	global_load_dwordx2 v[48:49], v[48:49], off
	s_nop 0
	global_load_dwordx2 v[122:123], v[76:77], off offset:-1024
	global_load_dwordx2 v[82:83], v[76:77], off offset:-512
	global_load_dwordx2 v[52:53], v[76:77], off
	v_pk_add_f32 v[58:59], v[58:59], v[60:61]
	v_pk_add_f32 v[60:61], v[56:57], v[62:63]
	s_waitcnt vmcnt(20)
	v_lshlrev_b32_e32 v62, 16, v98
	v_and_b32_e32 v63, 0xffff0000, v98
	v_lshlrev_b32_e32 v76, 16, v99
	v_and_b32_e32 v77, 0xffff0000, v99
	global_load_dwordx2 v[124:125], v[96:97], off offset:-1024
	global_load_dwordx2 v[86:87], v[96:97], off offset:-512
	global_load_dwordx2 v[56:57], v[96:97], off
	v_pk_add_f32 v[60:61], v[60:61], v[76:77]
	v_pk_add_f32 v[62:63], v[58:59], v[62:63]
	global_load_dwordx2 v[96:97], v[100:101], off offset:-1024
	global_load_dwordx2 v[98:99], v[100:101], off offset:-512
	global_load_dwordx2 v[58:59], v[100:101], off
	s_waitcnt vmcnt(25)
	v_lshlrev_b32_e32 v76, 16, v104
	v_and_b32_e32 v77, 0xffff0000, v104
	v_lshlrev_b32_e32 v100, 16, v105
	v_and_b32_e32 v101, 0xffff0000, v105
	v_pk_add_f32 v[62:63], v[62:63], v[76:77]
	v_pk_add_f32 v[76:77], v[60:61], v[100:101]
	global_load_dwordx2 v[100:101], v[102:103], off offset:-1024
	global_load_dwordx2 v[104:105], v[102:103], off offset:-512
	global_load_dwordx2 v[60:61], v[102:103], off
	s_waitcnt vmcnt(27)
	v_lshlrev_b32_e32 v102, 16, v108
	v_and_b32_e32 v103, 0xffff0000, v108
	v_lshlrev_b32_e32 v108, 16, v109
	v_and_b32_e32 v109, 0xffff0000, v109
	v_pk_add_f32 v[76:77], v[76:77], v[108:109]
	v_pk_add_f32 v[102:103], v[62:63], v[102:103]
	global_load_dwordx2 v[108:109], v[106:107], off offset:-1024
	global_load_dwordx2 v[126:127], v[106:107], off offset:-512
	global_load_dwordx2 v[62:63], v[106:107], off
	s_waitcnt vmcnt(29)
	v_lshlrev_b32_e32 v106, 16, v110
	v_and_b32_e32 v107, 0xffff0000, v110
	v_lshlrev_b32_e32 v110, 16, v111
	v_and_b32_e32 v111, 0xffff0000, v111
	v_pk_add_f32 v[102:103], v[102:103], v[106:107]
	s_waitcnt vmcnt(25)
	v_lshlrev_b32_e32 v130, 16, v114
	v_and_b32_e32 v131, 0xffff0000, v114
	v_pk_add_f32 v[106:107], v[76:77], v[110:111]
	v_lshlrev_b32_e32 v114, 16, v115
	v_and_b32_e32 v115, 0xffff0000, v115
	v_pk_add_f32 v[102:103], v[102:103], v[130:131]
	v_pk_add_f32 v[106:107], v[106:107], v[114:115]
	global_load_dwordx2 v[110:111], v[24:25], off offset:-1024
	global_load_dwordx2 v[128:129], v[24:25], off offset:-512
	global_load_dwordx2 v[76:77], v[24:25], off
	v_lshlrev_b32_e32 v114, 16, v44
	v_and_b32_e32 v115, 0xffff0000, v44
	v_lshlrev_b32_e32 v44, 16, v45
	v_and_b32_e32 v45, 0xffff0000, v45
	v_pk_add_f32 v[44:45], v[44:45], 0 op_sel_hi:[1,0]
	v_pk_add_f32 v[114:115], v[114:115], 0 op_sel_hi:[1,0]
	v_lshlrev_b32_e32 v130, 16, v84
	v_and_b32_e32 v131, 0xffff0000, v84
	v_lshlrev_b32_e32 v84, 16, v85
	v_and_b32_e32 v85, 0xffff0000, v85
	v_pk_add_f32 v[114:115], v[114:115], v[130:131]
	s_waitcnt vmcnt(27)
	v_pk_fma_f32 v[26:27], v[102:103], v[92:93], v[26:27]
	v_pk_fma_f32 v[28:29], v[106:107], v[94:95], v[28:29]
	v_bfe_u32 v92, v26, 16, 1
	v_add3_u32 v26, v26, v92, s41
	v_bfe_u32 v92, v27, 16, 1
	v_and_b32_sdwa v94, v29, v91 dst_sel:DWORD dst_unused:UNUSED_PAD src0_sel:WORD_1 src1_sel:DWORD
	v_add3_u32 v27, v27, v92, s41
	v_bfe_u32 v93, v28, 16, 1
	v_add3_u32 v29, v29, v94, s41
	v_and_b32_e32 v27, 0xffff0000, v27
	v_add3_u32 v93, v28, v93, s41
	v_and_b32_e32 v29, 0xffff0000, v29
	v_or_b32_sdwa v92, v27, v26 dst_sel:DWORD dst_unused:UNUSED_PAD src0_sel:DWORD src1_sel:WORD_1
	v_or_b32_sdwa v93, v29, v93 dst_sel:DWORD dst_unused:UNUSED_PAD src0_sel:DWORD src1_sel:WORD_1
	global_store_dwordx2 v[42:43], v[92:93], off
	global_load_dwordx4 v[92:95], v[22:23], off offset:1024
	v_pk_add_f32 v[44:45], v[44:45], v[84:85]
	v_lshlrev_b32_e32 v84, 16, v112
	v_and_b32_e32 v85, 0xffff0000, v112
	v_lshlrev_b32_e32 v112, 16, v113
	v_and_b32_e32 v113, 0xffff0000, v113
	v_pk_add_f32 v[44:45], v[44:45], v[112:113]
	v_pk_add_f32 v[84:85], v[114:115], v[84:85]
	s_waitcnt vmcnt(28)
	v_lshlrev_b32_e32 v112, 16, v116
	v_and_b32_e32 v113, 0xffff0000, v116
	v_lshlrev_b32_e32 v114, 16, v117
	v_and_b32_e32 v115, 0xffff0000, v117
	v_pk_add_f32 v[84:85], v[84:85], v[112:113]
	v_pk_add_f32 v[44:45], v[44:45], v[114:115]
	s_waitcnt vmcnt(25)
	v_lshlrev_b32_e32 v112, 16, v118
	v_and_b32_e32 v113, 0xffff0000, v118
	v_lshlrev_b32_e32 v114, 16, v119
	v_and_b32_e32 v115, 0xffff0000, v119
	v_pk_add_f32 v[44:45], v[44:45], v[114:115]
	v_pk_add_f32 v[84:85], v[84:85], v[112:113]
	s_waitcnt vmcnt(22)
	v_lshlrev_b32_e32 v112, 16, v120
	v_and_b32_e32 v113, 0xffff0000, v120
	v_lshlrev_b32_e32 v114, 16, v121
	v_and_b32_e32 v115, 0xffff0000, v121
	v_pk_add_f32 v[84:85], v[84:85], v[112:113]
	v_pk_add_f32 v[44:45], v[44:45], v[114:115]
	s_waitcnt vmcnt(19)
	v_lshlrev_b32_e32 v112, 16, v122
	v_and_b32_e32 v113, 0xffff0000, v122
	v_lshlrev_b32_e32 v114, 16, v123
	v_and_b32_e32 v115, 0xffff0000, v123
	v_pk_add_f32 v[44:45], v[44:45], v[114:115]
	v_pk_add_f32 v[84:85], v[84:85], v[112:113]
	s_waitcnt vmcnt(16)
	v_lshlrev_b32_e32 v112, 16, v124
	v_and_b32_e32 v113, 0xffff0000, v124
	v_lshlrev_b32_e32 v114, 16, v125
	v_and_b32_e32 v115, 0xffff0000, v125
	v_pk_add_f32 v[84:85], v[84:85], v[112:113]
	v_pk_add_f32 v[44:45], v[44:45], v[114:115]
	s_waitcnt vmcnt(13)
	v_lshlrev_b32_e32 v112, 16, v96
	v_and_b32_e32 v113, 0xffff0000, v96
	v_lshlrev_b32_e32 v96, 16, v97
	v_and_b32_e32 v97, 0xffff0000, v97
	v_pk_add_f32 v[44:45], v[44:45], v[96:97]
	v_pk_add_f32 v[84:85], v[84:85], v[112:113]
	s_waitcnt vmcnt(10)
	v_lshlrev_b32_e32 v96, 16, v100
	v_and_b32_e32 v97, 0xffff0000, v100
	v_lshlrev_b32_e32 v100, 16, v101
	v_and_b32_e32 v101, 0xffff0000, v101
	v_pk_add_f32 v[84:85], v[84:85], v[96:97]
	s_waitcnt vmcnt(7)
	v_lshlrev_b32_e32 v96, 16, v108
	v_and_b32_e32 v97, 0xffff0000, v108
	v_pk_add_f32 v[44:45], v[44:45], v[100:101]
	v_lshlrev_b32_e32 v100, 16, v109
	v_and_b32_e32 v101, 0xffff0000, v109
	v_pk_add_f32 v[84:85], v[84:85], v[96:97]
	s_waitcnt vmcnt(4)
	v_lshlrev_b32_e32 v96, 16, v110
	v_and_b32_e32 v97, 0xffff0000, v110
	v_pk_add_f32 v[44:45], v[44:45], v[100:101]
	v_lshlrev_b32_e32 v100, 16, v111
	v_and_b32_e32 v101, 0xffff0000, v111
	v_pk_add_f32 v[84:85], v[84:85], v[96:97]
	v_pk_add_f32 v[44:45], v[44:45], v[100:101]
	v_lshl_add_u64 v[102:103], v[24:25], 0, s[16:17]
	v_lshl_add_u64 v[106:107], v[24:25], 0, s[18:19]
	v_and_b32_sdwa v96, v28, v91 dst_sel:DWORD dst_unused:UNUSED_PAD src0_sel:WORD_1 src1_sel:DWORD
	v_add3_u32 v28, v28, v96, s41
	v_lshl_add_u64 v[42:43], v[24:25], 0, s[20:21]
	v_and_b32_e32 v26, 0xffff0000, v26
	v_and_b32_e32 v28, 0xffff0000, v28
	s_waitcnt vmcnt(0)
	v_pk_fma_f32 v[32:33], v[84:85], v[92:93], v[32:33]
	v_pk_fma_f32 v[30:31], v[44:45], v[94:95], v[30:31]
	v_and_b32_sdwa v92, v31, v91 dst_sel:DWORD dst_unused:UNUSED_PAD src0_sel:WORD_1 src1_sel:DWORD
	v_cvt_pk_bf16_f32 v44, v32, v33
	v_bfe_u32 v45, v30, 16, 1
	v_add3_u32 v31, v31, v92, s41
	v_add3_u32 v45, v30, v45, s41
	v_and_b32_e32 v31, 0xffff0000, v31
	v_or_b32_sdwa v45, v31, v45 dst_sel:DWORD dst_unused:UNUSED_PAD src0_sel:DWORD src1_sel:WORD_1
	global_store_dwordx2 v[102:103], v[44:45], off
	global_load_dwordx4 v[92:95], v[22:23], off offset:2048
	v_and_b32_sdwa v84, v33, v91 dst_sel:DWORD dst_unused:UNUSED_PAD src0_sel:WORD_1 src1_sel:DWORD
	v_and_b32_sdwa v85, v32, v91 dst_sel:DWORD dst_unused:UNUSED_PAD src0_sel:WORD_1 src1_sel:DWORD
	v_lshlrev_b32_e32 v44, 16, v70
	v_and_b32_e32 v45, 0xffff0000, v70
	v_lshlrev_b32_e32 v70, 16, v71
	v_and_b32_e32 v71, 0xffff0000, v71
	v_add3_u32 v33, v33, v84, s41
	v_add3_u32 v32, v32, v85, s41
	v_pk_add_f32 v[70:71], v[70:71], 0 op_sel_hi:[1,0]
	v_pk_add_f32 v[44:45], v[44:45], 0 op_sel_hi:[1,0]
	v_lshlrev_b32_e32 v84, 16, v72
	v_and_b32_e32 v85, 0xffff0000, v72
	v_lshlrev_b32_e32 v72, 16, v73
	v_and_b32_e32 v73, 0xffff0000, v73
	v_pk_add_f32 v[44:45], v[44:45], v[84:85]
	v_pk_add_f32 v[70:71], v[70:71], v[72:73]
	v_lshlrev_b32_e32 v72, 16, v64
	v_and_b32_e32 v73, 0xffff0000, v64
	v_lshlrev_b32_e32 v64, 16, v65
	v_and_b32_e32 v65, 0xffff0000, v65
	v_pk_add_f32 v[64:65], v[70:71], v[64:65]
	v_pk_add_f32 v[44:45], v[44:45], v[72:73]
	v_lshlrev_b32_e32 v70, 16, v74
	v_and_b32_e32 v71, 0xffff0000, v74
	v_pk_add_f32 v[44:45], v[44:45], v[70:71]
	v_lshlrev_b32_e32 v70, 16, v78
	v_and_b32_e32 v71, 0xffff0000, v78
	v_lshlrev_b32_e32 v72, 16, v75
	v_and_b32_e32 v73, 0xffff0000, v75
	v_pk_add_f32 v[44:45], v[44:45], v[70:71]
	v_lshlrev_b32_e32 v70, 16, v80
	v_and_b32_e32 v71, 0xffff0000, v80
	v_pk_add_f32 v[64:65], v[64:65], v[72:73]
	v_lshlrev_b32_e32 v72, 16, v79
	v_and_b32_e32 v73, 0xffff0000, v79
	v_pk_add_f32 v[44:45], v[44:45], v[70:71]
	v_lshlrev_b32_e32 v70, 16, v82
	v_and_b32_e32 v71, 0xffff0000, v82
	v_pk_add_f32 v[64:65], v[64:65], v[72:73]
	v_lshlrev_b32_e32 v72, 16, v81
	v_and_b32_e32 v73, 0xffff0000, v81
	v_pk_add_f32 v[44:45], v[44:45], v[70:71]
	v_lshlrev_b32_e32 v70, 16, v86
	v_and_b32_e32 v71, 0xffff0000, v86
	v_pk_add_f32 v[64:65], v[64:65], v[72:73]
	v_lshlrev_b32_e32 v72, 16, v83
	v_and_b32_e32 v73, 0xffff0000, v83
	v_pk_add_f32 v[44:45], v[44:45], v[70:71]
	v_lshlrev_b32_e32 v70, 16, v98
	v_and_b32_e32 v71, 0xffff0000, v98
	v_pk_add_f32 v[64:65], v[64:65], v[72:73]
	v_lshlrev_b32_e32 v72, 16, v87
	v_and_b32_e32 v73, 0xffff0000, v87
	v_pk_add_f32 v[44:45], v[44:45], v[70:71]
	v_lshlrev_b32_e32 v70, 16, v104
	v_and_b32_e32 v71, 0xffff0000, v104
	v_pk_add_f32 v[64:65], v[64:65], v[72:73]
	v_lshlrev_b32_e32 v72, 16, v99
	v_and_b32_e32 v73, 0xffff0000, v99
	v_pk_add_f32 v[44:45], v[44:45], v[70:71]
	v_lshlrev_b32_e32 v70, 16, v126
	v_and_b32_e32 v71, 0xffff0000, v126
	v_pk_add_f32 v[64:65], v[64:65], v[72:73]
	v_lshlrev_b32_e32 v72, 16, v105
	v_and_b32_e32 v73, 0xffff0000, v105
	v_pk_add_f32 v[44:45], v[44:45], v[70:71]
	v_lshlrev_b32_e32 v70, 16, v128
	v_and_b32_e32 v71, 0xffff0000, v128
	v_pk_add_f32 v[64:65], v[64:65], v[72:73]
	v_lshlrev_b32_e32 v72, 16, v127
	v_and_b32_e32 v73, 0xffff0000, v127
	v_pk_add_f32 v[44:45], v[44:45], v[70:71]
	v_pk_add_f32 v[64:65], v[64:65], v[72:73]
	v_lshlrev_b32_e32 v72, 16, v129
	v_and_b32_e32 v73, 0xffff0000, v129
	v_pk_add_f32 v[64:65], v[64:65], v[72:73]
	v_and_b32_sdwa v70, v30, v91 dst_sel:DWORD dst_unused:UNUSED_PAD src0_sel:WORD_1 src1_sel:DWORD
	v_add3_u32 v30, v30, v70, s41
	v_and_b32_e32 v33, 0xffff0000, v33
	s_waitcnt vmcnt(0)
	v_pk_fma_f32 v[40:41], v[44:45], v[92:93], v[40:41]
	v_pk_fma_f32 v[36:37], v[64:65], v[94:95], v[36:37]
	v_and_b32_sdwa v70, v37, v91 dst_sel:DWORD dst_unused:UNUSED_PAD src0_sel:WORD_1 src1_sel:DWORD
	v_cvt_pk_bf16_f32 v44, v40, v41
	v_bfe_u32 v45, v36, 16, 1
	v_add3_u32 v37, v37, v70, s41
	v_add3_u32 v45, v36, v45, s41
	v_and_b32_e32 v37, 0xffff0000, v37
	v_or_b32_sdwa v45, v37, v45 dst_sel:DWORD dst_unused:UNUSED_PAD src0_sel:DWORD src1_sel:WORD_1
	global_store_dwordx2 v[106:107], v[44:45], off
	global_load_dwordx4 v[70:73], v[22:23], off offset:3072
	v_and_b32_sdwa v64, v41, v91 dst_sel:DWORD dst_unused:UNUSED_PAD src0_sel:WORD_1 src1_sel:DWORD
	v_and_b32_sdwa v65, v40, v91 dst_sel:DWORD dst_unused:UNUSED_PAD src0_sel:WORD_1 src1_sel:DWORD
	v_add3_u32 v41, v41, v64, s41
	v_add3_u32 v40, v40, v65, s41
	v_lshlrev_b32_e32 v44, 16, v68
	v_and_b32_e32 v45, 0xffff0000, v68
	v_lshlrev_b32_e32 v64, 16, v69
	v_and_b32_e32 v65, 0xffff0000, v69
	v_pk_add_f32 v[64:65], v[64:65], 0 op_sel_hi:[1,0]
	v_pk_add_f32 v[44:45], v[44:45], 0 op_sel_hi:[1,0]
	v_lshlrev_b32_e32 v68, 16, v66
	v_and_b32_e32 v69, 0xffff0000, v66
	v_lshlrev_b32_e32 v66, 16, v67
	v_and_b32_e32 v67, 0xffff0000, v67
	v_pk_add_f32 v[44:45], v[44:45], v[68:69]
	v_pk_add_f32 v[64:65], v[64:65], v[66:67]
	v_lshlrev_b32_e32 v66, 16, v46
	v_and_b32_e32 v67, 0xffff0000, v46
	v_lshlrev_b32_e32 v46, 16, v47
	v_and_b32_e32 v47, 0xffff0000, v47
	v_pk_add_f32 v[46:47], v[64:65], v[46:47]
	v_pk_add_f32 v[44:45], v[44:45], v[66:67]
	v_lshlrev_b32_e32 v64, 16, v54
	v_and_b32_e32 v65, 0xffff0000, v54
	v_lshlrev_b32_e32 v54, 16, v55
	v_and_b32_e32 v55, 0xffff0000, v55
	v_pk_add_f32 v[44:45], v[44:45], v[64:65]
	v_pk_add_f32 v[46:47], v[46:47], v[54:55]
	v_lshlrev_b32_e32 v54, 16, v50
	v_and_b32_e32 v55, 0xffff0000, v50
	v_lshlrev_b32_e32 v50, 16, v51
	v_and_b32_e32 v51, 0xffff0000, v51
	v_pk_add_f32 v[46:47], v[46:47], v[50:51]
	v_pk_add_f32 v[44:45], v[44:45], v[54:55]
	v_lshlrev_b32_e32 v50, 16, v48
	v_and_b32_e32 v51, 0xffff0000, v48
	v_lshlrev_b32_e32 v48, 16, v49
	v_and_b32_e32 v49, 0xffff0000, v49
	v_pk_add_f32 v[44:45], v[44:45], v[50:51]
	v_pk_add_f32 v[46:47], v[46:47], v[48:49]
	v_lshlrev_b32_e32 v48, 16, v52
	v_and_b32_e32 v49, 0xffff0000, v52
	v_pk_add_f32 v[44:45], v[44:45], v[48:49]
	v_lshlrev_b32_e32 v48, 16, v56
	v_and_b32_e32 v49, 0xffff0000, v56
	v_lshlrev_b32_e32 v50, 16, v53
	v_and_b32_e32 v51, 0xffff0000, v53
	v_pk_add_f32 v[44:45], v[44:45], v[48:49]
	v_lshlrev_b32_e32 v48, 16, v58
	v_and_b32_e32 v49, 0xffff0000, v58
	v_pk_add_f32 v[46:47], v[46:47], v[50:51]
	v_lshlrev_b32_e32 v50, 16, v57
	v_and_b32_e32 v51, 0xffff0000, v57
	v_pk_add_f32 v[44:45], v[44:45], v[48:49]
	v_lshlrev_b32_e32 v48, 16, v60
	v_and_b32_e32 v49, 0xffff0000, v60
	v_pk_add_f32 v[46:47], v[46:47], v[50:51]
	v_lshlrev_b32_e32 v50, 16, v59
	v_and_b32_e32 v51, 0xffff0000, v59
	v_pk_add_f32 v[44:45], v[44:45], v[48:49]
	v_lshlrev_b32_e32 v48, 16, v62
	v_and_b32_e32 v49, 0xffff0000, v62
	v_pk_add_f32 v[46:47], v[46:47], v[50:51]
	v_lshlrev_b32_e32 v50, 16, v61
	v_and_b32_e32 v51, 0xffff0000, v61
	v_pk_add_f32 v[44:45], v[44:45], v[48:49]
	v_lshlrev_b32_e32 v48, 16, v76
	v_and_b32_e32 v49, 0xffff0000, v76
	v_pk_add_f32 v[46:47], v[46:47], v[50:51]
	v_lshlrev_b32_e32 v50, 16, v63
	v_and_b32_e32 v51, 0xffff0000, v63
	v_pk_add_f32 v[44:45], v[44:45], v[48:49]
	v_pk_add_f32 v[46:47], v[46:47], v[50:51]
	v_lshlrev_b32_e32 v50, 16, v77
	v_and_b32_e32 v51, 0xffff0000, v77
	v_pk_add_f32 v[46:47], v[46:47], v[50:51]
	v_and_b32_sdwa v48, v36, v91 dst_sel:DWORD dst_unused:UNUSED_PAD src0_sel:WORD_1 src1_sel:DWORD
	v_add3_u32 v36, v36, v48, s41
	v_and_b32_e32 v32, 0xffff0000, v32
	s_waitcnt vmcnt(0)
	v_pk_fma_f32 v[34:35], v[44:45], v[70:71], v[34:35]
	v_pk_fma_f32 v[38:39], v[46:47], v[72:73], v[38:39]
	v_bfe_u32 v44, v34, 16, 1
	v_add3_u32 v44, v34, v44, s41
	v_bfe_u32 v45, v35, 16, 1
	v_and_b32_sdwa v46, v35, v91 dst_sel:DWORD dst_unused:UNUSED_PAD src0_sel:WORD_1 src1_sel:DWORD
	v_lshrrev_b32_e32 v44, 16, v44
	v_add3_u32 v45, v35, v45, s41
	v_and_b32_sdwa v47, v34, v91 dst_sel:DWORD dst_unused:UNUSED_PAD src0_sel:WORD_1 src1_sel:DWORD
	v_add3_u32 v35, v35, v46, s41
	v_and_b32_sdwa v46, v39, v91 dst_sel:DWORD dst_unused:UNUSED_PAD src0_sel:WORD_1 src1_sel:DWORD
	v_and_or_b32 v44, v45, s3, v44
	v_bfe_u32 v45, v38, 16, 1
	v_add3_u32 v34, v34, v47, s41
	v_and_b32_sdwa v47, v38, v91 dst_sel:DWORD dst_unused:UNUSED_PAD src0_sel:WORD_1 src1_sel:DWORD
	v_add3_u32 v39, v39, v46, s41
	v_add3_u32 v45, v38, v45, s41
	v_add3_u32 v38, v38, v47, s41
	v_and_b32_e32 v39, 0xffff0000, v39
	v_and_b32_e32 v30, 0xffff0000, v30
	v_and_b32_e32 v41, 0xffff0000, v41
	v_and_b32_e32 v40, 0xffff0000, v40
	v_and_b32_e32 v36, 0xffff0000, v36
	v_and_b32_e32 v35, 0xffff0000, v35
	v_and_b32_e32 v34, 0xffff0000, v34
	v_and_b32_e32 v38, 0xffff0000, v38
	v_or_b32_sdwa v45, v39, v45 dst_sel:DWORD dst_unused:UNUSED_PAD src0_sel:DWORD src1_sel:WORD_1
	global_store_dwordx2 v[42:43], v[44:45], off
	s_branch .LBB0_2016

.LBB0_2231:
	v_pk_mul_f32 v[62:63], v[32:33], v[32:33]
	v_pk_mul_f32 v[64:65], v[30:31], v[30:31]
	v_pk_mul_f32 v[58:59], v[34:35], v[34:35]
	v_pk_mul_f32 v[60:61], v[38:39], v[38:39]
	v_pk_mov_b32 v[66:67], v[64:65], v[62:63] op_sel:[1,0]
	v_mov_b32_e32 v65, v63
	v_pk_add_f32 v[62:63], v[66:67], v[64:65]
	v_pk_mov_b32 v[64:65], v[60:61], v[58:59] op_sel:[1,0]
	v_mov_b32_e32 v61, v59
	v_pk_add_f32 v[58:59], v[64:65], v[60:61]
	s_add_i32 s10, s6, 0xfffffc00
	v_pk_add_f32 v[58:59], v[58:59], v[58:59] op_sel_hi:[0,1]
	v_mul_f32_e32 v58, v44, v44
	s_lshr_b32 s10, s10, 12
	v_pk_fma_f32 v[60:61], v[44:45], v[44:45], v[58:59] op_sel_hi:[1,1,0]
	v_mul_f32_e32 v58, v40, v40
	s_mulk_i32 s10, 0x1800
	s_and_b64 s[4:5], s[4:5], exec
	v_pk_add_f32 v[62:63], v[62:63], v[62:63] op_sel_hi:[0,1]
	v_pk_fma_f32 v[64:65], v[40:41], v[40:41], v[58:59] op_sel_hi:[1,1,0]
	s_cselect_b32 s10, 0x6000, s10
	v_mul_f32_e32 v60, v36, v36
	v_mul_f32_e32 v64, v37, v37
	v_mul_f32_e32 v62, v42, v42
	v_mul_f32_e32 v58, v43, v43
	s_lshl_b64 s[4:5], s[10:11], 2
	v_pk_add_f32 v[66:67], v[60:61], v[64:65]
	v_pk_add_f32 v[68:69], v[62:63], v[58:59]
	v_lshl_add_u64 v[54:55], v[24:25], 0, s[4:5]
	v_lshl_add_u64 v[70:71], v[22:23], 0, s[4:5]
	v_pk_add_f32 v[66:67], v[66:67], v[68:69]
	global_load_dwordx4 v[18:21], v[54:55], off
	global_load_dwordx4 v[46:49], v[54:55], off offset:1024
	global_load_dwordx4 v[50:53], v[54:55], off offset:2048
	s_nop 0
	global_load_dwordx4 v[54:57], v[54:55], off offset:3072
	s_nop 0
	global_load_dwordx4 v[58:61], v[70:71], off offset:2048
	global_load_dwordx4 v[62:65], v[70:71], off offset:3072
	v_add_f32_e32 v74, v66, v67
	global_load_dwordx4 v[66:69], v[70:71], off
	s_nop 0
	global_load_dwordx4 v[70:73], v[70:71], off offset:1024
	v_add_f32_dpp v74, v74, v74 row_ror:8 row_mask:0xf bank_mask:0xf bound_ctrl:1
	s_add_i32 s6, s6, s8
	s_cmpk_lt_i32 s6, 0x4400
	v_add_f32_dpp v74, v74, v74 row_ror:4 row_mask:0xf bank_mask:0xf bound_ctrl:1
	s_waitcnt vmcnt(7)
	v_pk_add_f32 v[18:19], v[18:19], 1.0 op_sel_hi:[1,0]
	v_add_f32_dpp v74, v74, v74 row_ror:2 row_mask:0xf bank_mask:0xf bound_ctrl:1
	v_pk_add_f32 v[20:21], v[20:21], 1.0 op_sel_hi:[1,0]
	s_waitcnt vmcnt(6)
	v_pk_add_f32 v[46:47], v[46:47], 1.0 op_sel_hi:[1,0]
	v_add_f32_dpp v74, v74, v74 row_ror:1 row_mask:0xf bank_mask:0xf bound_ctrl:1
	ds_bpermute_b32 v75, v1, v74
	v_pk_add_f32 v[48:49], v[48:49], 1.0 op_sel_hi:[1,0]
	s_waitcnt vmcnt(5)
	v_pk_add_f32 v[50:51], v[50:51], 1.0 op_sel_hi:[1,0]
	v_pk_add_f32 v[52:53], v[52:53], 1.0 op_sel_hi:[1,0]
	s_waitcnt vmcnt(4)
	v_pk_add_f32 v[54:55], v[54:55], 1.0 op_sel_hi:[1,0]
	s_waitcnt lgkmcnt(0)
	v_add_f32_e32 v74, v74, v75
	ds_bpermute_b32 v75, v94, v74
	v_pk_add_f32 v[56:57], v[56:57], 1.0 op_sel_hi:[1,0]
	s_waitcnt lgkmcnt(0)
	v_add_f32_e32 v74, v74, v75
	v_fmamk_f32 v74, v74, 0x3a800000, v95
	v_mul_f32_e32 v75, 0x4f800000, v74
	v_cmp_gt_f32_e32 vcc, s41, v74
	s_nop 1
	v_cndmask_b32_e32 v74, v74, v75, vcc
	v_sqrt_f32_e32 v75, v74
	s_nop 0
	v_add_u32_e32 v76, -1, v75
	v_add_u32_e32 v77, 1, v75
	v_fma_f32 v78, -v76, v75, v74
	v_fma_f32 v79, -v77, v75, v74
	v_cmp_ge_f32_e64 s[4:5], 0, v78
	s_nop 1
	v_cndmask_b32_e64 v75, v75, v76, s[4:5]
	v_cmp_lt_f32_e64 s[4:5], 0, v79
	s_nop 1
	v_cndmask_b32_e64 v75, v75, v77, s[4:5]
	v_mul_f32_e32 v76, 0x37800000, v75
	v_cndmask_b32_e32 v75, v75, v76, vcc
	v_cmp_class_f32_e32 vcc, v74, v96
	s_nop 1
	v_cndmask_b32_e32 v74, v75, v74, vcc
	v_div_scale_f32 v75, s[4:5], v74, v74, 1.0
	v_rcp_f32_e32 v76, v75
	v_div_scale_f32 v77, vcc, 1.0, v74, 1.0
	v_fma_f32 v78, -v75, v76, 1.0
	v_fmac_f32_e32 v76, v78, v76
	v_mul_f32_e32 v78, v77, v76
	v_fma_f32 v79, -v75, v78, v77
	v_fmac_f32_e32 v78, v79, v76
	v_fma_f32 v75, -v75, v78, v77
	v_div_fmas_f32 v75, v75, v76, v78
	v_div_fixup_f32 v74, v75, v74, 1.0
	v_pk_mul_f32 v[30:31], v[30:31], v[74:75] op_sel_hi:[1,0]
	v_pk_mul_f32 v[32:33], v[32:33], v[74:75] op_sel_hi:[1,0]
	v_pk_mul_f32 v[30:31], v[10:11], v[30:31]
	v_pk_mul_f32 v[32:33], v[12:13], v[32:33]
	s_waitcnt vmcnt(1)
	v_pk_fma_f32 v[18:19], v[18:19], v[30:31], v[66:67]
	v_pk_fma_f32 v[20:21], v[20:21], v[32:33], v[68:69]
	v_bfe_u32 v30, v18, 16, 1
	v_add3_u32 v18, v18, v30, s40
	v_bfe_u32 v30, v19, 16, 1
	v_lshrrev_b32_e32 v18, 16, v18
	v_add3_u32 v19, v19, v30, s40
	v_and_or_b32 v18, v19, s3, v18
	v_bfe_u32 v19, v20, 16, 1
	v_add3_u32 v19, v20, v19, s40
	v_bfe_u32 v20, v21, 16, 1
	v_pk_mul_f32 v[38:39], v[38:39], v[74:75] op_sel_hi:[1,0]
	v_lshrrev_b32_e32 v19, 16, v19
	v_add3_u32 v20, v21, v20, s40
	v_pk_mul_f32 v[38:39], v[2:3], v[38:39]
	v_and_or_b32 v19, v20, s3, v19
	v_add_co_u32_e32 v20, vcc, s42, v28
	s_waitcnt vmcnt(0)
	v_pk_fma_f32 v[38:39], v[46:47], v[38:39], v[70:71]
	v_addc_co_u32_e32 v21, vcc, -1, v29, vcc
	v_pk_mul_f32 v[34:35], v[34:35], v[74:75] op_sel_hi:[1,0]
	global_store_dwordx2 v[20:21], v[18:19], off offset:-1536
	v_pk_mul_f32 v[34:35], v[4:5], v[34:35]
	v_pk_fma_f32 v[34:35], v[48:49], v[34:35], v[72:73]
	v_cvt_pk_bf16_f32 v18, v38, v39
	v_pk_mul_f32 v[44:45], v[44:45], v[74:75] op_sel_hi:[1,0]
	v_pk_mul_f32 v[44:45], v[6:7], v[44:45]
	v_pk_fma_f32 v[44:45], v[50:51], v[44:45], v[58:59]
	v_cvt_pk_bf16_f32 v19, v34, v35
	v_pk_mul_f32 v[40:41], v[40:41], v[74:75] op_sel_hi:[1,0]
	global_store_dwordx2 v[20:21], v[18:19], off offset:-1024
	v_pk_mul_f32 v[40:41], v[8:9], v[40:41]
	v_pk_fma_f32 v[40:41], v[52:53], v[40:41], v[60:61]
	v_cvt_pk_bf16_f32 v18, v44, v45
	v_pk_mul_f32 v[36:37], v[36:37], v[74:75] op_sel_hi:[1,0]
	v_pk_mul_f32 v[36:37], v[14:15], v[36:37]
	v_pk_fma_f32 v[36:37], v[54:55], v[36:37], v[62:63]
	v_cvt_pk_bf16_f32 v19, v40, v41
	v_pk_mul_f32 v[42:43], v[42:43], v[74:75] op_sel_hi:[1,0]
	global_store_dwordx2 v[20:21], v[18:19], off offset:-512
	v_pk_mul_f32 v[42:43], v[16:17], v[42:43]
	v_pk_fma_f32 v[42:43], v[56:57], v[42:43], v[64:65]
	v_cvt_pk_bf16_f32 v18, v36, v37
	v_cvt_pk_bf16_f32 v19, v42, v43
	v_lshl_add_u64 v[28:29], v[28:29], 0, s[12:13]
	global_store_dwordx2 v[20:21], v[18:19], off
	s_cbranch_scc0 .LBB0_2234
.LBB0_2232:
	v_add_co_u32_e32 v18, vcc, 0xdcc00000, v28
	s_cmpk_lt_i32 s6, 0x400
	s_nop 0
	v_addc_co_u32_e32 v19, vcc, -1, v29, vcc
	global_load_dwordx2 v[20:21], v[18:19], off offset:-1536
	global_load_dwordx2 v[34:35], v[18:19], off offset:-1024
	global_load_dwordx2 v[36:37], v[18:19], off offset:-512
	s_nop 0
	global_load_dwordx2 v[18:19], v[18:19], off
	s_cselect_b64 s[4:5], -1, 0
	s_cmpk_gt_i32 s6, 0x3ff
	s_waitcnt vmcnt(3)
	v_lshlrev_b32_e32 v30, 16, v20
	v_and_b32_e32 v31, 0xffff0000, v20
	v_lshlrev_b32_e32 v32, 16, v21
	v_and_b32_e32 v33, 0xffff0000, v21
	s_waitcnt vmcnt(2)
	v_lshlrev_b32_e32 v38, 16, v34
	v_and_b32_e32 v39, 0xffff0000, v34
	v_lshlrev_b32_e32 v34, 16, v35
	v_and_b32_e32 v35, 0xffff0000, v35
	s_waitcnt vmcnt(1)
	v_lshlrev_b32_e32 v44, 16, v36
	v_and_b32_e32 v45, 0xffff0000, v36
	v_lshlrev_b32_e32 v40, 16, v37
	v_and_b32_e32 v41, 0xffff0000, v37
	s_waitcnt vmcnt(0)
	v_lshlrev_b32_e32 v36, 16, v18
	v_and_b32_e32 v37, 0xffff0000, v18
	v_lshlrev_b32_e32 v42, 16, v19
	v_and_b32_e32 v43, 0xffff0000, v19
	s_cbranch_scc1 .LBB0_2231
	v_add_co_u32_e32 v76, vcc, 0xfec00000, v28
	v_lshl_add_u64 v[46:47], v[28:29], 0, s[14:15]
	s_nop 0
	v_addc_co_u32_e32 v77, vcc, -1, v29, vcc
	v_add_co_u32_e32 v74, vcc, s7, v28
	global_load_dwordx2 v[50:51], v[76:77], off offset:-1536
	s_nop 0
	v_addc_co_u32_e32 v75, vcc, -1, v29, vcc
	v_add_co_u32_e32 v78, vcc, s9, v28
	global_load_dwordx2 v[48:49], v[28:29], off offset:-1536
	s_nop 0
	v_addc_co_u32_e32 v79, vcc, -1, v29, vcc
	v_add_co_u32_e32 v66, vcc, s22, v28
	global_load_dwordx2 v[72:73], v[78:79], off offset:-1536
	global_load_dwordx2 v[52:53], v[74:75], off offset:-1536
	v_addc_co_u32_e32 v67, vcc, -1, v29, vcc
	v_add_co_u32_e32 v62, vcc, s23, v28
	global_load_dwordx2 v[70:71], v[66:67], off offset:-1536
	s_nop 0
	v_addc_co_u32_e32 v63, vcc, -1, v29, vcc
	v_add_co_u32_e32 v56, vcc, s30, v28
	global_load_dwordx2 v[68:69], v[62:63], off offset:-1536
	s_nop 0
	v_addc_co_u32_e32 v57, vcc, -1, v29, vcc
	v_add_co_u32_e32 v54, vcc, s31, v28
	global_load_dwordx2 v[64:65], v[56:57], off offset:-1536
	s_nop 0
	v_addc_co_u32_e32 v55, vcc, -1, v29, vcc
	global_load_dwordx2 v[58:59], v[54:55], off offset:-1536
	v_add_co_u32_e32 v84, vcc, s33, v28
	s_waitcnt vmcnt(7)
	v_lshlrev_b32_e32 v106, 16, v50
	v_addc_co_u32_e32 v85, vcc, -1, v29, vcc
	global_load_dwordx2 v[86:87], v[84:85], off offset:-1536
	global_load_dwordx4 v[18:21], v[26:27], off
	v_add_co_u32_e32 v80, vcc, s36, v28
	v_and_b32_e32 v107, 0xffff0000, v50
	s_nop 0
	v_addc_co_u32_e32 v81, vcc, -1, v29, vcc
	global_load_dwordx2 v[82:83], v[80:81], off offset:-1536
	global_load_dwordx2 v[60:61], v[76:77], off offset:-1024
	global_load_dwordx2 v[88:89], v[76:77], off offset:-512
	s_nop 0
	global_load_dwordx2 v[76:77], v[76:77], off
	v_add_co_u32_e32 v98, vcc, s37, v28
	v_lshlrev_b32_e32 v50, 16, v51
	s_nop 0
	v_addc_co_u32_e32 v99, vcc, -1, v29, vcc
	global_load_dwordx2 v[100:101], v[98:99], off offset:-1536
	global_load_dwordx2 v[102:103], v[74:75], off offset:-1024
	global_load_dwordx2 v[90:91], v[74:75], off offset:-512
	s_nop 0
	global_load_dwordx2 v[74:75], v[74:75], off
	s_nop 0
	global_load_dwordx2 v[104:105], v[78:79], off offset:-1024
	global_load_dwordx2 v[92:93], v[78:79], off offset:-512
	s_nop 0
	global_load_dwordx2 v[78:79], v[78:79], off
	v_and_b32_e32 v51, 0xffff0000, v51
	v_pk_add_f32 v[50:51], v[50:51], 0 op_sel_hi:[1,0]
	v_pk_add_f32 v[106:107], v[106:107], 0 op_sel_hi:[1,0]
	s_waitcnt vmcnt(17)
	v_lshlrev_b32_e32 v108, 16, v52
	v_and_b32_e32 v109, 0xffff0000, v52
	v_lshlrev_b32_e32 v52, 16, v53
	v_and_b32_e32 v53, 0xffff0000, v53
	v_pk_add_f32 v[106:107], v[106:107], v[108:109]
	v_pk_add_f32 v[50:51], v[50:51], v[52:53]
	v_lshlrev_b32_e32 v52, 16, v72
	v_and_b32_e32 v53, 0xffff0000, v72
	v_lshlrev_b32_e32 v72, 16, v73
	v_and_b32_e32 v73, 0xffff0000, v73
	v_pk_add_f32 v[108:109], v[50:51], v[72:73]
	v_pk_add_f32 v[52:53], v[106:107], v[52:53]
	global_load_dwordx2 v[106:107], v[66:67], off offset:-1024
	global_load_dwordx2 v[72:73], v[66:67], off offset:-512
	global_load_dwordx2 v[50:51], v[66:67], off
	s_waitcnt vmcnt(19)
	v_lshlrev_b32_e32 v66, 16, v70
	v_and_b32_e32 v67, 0xffff0000, v70
	v_lshlrev_b32_e32 v70, 16, v71
	v_and_b32_e32 v71, 0xffff0000, v71
	v_pk_add_f32 v[66:67], v[52:53], v[66:67]
	v_pk_add_f32 v[108:109], v[108:109], v[70:71]
	global_load_dwordx2 v[110:111], v[62:63], off offset:-1024
	global_load_dwordx2 v[70:71], v[62:63], off offset:-512
	global_load_dwordx2 v[52:53], v[62:63], off
	s_waitcnt vmcnt(21)
	v_lshlrev_b32_e32 v62, 16, v68
	v_and_b32_e32 v63, 0xffff0000, v68
	v_lshlrev_b32_e32 v68, 16, v69
	v_and_b32_e32 v69, 0xffff0000, v69
	v_pk_add_f32 v[108:109], v[108:109], v[68:69]
	v_pk_add_f32 v[62:63], v[66:67], v[62:63]
	s_waitcnt vmcnt(20)
	v_lshlrev_b32_e32 v66, 16, v64
	v_and_b32_e32 v67, 0xffff0000, v64
	v_lshlrev_b32_e32 v64, 16, v65
	v_and_b32_e32 v65, 0xffff0000, v65
	v_pk_add_f32 v[62:63], v[62:63], v[66:67]
	v_pk_add_f32 v[64:65], v[108:109], v[64:65]
	s_waitcnt vmcnt(19)
	v_lshlrev_b32_e32 v66, 16, v58
	v_and_b32_e32 v67, 0xffff0000, v58
	v_lshlrev_b32_e32 v58, 16, v59
	v_and_b32_e32 v59, 0xffff0000, v59
	global_load_dwordx2 v[112:113], v[56:57], off offset:-1024
	global_load_dwordx2 v[68:69], v[56:57], off offset:-512
	s_nop 0
	global_load_dwordx2 v[56:57], v[56:57], off
	s_nop 0
	global_load_dwordx2 v[108:109], v[54:55], off offset:-1024
	global_load_dwordx2 v[114:115], v[54:55], off offset:-512
	s_nop 0
	global_load_dwordx2 v[54:55], v[54:55], off
	v_pk_add_f32 v[64:65], v[64:65], v[58:59]
	v_pk_add_f32 v[62:63], v[62:63], v[66:67]
	global_load_dwordx2 v[116:117], v[84:85], off offset:-1024
	global_load_dwordx2 v[118:119], v[84:85], off offset:-512
	global_load_dwordx2 v[58:59], v[84:85], off
	v_lshlrev_b32_e32 v124, 16, v48
	v_and_b32_e32 v125, 0xffff0000, v48
	v_lshlrev_b32_e32 v48, 16, v49
	v_and_b32_e32 v49, 0xffff0000, v49
	s_waitcnt vmcnt(27)
	v_lshlrev_b32_e32 v66, 16, v86
	v_and_b32_e32 v67, 0xffff0000, v86
	v_lshlrev_b32_e32 v84, 16, v87
	v_and_b32_e32 v85, 0xffff0000, v87
	v_pk_add_f32 v[66:67], v[62:63], v[66:67]
	v_pk_add_f32 v[64:65], v[64:65], v[84:85]
	global_load_dwordx2 v[84:85], v[80:81], off offset:-1024
	global_load_dwordx2 v[86:87], v[80:81], off offset:-512
	global_load_dwordx2 v[62:63], v[80:81], off
	s_waitcnt vmcnt(28)
	v_lshlrev_b32_e32 v80, 16, v82
	v_and_b32_e32 v81, 0xffff0000, v82
	v_lshlrev_b32_e32 v82, 16, v83
	v_and_b32_e32 v83, 0xffff0000, v83
	v_pk_add_f32 v[82:83], v[64:65], v[82:83]
	v_pk_add_f32 v[66:67], v[66:67], v[80:81]
	global_load_dwordx2 v[80:81], v[98:99], off offset:-1024
	global_load_dwordx2 v[120:121], v[98:99], off offset:-512
	global_load_dwordx2 v[64:65], v[98:99], off
	s_waitcnt vmcnt(27)
	v_lshlrev_b32_e32 v98, 16, v100
	v_and_b32_e32 v99, 0xffff0000, v100
	v_lshlrev_b32_e32 v100, 16, v101
	v_and_b32_e32 v101, 0xffff0000, v101
	v_pk_add_f32 v[98:99], v[66:67], v[98:99]
	v_pk_add_f32 v[82:83], v[82:83], v[100:101]
	global_load_dwordx2 v[100:101], v[28:29], off offset:-1024
	global_load_dwordx2 v[122:123], v[28:29], off offset:-512
	global_load_dwordx2 v[66:67], v[28:29], off
	v_pk_add_f32 v[48:49], v[82:83], v[48:49]
	v_pk_add_f32 v[82:83], v[98:99], v[124:125]
	v_pk_fma_f32 v[32:33], v[48:49], v[20:21], v[32:33]
	v_pk_fma_f32 v[18:19], v[82:83], v[18:19], v[30:31]
	v_lshlrev_b32_e32 v48, 16, v60
	v_bfe_u32 v20, v18, 16, 1
	v_add3_u32 v30, v18, v20, s40
	v_bfe_u32 v18, v19, 16, 1
	v_and_b32_sdwa v20, v33, v97 dst_sel:DWORD dst_unused:UNUSED_PAD src0_sel:WORD_1 src1_sel:DWORD
	v_add3_u32 v18, v19, v18, s40
	v_bfe_u32 v19, v32, 16, 1
	v_add3_u32 v20, v33, v20, s40
	v_and_b32_e32 v31, 0xffff0000, v18
	v_add3_u32 v19, v32, v19, s40
	v_and_b32_e32 v33, 0xffff0000, v20
	v_or_b32_sdwa v18, v31, v30 dst_sel:DWORD dst_unused:UNUSED_PAD src0_sel:DWORD src1_sel:WORD_1
	v_or_b32_sdwa v19, v33, v19 dst_sel:DWORD dst_unused:UNUSED_PAD src0_sel:DWORD src1_sel:WORD_1
	global_store_dwordx2 v[46:47], v[18:19], off
	global_load_dwordx4 v[18:21], v[26:27], off offset:1024
	v_and_b32_e32 v49, 0xffff0000, v60
	v_lshlrev_b32_e32 v60, 16, v61
	v_and_b32_e32 v61, 0xffff0000, v61
	v_pk_add_f32 v[48:49], v[48:49], 0 op_sel_hi:[1,0]
	v_pk_add_f32 v[60:61], v[60:61], 0 op_sel_hi:[1,0]
	s_waitcnt vmcnt(31)
	v_lshlrev_b32_e32 v82, 16, v102
	v_and_b32_e32 v83, 0xffff0000, v102
	v_lshlrev_b32_e32 v98, 16, v103
	v_and_b32_e32 v99, 0xffff0000, v103
	v_pk_add_f32 v[60:61], v[60:61], v[98:99]
	v_pk_add_f32 v[48:49], v[48:49], v[82:83]
	s_waitcnt vmcnt(28)
	v_lshlrev_b32_e32 v82, 16, v104
	v_and_b32_e32 v83, 0xffff0000, v104
	v_lshlrev_b32_e32 v98, 16, v105
	v_and_b32_e32 v99, 0xffff0000, v105
	v_pk_add_f32 v[48:49], v[48:49], v[82:83]
	v_pk_add_f32 v[60:61], v[60:61], v[98:99]
	s_waitcnt vmcnt(25)
	v_lshlrev_b32_e32 v82, 16, v106
	v_and_b32_e32 v83, 0xffff0000, v106
	v_lshlrev_b32_e32 v98, 16, v107
	v_and_b32_e32 v99, 0xffff0000, v107
	v_pk_add_f32 v[60:61], v[60:61], v[98:99]
	v_pk_add_f32 v[48:49], v[48:49], v[82:83]
	s_waitcnt vmcnt(22)
	v_lshlrev_b32_e32 v82, 16, v110
	v_and_b32_e32 v83, 0xffff0000, v110
	v_lshlrev_b32_e32 v98, 16, v111
	v_and_b32_e32 v99, 0xffff0000, v111
	v_pk_add_f32 v[48:49], v[48:49], v[82:83]
	v_pk_add_f32 v[60:61], v[60:61], v[98:99]
	s_waitcnt vmcnt(19)
	v_lshlrev_b32_e32 v82, 16, v112
	v_and_b32_e32 v83, 0xffff0000, v112
	v_lshlrev_b32_e32 v98, 16, v113
	v_and_b32_e32 v99, 0xffff0000, v113
	v_pk_add_f32 v[60:61], v[60:61], v[98:99]
	v_pk_add_f32 v[48:49], v[48:49], v[82:83]
	s_waitcnt vmcnt(16)
	v_lshlrev_b32_e32 v82, 16, v108
	v_and_b32_e32 v83, 0xffff0000, v108
	v_lshlrev_b32_e32 v98, 16, v109
	v_and_b32_e32 v99, 0xffff0000, v109
	v_pk_add_f32 v[48:49], v[48:49], v[82:83]
	v_pk_add_f32 v[60:61], v[60:61], v[98:99]
	s_waitcnt vmcnt(13)
	v_lshlrev_b32_e32 v82, 16, v116
	v_and_b32_e32 v83, 0xffff0000, v116
	v_lshlrev_b32_e32 v98, 16, v117
	v_and_b32_e32 v99, 0xffff0000, v117
	v_pk_add_f32 v[60:61], v[60:61], v[98:99]
	v_pk_add_f32 v[48:49], v[48:49], v[82:83]
	s_waitcnt vmcnt(10)
	v_lshlrev_b32_e32 v82, 16, v84
	v_and_b32_e32 v83, 0xffff0000, v84
	v_lshlrev_b32_e32 v84, 16, v85
	v_and_b32_e32 v85, 0xffff0000, v85
	v_pk_add_f32 v[48:49], v[48:49], v[82:83]
	v_pk_add_f32 v[60:61], v[60:61], v[84:85]
	s_waitcnt vmcnt(7)
	v_lshlrev_b32_e32 v82, 16, v80
	v_and_b32_e32 v83, 0xffff0000, v80
	v_lshlrev_b32_e32 v80, 16, v81
	v_and_b32_e32 v81, 0xffff0000, v81
	v_pk_add_f32 v[60:61], v[60:61], v[80:81]
	v_pk_add_f32 v[48:49], v[48:49], v[82:83]
	s_waitcnt vmcnt(4)
	v_lshlrev_b32_e32 v80, 16, v100
	v_and_b32_e32 v81, 0xffff0000, v100
	v_pk_add_f32 v[48:49], v[48:49], v[80:81]
	v_lshlrev_b32_e32 v82, 16, v101
	v_and_b32_e32 v83, 0xffff0000, v101
	v_pk_add_f32 v[60:61], v[60:61], v[82:83]
	v_lshl_add_u64 v[46:47], v[28:29], 0, s[16:17]
	v_lshlrev_b32_e32 v80, 16, v89
	v_and_b32_e32 v81, 0xffff0000, v89
	v_pk_add_f32 v[80:81], v[80:81], 0 op_sel_hi:[1,0]
	v_lshlrev_b32_e32 v82, 16, v90
	v_and_b32_e32 v83, 0xffff0000, v90
	v_lshlrev_b32_e32 v84, 16, v91
	v_and_b32_e32 v85, 0xffff0000, v91
	v_pk_add_f32 v[80:81], v[80:81], v[84:85]
	v_lshlrev_b32_e32 v84, 16, v93
	v_and_b32_e32 v85, 0xffff0000, v93
	v_pk_add_f32 v[80:81], v[80:81], v[84:85]
	v_and_b32_e32 v30, 0xffff0000, v30
	s_waitcnt vmcnt(0)
	v_pk_fma_f32 v[38:39], v[48:49], v[18:19], v[38:39]
	s_nop 0
	v_pk_fma_f32 v[34:35], v[60:61], v[20:21], v[34:35]
	v_and_b32_sdwa v20, v35, v97 dst_sel:DWORD dst_unused:UNUSED_PAD src0_sel:WORD_1 src1_sel:DWORD
	v_cvt_pk_bf16_f32 v18, v38, v39
	v_bfe_u32 v19, v34, 16, 1
	v_add3_u32 v20, v35, v20, s40
	v_add3_u32 v19, v34, v19, s40
	v_and_b32_e32 v35, 0xffff0000, v20
	v_or_b32_sdwa v19, v35, v19 dst_sel:DWORD dst_unused:UNUSED_PAD src0_sel:DWORD src1_sel:WORD_1
	global_store_dwordx2 v[46:47], v[18:19], off
	global_load_dwordx4 v[18:21], v[26:27], off offset:2048
	v_and_b32_sdwa v60, v32, v97 dst_sel:DWORD dst_unused:UNUSED_PAD src0_sel:WORD_1 src1_sel:DWORD
	v_add3_u32 v32, v32, v60, s40
	v_and_b32_sdwa v60, v39, v97 dst_sel:DWORD dst_unused:UNUSED_PAD src0_sel:WORD_1 src1_sel:DWORD
	v_and_b32_sdwa v61, v38, v97 dst_sel:DWORD dst_unused:UNUSED_PAD src0_sel:WORD_1 src1_sel:DWORD
	v_add3_u32 v39, v39, v60, s40
	v_add3_u32 v38, v38, v61, s40
	v_lshlrev_b32_e32 v60, 16, v88
	v_and_b32_e32 v61, 0xffff0000, v88
	v_pk_add_f32 v[60:61], v[60:61], 0 op_sel_hi:[1,0]
	v_lshl_add_u64 v[46:47], v[28:29], 0, s[18:19]
	v_pk_add_f32 v[60:61], v[60:61], v[82:83]
	v_lshlrev_b32_e32 v82, 16, v92
	v_and_b32_e32 v83, 0xffff0000, v92
	v_pk_add_f32 v[60:61], v[60:61], v[82:83]
	v_lshlrev_b32_e32 v82, 16, v72
	v_and_b32_e32 v83, 0xffff0000, v72
	v_lshlrev_b32_e32 v72, 16, v73
	v_and_b32_e32 v73, 0xffff0000, v73
	v_pk_add_f32 v[72:73], v[80:81], v[72:73]
	v_pk_add_f32 v[60:61], v[60:61], v[82:83]
	v_lshlrev_b32_e32 v80, 16, v70
	v_and_b32_e32 v81, 0xffff0000, v70
	v_lshlrev_b32_e32 v70, 16, v71
	v_and_b32_e32 v71, 0xffff0000, v71
	v_pk_add_f32 v[60:61], v[60:61], v[80:81]
	v_pk_add_f32 v[70:71], v[72:73], v[70:71]
	v_lshlrev_b32_e32 v72, 16, v68
	v_and_b32_e32 v73, 0xffff0000, v68
	v_lshlrev_b32_e32 v68, 16, v69
	v_and_b32_e32 v69, 0xffff0000, v69
	v_pk_add_f32 v[68:69], v[70:71], v[68:69]
	v_pk_add_f32 v[60:61], v[60:61], v[72:73]
	v_lshlrev_b32_e32 v70, 16, v114
	v_and_b32_e32 v71, 0xffff0000, v114
	v_pk_add_f32 v[60:61], v[60:61], v[70:71]
	v_lshlrev_b32_e32 v70, 16, v118
	v_and_b32_e32 v71, 0xffff0000, v118
	v_lshlrev_b32_e32 v72, 16, v115
	v_and_b32_e32 v73, 0xffff0000, v115
	v_pk_add_f32 v[60:61], v[60:61], v[70:71]
	v_lshlrev_b32_e32 v70, 16, v86
	v_and_b32_e32 v71, 0xffff0000, v86
	v_pk_add_f32 v[68:69], v[68:69], v[72:73]
	v_lshlrev_b32_e32 v72, 16, v119
	v_and_b32_e32 v73, 0xffff0000, v119
	v_pk_add_f32 v[60:61], v[60:61], v[70:71]
	v_lshlrev_b32_e32 v70, 16, v120
	v_and_b32_e32 v71, 0xffff0000, v120
	v_pk_add_f32 v[68:69], v[68:69], v[72:73]
	v_lshlrev_b32_e32 v72, 16, v87
	v_and_b32_e32 v73, 0xffff0000, v87
	v_pk_add_f32 v[60:61], v[60:61], v[70:71]
	v_lshlrev_b32_e32 v70, 16, v122
	v_and_b32_e32 v71, 0xffff0000, v122
	v_pk_add_f32 v[68:69], v[68:69], v[72:73]
	v_lshlrev_b32_e32 v72, 16, v121
	v_and_b32_e32 v73, 0xffff0000, v121
	v_pk_add_f32 v[60:61], v[60:61], v[70:71]
	v_pk_add_f32 v[68:69], v[68:69], v[72:73]
	v_lshlrev_b32_e32 v72, 16, v123
	v_and_b32_e32 v73, 0xffff0000, v123
	v_pk_add_f32 v[68:69], v[68:69], v[72:73]
	v_lshlrev_b32_e32 v70, 16, v75
	v_and_b32_e32 v71, 0xffff0000, v75
	v_lshl_add_u64 v[48:49], v[28:29], 0, s[20:21]
	v_and_b32_e32 v32, 0xffff0000, v32
	v_and_b32_e32 v39, 0xffff0000, v39
	v_and_b32_e32 v38, 0xffff0000, v38
	s_waitcnt vmcnt(0)
	v_pk_fma_f32 v[44:45], v[60:61], v[18:19], v[44:45]
	s_nop 0
	v_pk_fma_f32 v[40:41], v[68:69], v[20:21], v[40:41]
	v_and_b32_sdwa v20, v41, v97 dst_sel:DWORD dst_unused:UNUSED_PAD src0_sel:WORD_1 src1_sel:DWORD
	v_cvt_pk_bf16_f32 v18, v44, v45
	v_bfe_u32 v19, v40, 16, 1
	v_add3_u32 v20, v41, v20, s40
	v_add3_u32 v19, v40, v19, s40
	v_and_b32_e32 v41, 0xffff0000, v20
	v_or_b32_sdwa v19, v41, v19 dst_sel:DWORD dst_unused:UNUSED_PAD src0_sel:DWORD src1_sel:WORD_1
	global_store_dwordx2 v[46:47], v[18:19], off
	global_load_dwordx4 v[18:21], v[26:27], off offset:3072
	v_and_b32_sdwa v46, v34, v97 dst_sel:DWORD dst_unused:UNUSED_PAD src0_sel:WORD_1 src1_sel:DWORD
	v_add3_u32 v34, v34, v46, s40
	v_and_b32_sdwa v46, v45, v97 dst_sel:DWORD dst_unused:UNUSED_PAD src0_sel:WORD_1 src1_sel:DWORD
	v_and_b32_sdwa v47, v44, v97 dst_sel:DWORD dst_unused:UNUSED_PAD src0_sel:WORD_1 src1_sel:DWORD
	v_add3_u32 v45, v45, v46, s40
	v_add3_u32 v44, v44, v47, s40
	v_lshlrev_b32_e32 v46, 16, v76
	v_and_b32_e32 v47, 0xffff0000, v76
	v_lshlrev_b32_e32 v60, 16, v77
	v_and_b32_e32 v61, 0xffff0000, v77
	v_pk_add_f32 v[46:47], v[46:47], 0 op_sel_hi:[1,0]
	v_pk_add_f32 v[60:61], v[60:61], 0 op_sel_hi:[1,0]
	v_lshlrev_b32_e32 v68, 16, v74
	v_and_b32_e32 v69, 0xffff0000, v74
	v_pk_add_f32 v[60:61], v[60:61], v[70:71]
	v_pk_add_f32 v[46:47], v[46:47], v[68:69]
	v_lshlrev_b32_e32 v68, 16, v78
	v_and_b32_e32 v69, 0xffff0000, v78
	v_lshlrev_b32_e32 v70, 16, v79
	v_and_b32_e32 v71, 0xffff0000, v79
	v_pk_add_f32 v[46:47], v[46:47], v[68:69]
	v_pk_add_f32 v[60:61], v[60:61], v[70:71]
	v_lshlrev_b32_e32 v68, 16, v50
	v_and_b32_e32 v69, 0xffff0000, v50
	v_lshlrev_b32_e32 v50, 16, v51
	v_and_b32_e32 v51, 0xffff0000, v51
	v_pk_add_f32 v[50:51], v[60:61], v[50:51]
	v_pk_add_f32 v[46:47], v[46:47], v[68:69]
	v_lshlrev_b32_e32 v60, 16, v52
	v_and_b32_e32 v61, 0xffff0000, v52
	v_lshlrev_b32_e32 v52, 16, v53
	v_and_b32_e32 v53, 0xffff0000, v53
	v_pk_add_f32 v[46:47], v[46:47], v[60:61]
	v_pk_add_f32 v[50:51], v[50:51], v[52:53]
	v_lshlrev_b32_e32 v52, 16, v56
	v_and_b32_e32 v53, 0xffff0000, v56
	v_pk_add_f32 v[46:47], v[46:47], v[52:53]
	v_lshlrev_b32_e32 v52, 16, v54
	v_and_b32_e32 v53, 0xffff0000, v54
	v_pk_add_f32 v[46:47], v[46:47], v[52:53]
	v_lshlrev_b32_e32 v52, 16, v58
	v_and_b32_e32 v53, 0xffff0000, v58
	v_lshlrev_b32_e32 v56, 16, v57
	v_and_b32_e32 v57, 0xffff0000, v57
	v_pk_add_f32 v[46:47], v[46:47], v[52:53]
	v_lshlrev_b32_e32 v52, 16, v62
	v_and_b32_e32 v53, 0xffff0000, v62
	v_pk_add_f32 v[50:51], v[50:51], v[56:57]
	v_lshlrev_b32_e32 v54, 16, v55
	v_and_b32_e32 v55, 0xffff0000, v55
	v_pk_add_f32 v[46:47], v[46:47], v[52:53]
	v_lshlrev_b32_e32 v52, 16, v64
	v_and_b32_e32 v53, 0xffff0000, v64
	v_pk_add_f32 v[50:51], v[50:51], v[54:55]
	v_lshlrev_b32_e32 v54, 16, v59
	v_and_b32_e32 v55, 0xffff0000, v59
	v_pk_add_f32 v[46:47], v[46:47], v[52:53]
	v_lshlrev_b32_e32 v52, 16, v66
	v_and_b32_e32 v53, 0xffff0000, v66
	v_pk_add_f32 v[50:51], v[50:51], v[54:55]
	v_lshlrev_b32_e32 v54, 16, v63
	v_and_b32_e32 v55, 0xffff0000, v63
	v_pk_add_f32 v[46:47], v[46:47], v[52:53]
	v_pk_add_f32 v[50:51], v[50:51], v[54:55]
	v_lshlrev_b32_e32 v54, 16, v65
	v_and_b32_e32 v55, 0xffff0000, v65
	v_pk_add_f32 v[50:51], v[50:51], v[54:55]
	v_lshlrev_b32_e32 v54, 16, v67
	v_and_b32_e32 v55, 0xffff0000, v67
	v_pk_add_f32 v[50:51], v[50:51], v[54:55]
	v_and_b32_sdwa v52, v40, v97 dst_sel:DWORD dst_unused:UNUSED_PAD src0_sel:WORD_1 src1_sel:DWORD
	v_add3_u32 v40, v40, v52, s40
	v_and_b32_e32 v34, 0xffff0000, v34
	v_and_b32_e32 v45, 0xffff0000, v45
	v_and_b32_e32 v44, 0xffff0000, v44
	v_and_b32_e32 v40, 0xffff0000, v40
	s_waitcnt vmcnt(0)
	v_pk_fma_f32 v[18:19], v[46:47], v[18:19], v[36:37]
	s_nop 0
	v_pk_fma_f32 v[20:21], v[50:51], v[20:21], v[42:43]
	v_cvt_pk_bf16_f32 v46, v18, v19
	v_bfe_u32 v36, v20, 16, 1
	v_and_b32_sdwa v37, v18, v97 dst_sel:DWORD dst_unused:UNUSED_PAD src0_sel:WORD_1 src1_sel:DWORD
	v_add3_u32 v47, v20, v36, s40
	v_and_b32_sdwa v36, v19, v97 dst_sel:DWORD dst_unused:UNUSED_PAD src0_sel:WORD_1 src1_sel:DWORD
	v_add3_u32 v18, v18, v37, s40
	v_add3_u32 v19, v19, v36, s40
	v_and_b32_e32 v36, 0xffff0000, v18
	v_and_b32_sdwa v18, v21, v97 dst_sel:DWORD dst_unused:UNUSED_PAD src0_sel:WORD_1 src1_sel:DWORD
	v_and_b32_e32 v37, 0xffff0000, v19
	v_and_b32_sdwa v19, v20, v97 dst_sel:DWORD dst_unused:UNUSED_PAD src0_sel:WORD_1 src1_sel:DWORD
	v_add3_u32 v18, v21, v18, s40
	v_add3_u32 v19, v20, v19, s40
	v_and_b32_e32 v43, 0xffff0000, v18
	v_and_b32_e32 v42, 0xffff0000, v19
	v_or_b32_sdwa v47, v43, v47 dst_sel:DWORD dst_unused:UNUSED_PAD src0_sel:DWORD src1_sel:WORD_1
	global_store_dwordx2 v[48:49], v[46:47], off
	s_branch .LBB0_2231

.LBB0_2365:
	s_waitcnt vmcnt(2)
	v_lshlrev_b32_e32 v76, 16, v9
	v_lshlrev_b32_e32 v75, 16, v5
	s_waitcnt vmcnt(1)
	v_mul_f32_e32 v79, v71, v76
	s_waitcnt vmcnt(0)
	v_lshlrev_b32_e32 v78, 16, v17
	v_fma_f32 v79, v70, v75, -v79
	v_mul_f32_e32 v70, v70, v76
	v_lshlrev_b32_e32 v77, 16, v13
	v_fmac_f32_e32 v70, v71, v75
	v_mul_f32_e32 v71, v69, v78
	v_fma_f32 v71, v68, v77, -v71
	v_mul_f32_e32 v68, v68, v78
	v_lshlrev_b32_e32 v75, 16, v8
	v_fmac_f32_e32 v68, v69, v77
	v_lshlrev_b32_e32 v69, 16, v4
	v_mul_f32_e32 v78, v65, v75
	v_lshlrev_b32_e32 v77, 16, v16
	v_fma_f32 v78, v64, v69, -v78
	v_mul_f32_e32 v64, v64, v75
	v_lshlrev_b32_e32 v76, 16, v12
	v_fmac_f32_e32 v64, v65, v69
	v_mul_f32_e32 v65, v63, v77
	v_fma_f32 v65, v62, v76, -v65
	v_mul_f32_e32 v62, v62, v77
	v_and_b32_e32 v8, 0xffff0000, v8
	v_fmac_f32_e32 v62, v63, v76
	v_and_b32_e32 v4, 0xffff0000, v4
	v_and_b32_e32 v16, 0xffff0000, v16
	v_mul_f32_e32 v63, v67, v8
	v_mul_f32_e32 v8, v66, v8
	v_and_b32_e32 v12, 0xffff0000, v12
	v_fma_f32 v63, v66, v4, -v63
	v_fmac_f32_e32 v8, v67, v4
	v_mul_f32_e32 v4, v61, v16
	v_fma_f32 v4, v60, v12, -v4
	v_mul_f32_e32 v66, 0x3d800000, v4
	v_mul_f32_e32 v4, v60, v16
	v_mul_f32_e32 v78, 0x3d800000, v78
	v_fmac_f32_e32 v4, v61, v12
	v_mul_f32_e32 v63, 0x3d800000, v63
	v_mul_f32_e32 v16, 0x3d800000, v4
	v_mul_f32_e32 v64, 0x3d800000, v64
	v_mul_f32_e32 v8, 0x3d800000, v8
	v_cvt_pk_bf16_f32 v4, v78, v63
	v_bfe_u32 v12, v64, 16, 1
	v_add3_u32 v12, v64, v12, s45
	v_bfe_u32 v60, v8, 16, 1
	v_mul_f32_e32 v65, 0x3d800000, v65
	v_lshrrev_b32_e32 v12, 16, v12
	v_add3_u32 v8, v8, v60, s45
	v_and_or_b32 v8, v8, s44, v12
	v_mul_f32_e32 v62, 0x3d800000, v62
	v_cvt_pk_bf16_f32 v12, v65, v66
	v_bfe_u32 v60, v62, 16, 1
	v_add3_u32 v60, v62, v60, s45
	v_bfe_u32 v61, v16, 16, 1
	v_lshrrev_b32_e32 v60, 16, v60
	v_add3_u32 v16, v16, v61, s45
	v_and_b32_e32 v61, 0xffff0000, v9
	v_lshlrev_b32_e32 v9, 16, v7
	v_and_or_b32 v16, v16, s44, v60
	v_and_b32_e32 v60, 0xffff0000, v5
	v_lshlrev_b32_e32 v5, 16, v3
	v_mul_f32_e32 v64, v33, v9
	v_mul_f32_e32 v9, v32, v9
	v_and_b32_e32 v63, 0xffff0000, v17
	v_lshlrev_b32_e32 v17, 16, v15
	v_fmac_f32_e32 v9, v33, v5
	v_and_b32_e32 v62, 0xffff0000, v13
	v_lshlrev_b32_e32 v13, 16, v11
	v_fma_f32 v64, v32, v5, -v64
	v_mul_f32_e32 v5, 0x3d800000, v9
	v_mul_f32_e32 v9, v31, v17
	v_mul_f32_e32 v17, v30, v17
	v_fmac_f32_e32 v17, v31, v13
	v_and_b32_e32 v7, 0xffff0000, v7
	v_fma_f32 v9, v30, v13, -v9
	v_mul_f32_e32 v13, 0x3d800000, v17
	v_and_b32_e32 v3, 0xffff0000, v3
	v_and_b32_e32 v15, 0xffff0000, v15
	v_mul_f32_e32 v17, v57, v7
	v_mul_f32_e32 v7, v56, v7
	v_and_b32_e32 v11, 0xffff0000, v11
	v_fma_f32 v17, v56, v3, -v17
	v_fmac_f32_e32 v7, v57, v3
	v_mul_f32_e32 v3, v27, v15
	v_fma_f32 v3, v26, v11, -v3
	v_mul_f32_e32 v30, 0x3d800000, v3
	v_mul_f32_e32 v3, v26, v15
	v_mul_f32_e32 v64, 0x3d800000, v64
	v_fmac_f32_e32 v3, v27, v11
	v_mul_f32_e32 v17, 0x3d800000, v17
	v_mul_f32_e32 v15, 0x3d800000, v3
	v_mul_f32_e32 v7, 0x3d800000, v7
	v_cvt_pk_bf16_f32 v3, v64, v17
	v_bfe_u32 v11, v5, 16, 1
	v_add3_u32 v5, v5, v11, s45
	v_bfe_u32 v11, v7, 16, 1
	v_mul_f32_e32 v9, 0x3d800000, v9
	v_lshrrev_b32_e32 v5, 16, v5
	v_add3_u32 v7, v7, v11, s45
	v_and_or_b32 v7, v7, s44, v5
	v_bfe_u32 v5, v9, 16, 1
	v_add3_u32 v5, v9, v5, s45
	v_bfe_u32 v9, v30, 16, 1
	v_lshrrev_b32_e32 v5, 16, v5
	v_add3_u32 v9, v30, v9, s45
	v_and_or_b32 v11, v9, s44, v5
	v_cvt_pk_bf16_f32 v15, v13, v15
	v_lshlrev_b32_e32 v9, 16, v6
	v_lshlrev_b32_e32 v5, 16, v2
	v_mul_f32_e32 v26, v23, v9
	v_mul_f32_e32 v9, v22, v9
	v_lshlrev_b32_e32 v17, 16, v14
	v_fmac_f32_e32 v9, v23, v5
	v_lshlrev_b32_e32 v13, 16, v10
	v_fma_f32 v26, v22, v5, -v26
	v_mul_f32_e32 v5, 0x3d800000, v9
	v_mul_f32_e32 v9, v21, v17
	v_mul_f32_e32 v17, v20, v17
	v_fmac_f32_e32 v17, v21, v13
	v_and_b32_e32 v6, 0xffff0000, v6
	v_fma_f32 v9, v20, v13, -v9
	v_mul_f32_e32 v13, 0x3d800000, v17
	v_and_b32_e32 v2, 0xffff0000, v2
	v_and_b32_e32 v14, 0xffff0000, v14
	v_mul_f32_e32 v17, v25, v6
	v_mul_f32_e32 v6, v24, v6
	v_and_b32_e32 v10, 0xffff0000, v10
	v_fma_f32 v17, v24, v2, -v17
	v_fmac_f32_e32 v6, v25, v2
	v_mul_f32_e32 v2, v19, v14
	v_fma_f32 v2, v18, v10, -v2
	v_mul_f32_e32 v20, 0x3d800000, v2
	v_mul_f32_e32 v2, v18, v14
	v_mul_f32_e32 v26, 0x3d800000, v26
	v_fmac_f32_e32 v2, v19, v10
	v_mul_f32_e32 v17, 0x3d800000, v17
	v_mul_f32_e32 v14, 0x3d800000, v2
	v_mul_f32_e32 v6, 0x3d800000, v6
	v_cvt_pk_bf16_f32 v2, v26, v17
	v_bfe_u32 v10, v5, 16, 1
	v_add3_u32 v5, v5, v10, s45
	v_bfe_u32 v10, v6, 16, 1
	v_mul_f32_e32 v9, 0x3d800000, v9
	v_lshrrev_b32_e32 v5, 16, v5
	v_add3_u32 v6, v6, v10, s45
	v_and_or_b32 v6, v6, s44, v5
	v_bfe_u32 v5, v9, 16, 1
	v_add3_u32 v5, v9, v5, s45
	v_bfe_u32 v9, v20, 16, 1
	v_lshrrev_b32_e32 v5, 16, v5
	v_add3_u32 v9, v20, v9, s45
	v_and_or_b32 v10, v9, s44, v5
	v_pk_mul_f32 v[18:19], v[58:59], v[60:61]
	v_cvt_pk_bf16_f32 v14, v13, v14
	v_sub_f32_e32 v5, v18, v19
	v_pk_mul_f32 v[18:19], v[58:59], v[60:61] op_sel:[1,0] op_sel_hi:[0,1]
	v_add_f32_e32 v9, v18, v19
	v_pk_mul_f32 v[18:19], v[28:29], v[62:63]
	v_mul_f32_e32 v79, 0x3d800000, v79
	v_sub_f32_e32 v13, v18, v19
	v_pk_mul_f32 v[18:19], v[28:29], v[62:63] op_sel:[1,0] op_sel_hi:[0,1]
	v_mul_f32_e32 v5, 0x3d800000, v5
	v_add_f32_e32 v17, v18, v19
	v_bfe_u32 v18, v79, 16, 1
	v_add3_u32 v18, v79, v18, s45
	v_bfe_u32 v19, v5, 16, 1
	v_mul_f32_e32 v70, 0x3d800000, v70
	v_lshrrev_b32_e32 v18, 16, v18
	v_add3_u32 v5, v5, v19, s45
	v_mul_f32_e32 v9, 0x3d800000, v9
	v_and_or_b32 v5, v5, s44, v18
	v_bfe_u32 v18, v70, 16, 1
	v_add3_u32 v18, v70, v18, s45
	v_bfe_u32 v19, v9, 16, 1
	v_mul_f32_e32 v71, 0x3d800000, v71
	v_lshrrev_b32_e32 v18, 16, v18
	v_add3_u32 v9, v9, v19, s45
	v_mul_f32_e32 v13, 0x3d800000, v13
	v_and_or_b32 v9, v9, s44, v18
	v_bfe_u32 v18, v71, 16, 1
	v_add3_u32 v18, v71, v18, s45
	v_bfe_u32 v19, v13, 16, 1
	v_mul_f32_e32 v68, 0x3d800000, v68
	v_lshrrev_b32_e32 v18, 16, v18
	v_add3_u32 v13, v13, v19, s45
	v_mul_f32_e32 v17, 0x3d800000, v17
	v_and_or_b32 v13, v13, s44, v18
	v_bfe_u32 v18, v68, 16, 1
	v_add3_u32 v18, v68, v18, s45
	v_bfe_u32 v19, v17, 16, 1
	v_lshrrev_b32_e32 v18, 16, v18
	v_add3_u32 v17, v17, v19, s45
	v_and_or_b32 v17, v17, s44, v18
	v_mul_lo_u32 v18, v74, s43
	v_add3_u32 v18, 0, v18, v54
	ds_write_b128 v18, v[2:5]
	ds_write_b128 v18, v[6:9] offset:128
	ds_write_b128 v18, v[10:13] offset:256
	ds_write_b128 v18, v[14:17] offset:384
	v_add_u32_e32 v2, 0x200, v73
	v_cmp_lt_i32_e32 vcc, s46, v73
	v_add_u32_e32 v72, 0x1000, v72
	s_or_b64 s[20:21], vcc, s[20:21]
	v_mov_b32_e32 v73, v2
	s_andn2_b64 exec, exec, s[20:21]
	s_cbranch_execz .LBB0_2382

.LBB0_2446:
	s_waitcnt vmcnt(0)
	v_lshlrev_b32_e32 v96, 16, v33
	v_lshlrev_b32_e32 v54, 16, v29
	v_mul_f32_e32 v97, v121, v96
	v_fma_f32 v125, v120, v54, -v97
	v_mul_f32_e32 v54, v121, v54
	v_fmac_f32_e32 v54, v120, v96
	v_lshlrev_b32_e32 v96, 16, v28
	v_lshlrev_b32_e32 v97, 16, v32
	v_mul_f32_e32 v120, v119, v97
	v_mul_f32_e32 v119, v119, v96
	v_fma_f32 v120, v118, v96, -v120
	v_fmac_f32_e32 v119, v118, v97
	v_lshlrev_b32_e32 v96, 16, v27
	v_lshlrev_b32_e32 v97, 16, v31
	v_mul_f32_e32 v118, v117, v97
	v_mul_f32_e32 v117, v117, v96
	v_fmac_f32_e32 v117, v116, v97
	v_lshlrev_b32_e32 v97, 16, v30
	v_fma_f32 v118, v116, v96, -v118
	v_lshlrev_b32_e32 v96, 16, v26
	v_mul_f32_e32 v116, v113, v97
	v_fma_f32 v116, v112, v96, -v116
	v_mul_f32_e32 v121, v113, v96
	v_and_b32_e32 v96, 0xffff0000, v30
	v_fmac_f32_e32 v121, v112, v97
	v_and_b32_e32 v97, 0xffff0000, v26
	v_mul_f32_e32 v26, v109, v96
	v_pk_fma_f32 v[112:113], v[108:109], v[96:97], v[26:27] op_sel:[0,1,0] op_sel_hi:[1,0,0] neg_lo:[0,0,1] neg_hi:[0,0,1]
	v_mul_f32_e32 v26, v109, v97
	v_pk_fma_f32 v[96:97], v[108:109], v[96:97], v[26:27] op_sel_hi:[1,1,0]
	v_cvt_pk_bf16_f32 v30, v116, v112
	v_bfe_u32 v26, v121, 16, 1
	v_add3_u32 v26, v121, v26, s45
	v_bfe_u32 v97, v96, 16, 1
	v_lshrrev_b32_e32 v26, 16, v26
	v_add3_u32 v96, v96, v97, s45
	v_and_or_b32 v26, v96, s44, v26
	v_and_b32_e32 v96, 0xffff0000, v31
	v_and_b32_e32 v97, 0xffff0000, v27
	v_mul_f32_e32 v108, v111, v96
	v_pk_fma_f32 v[108:109], v[110:111], v[96:97], v[108:109] op_sel:[0,1,0] op_sel_hi:[1,0,0] neg_lo:[0,0,1] neg_hi:[0,0,1]
	v_mul_f32_e32 v112, v111, v97
	v_pk_fma_f32 v[96:97], v[110:111], v[96:97], v[112:113] op_sel_hi:[1,1,0]
	v_cvt_pk_bf16_f32 v31, v118, v108
	v_bfe_u32 v27, v117, 16, 1
	v_add3_u32 v27, v117, v27, s45
	v_bfe_u32 v97, v96, 16, 1
	v_lshrrev_b32_e32 v27, 16, v27
	v_add3_u32 v96, v96, v97, s45
	v_and_or_b32 v27, v96, s44, v27
	v_and_b32_e32 v96, 0xffff0000, v32
	v_and_b32_e32 v97, 0xffff0000, v28
	v_mul_f32_e32 v28, v115, v96
	v_pk_fma_f32 v[108:109], v[114:115], v[96:97], v[28:29] op_sel:[0,1,0] op_sel_hi:[1,0,0] neg_lo:[0,0,1] neg_hi:[0,0,1]
	v_mul_f32_e32 v28, v115, v97
	v_pk_fma_f32 v[96:97], v[114:115], v[96:97], v[28:29] op_sel_hi:[1,1,0]
	v_cvt_pk_bf16_f32 v32, v120, v108
	v_bfe_u32 v28, v119, 16, 1
	v_add3_u32 v28, v119, v28, s45
	v_bfe_u32 v97, v96, 16, 1
	v_lshrrev_b32_e32 v28, 16, v28
	v_add3_u32 v96, v96, v97, s45
	v_and_or_b32 v28, v96, s44, v28
	v_and_b32_e32 v96, 0xffff0000, v33
	v_lshlrev_b32_e32 v33, 16, v25
	v_and_b32_e32 v97, 0xffff0000, v29
	v_lshlrev_b32_e32 v29, 16, v21
	v_mul_f32_e32 v108, v107, v33
	v_fma_f32 v108, v106, v29, -v108
	v_mul_f32_e32 v29, v107, v29
	v_fmac_f32_e32 v29, v106, v33
	v_lshlrev_b32_e32 v106, 16, v24
	v_lshlrev_b32_e32 v33, 16, v20
	v_mul_f32_e32 v107, v105, v106
	v_fma_f32 v107, v104, v33, -v107
	v_mul_f32_e32 v33, v105, v33
	v_lshlrev_b32_e32 v105, 16, v23
	v_fmac_f32_e32 v33, v104, v106
	v_lshlrev_b32_e32 v104, 16, v19
	v_mul_f32_e32 v106, v103, v105
	v_fma_f32 v106, v102, v104, -v106
	v_mul_f32_e32 v104, v103, v104
	v_fmac_f32_e32 v104, v102, v105
	v_lshlrev_b32_e32 v102, 16, v18
	v_lshlrev_b32_e32 v103, 16, v22
	v_mul_f32_e32 v105, v95, v103
	v_mul_f32_e32 v109, v95, v102
	v_fma_f32 v105, v94, v102, -v105
	v_fmac_f32_e32 v109, v94, v103
	v_and_b32_e32 v94, 0xffff0000, v22
	v_and_b32_e32 v95, 0xffff0000, v18
	v_mul_f32_e32 v18, v91, v94
	v_pk_fma_f32 v[102:103], v[90:91], v[94:95], v[18:19] op_sel:[0,1,0] op_sel_hi:[1,0,0] neg_lo:[0,0,1] neg_hi:[0,0,1]
	v_mul_f32_e32 v18, v91, v95
	v_pk_fma_f32 v[90:91], v[90:91], v[94:95], v[18:19] op_sel_hi:[1,1,0]
	v_cvt_pk_bf16_f32 v22, v105, v102
	v_bfe_u32 v18, v109, 16, 1
	v_add3_u32 v18, v109, v18, s45
	v_bfe_u32 v91, v90, 16, 1
	v_lshrrev_b32_e32 v18, 16, v18
	v_add3_u32 v90, v90, v91, s45
	v_and_or_b32 v18, v90, s44, v18
	v_and_b32_e32 v90, 0xffff0000, v23
	v_and_b32_e32 v91, 0xffff0000, v19
	v_mul_f32_e32 v94, v93, v90
	v_pk_fma_f32 v[94:95], v[92:93], v[90:91], v[94:95] op_sel:[0,1,0] op_sel_hi:[1,0,0] neg_lo:[0,0,1] neg_hi:[0,0,1]
	v_mul_f32_e32 v102, v93, v91
	v_pk_fma_f32 v[90:91], v[92:93], v[90:91], v[102:103] op_sel_hi:[1,1,0]
	v_cvt_pk_bf16_f32 v23, v106, v94
	v_bfe_u32 v19, v104, 16, 1
	v_add3_u32 v19, v104, v19, s45
	v_bfe_u32 v91, v90, 16, 1
	v_lshrrev_b32_e32 v19, 16, v19
	v_add3_u32 v90, v90, v91, s45
	v_and_or_b32 v19, v90, s44, v19
	v_and_b32_e32 v90, 0xffff0000, v24
	v_and_b32_e32 v91, 0xffff0000, v20
	v_mul_f32_e32 v20, v99, v90
	v_pk_fma_f32 v[92:93], v[98:99], v[90:91], v[20:21] op_sel:[0,1,0] op_sel_hi:[1,0,0] neg_lo:[0,0,1] neg_hi:[0,0,1]
	v_mul_f32_e32 v20, v99, v91
	v_pk_fma_f32 v[90:91], v[98:99], v[90:91], v[20:21] op_sel_hi:[1,1,0]
	v_cvt_pk_bf16_f32 v24, v107, v92
	v_bfe_u32 v20, v33, 16, 1
	v_add3_u32 v20, v33, v20, s45
	v_bfe_u32 v33, v90, 16, 1
	v_add3_u32 v33, v90, v33, s45
	v_and_b32_e32 v90, 0xffff0000, v25
	v_and_b32_e32 v91, 0xffff0000, v21
	v_mul_f32_e32 v92, v101, v90
	v_pk_fma_f32 v[92:93], v[100:101], v[90:91], v[92:93] op_sel:[0,1,0] op_sel_hi:[1,0,0] neg_lo:[0,0,1] neg_hi:[0,0,1]
	v_mul_f32_e32 v94, v101, v91
	v_pk_fma_f32 v[90:91], v[100:101], v[90:91], v[94:95] op_sel_hi:[1,1,0]
	v_cvt_pk_bf16_f32 v25, v108, v92
	v_bfe_u32 v21, v29, 16, 1
	v_lshrrev_b32_e32 v20, 16, v20
	v_add3_u32 v21, v29, v21, s45
	v_bfe_u32 v29, v90, 16, 1
	v_and_or_b32 v20, v33, s44, v20
	v_lshrrev_b32_e32 v21, 16, v21
	v_add3_u32 v29, v90, v29, s45
	v_lshlrev_b32_e32 v33, 16, v17
	v_and_or_b32 v21, v29, s44, v21
	v_lshlrev_b32_e32 v29, 16, v13
	v_mul_f32_e32 v90, v87, v33
	v_fma_f32 v90, v86, v29, -v90
	v_mul_f32_e32 v29, v87, v29
	v_fmac_f32_e32 v29, v86, v33
	v_lshlrev_b32_e32 v86, 16, v16
	v_lshlrev_b32_e32 v33, 16, v12
	v_mul_f32_e32 v87, v85, v86
	v_fma_f32 v87, v84, v33, -v87
	v_mul_f32_e32 v33, v85, v33
	v_lshlrev_b32_e32 v85, 16, v15
	v_fmac_f32_e32 v33, v84, v86
	v_lshlrev_b32_e32 v84, 16, v11
	v_mul_f32_e32 v86, v83, v85
	v_fma_f32 v86, v82, v84, -v86
	v_mul_f32_e32 v84, v83, v84
	v_fmac_f32_e32 v84, v82, v85
	v_lshlrev_b32_e32 v82, 16, v10
	v_lshlrev_b32_e32 v83, 16, v14
	v_mul_f32_e32 v85, v77, v83
	v_mul_f32_e32 v91, v77, v82
	v_fma_f32 v85, v76, v82, -v85
	v_fmac_f32_e32 v91, v76, v83
	v_and_b32_e32 v76, 0xffff0000, v14
	v_and_b32_e32 v77, 0xffff0000, v10
	v_mul_f32_e32 v10, v73, v76
	v_pk_fma_f32 v[82:83], v[72:73], v[76:77], v[10:11] op_sel:[0,1,0] op_sel_hi:[1,0,0] neg_lo:[0,0,1] neg_hi:[0,0,1]
	v_mul_f32_e32 v10, v73, v77
	v_pk_fma_f32 v[72:73], v[72:73], v[76:77], v[10:11] op_sel_hi:[1,1,0]
	v_cvt_pk_bf16_f32 v14, v85, v82
	v_bfe_u32 v10, v91, 16, 1
	v_add3_u32 v10, v91, v10, s45
	v_bfe_u32 v73, v72, 16, 1
	v_lshrrev_b32_e32 v10, 16, v10
	v_add3_u32 v72, v72, v73, s45
	v_and_or_b32 v10, v72, s44, v10
	v_and_b32_e32 v72, 0xffff0000, v15
	v_and_b32_e32 v73, 0xffff0000, v11
	v_mul_f32_e32 v76, v75, v72
	v_pk_fma_f32 v[76:77], v[74:75], v[72:73], v[76:77] op_sel:[0,1,0] op_sel_hi:[1,0,0] neg_lo:[0,0,1] neg_hi:[0,0,1]
	v_mul_f32_e32 v82, v75, v73
	v_pk_fma_f32 v[72:73], v[74:75], v[72:73], v[82:83] op_sel_hi:[1,1,0]
	v_cvt_pk_bf16_f32 v15, v86, v76
	v_bfe_u32 v11, v84, 16, 1
	v_add3_u32 v11, v84, v11, s45
	v_bfe_u32 v73, v72, 16, 1
	v_lshrrev_b32_e32 v11, 16, v11
	v_add3_u32 v72, v72, v73, s45
	v_and_or_b32 v11, v72, s44, v11
	v_and_b32_e32 v72, 0xffff0000, v16
	v_and_b32_e32 v73, 0xffff0000, v12
	v_mul_f32_e32 v12, v79, v72
	v_pk_fma_f32 v[74:75], v[78:79], v[72:73], v[12:13] op_sel:[0,1,0] op_sel_hi:[1,0,0] neg_lo:[0,0,1] neg_hi:[0,0,1]
	v_mul_f32_e32 v12, v79, v73
	v_pk_fma_f32 v[72:73], v[78:79], v[72:73], v[12:13] op_sel_hi:[1,1,0]
	v_cvt_pk_bf16_f32 v16, v87, v74
	v_bfe_u32 v12, v33, 16, 1
	v_add3_u32 v12, v33, v12, s45
	v_bfe_u32 v33, v72, 16, 1
	v_add3_u32 v33, v72, v33, s45
	v_and_b32_e32 v72, 0xffff0000, v17
	v_and_b32_e32 v73, 0xffff0000, v13
	v_mul_f32_e32 v74, v81, v72
	v_pk_fma_f32 v[74:75], v[80:81], v[72:73], v[74:75] op_sel:[0,1,0] op_sel_hi:[1,0,0] neg_lo:[0,0,1] neg_hi:[0,0,1]
	v_mul_f32_e32 v76, v81, v73
	v_pk_fma_f32 v[72:73], v[80:81], v[72:73], v[76:77] op_sel_hi:[1,1,0]
	v_cvt_pk_bf16_f32 v17, v90, v74
	v_bfe_u32 v13, v29, 16, 1
	v_lshrrev_b32_e32 v12, 16, v12
	v_add3_u32 v13, v29, v13, s45
	v_bfe_u32 v29, v72, 16, 1
	v_and_or_b32 v12, v33, s44, v12
	v_lshrrev_b32_e32 v13, 16, v13
	v_add3_u32 v29, v72, v29, s45
	v_lshlrev_b32_e32 v33, 16, v9
	v_and_or_b32 v13, v29, s44, v13
	v_lshlrev_b32_e32 v29, 16, v5
	v_mul_f32_e32 v72, v71, v33
	v_fma_f32 v72, v70, v29, -v72
	v_mul_f32_e32 v29, v71, v29
	v_fmac_f32_e32 v29, v70, v33
	v_lshlrev_b32_e32 v70, 16, v8
	v_lshlrev_b32_e32 v33, 16, v4
	v_mul_f32_e32 v71, v69, v70
	v_fma_f32 v71, v68, v33, -v71
	v_mul_f32_e32 v33, v69, v33
	v_lshlrev_b32_e32 v69, 16, v7
	v_fmac_f32_e32 v33, v68, v70
	v_lshlrev_b32_e32 v68, 16, v3
	v_mul_f32_e32 v70, v67, v69
	v_fma_f32 v70, v66, v68, -v70
	v_mul_f32_e32 v68, v67, v68
	v_fmac_f32_e32 v68, v66, v69
	v_lshlrev_b32_e32 v66, 16, v2
	v_lshlrev_b32_e32 v67, 16, v6
	v_mul_f32_e32 v69, v61, v67
	v_mul_f32_e32 v73, v61, v66
	v_fma_f32 v69, v60, v66, -v69
	v_fmac_f32_e32 v73, v60, v67
	v_and_b32_e32 v60, 0xffff0000, v6
	v_and_b32_e32 v61, 0xffff0000, v2
	v_mul_f32_e32 v2, v57, v60
	v_pk_fma_f32 v[66:67], v[56:57], v[60:61], v[2:3] op_sel:[0,1,0] op_sel_hi:[1,0,0] neg_lo:[0,0,1] neg_hi:[0,0,1]
	v_mul_f32_e32 v2, v57, v61
	v_pk_fma_f32 v[56:57], v[56:57], v[60:61], v[2:3] op_sel_hi:[1,1,0]
	v_cvt_pk_bf16_f32 v2, v69, v66
	v_bfe_u32 v6, v73, 16, 1
	v_add3_u32 v6, v73, v6, s45
	v_bfe_u32 v57, v56, 16, 1
	v_lshrrev_b32_e32 v6, 16, v6
	v_add3_u32 v56, v56, v57, s45
	v_and_or_b32 v6, v56, s44, v6
	v_and_b32_e32 v56, 0xffff0000, v7
	v_and_b32_e32 v57, 0xffff0000, v3
	v_mul_f32_e32 v60, v59, v56
	v_pk_fma_f32 v[60:61], v[58:59], v[56:57], v[60:61] op_sel:[0,1,0] op_sel_hi:[1,0,0] neg_lo:[0,0,1] neg_hi:[0,0,1]
	v_mul_f32_e32 v66, v59, v57
	v_pk_fma_f32 v[56:57], v[58:59], v[56:57], v[66:67] op_sel_hi:[1,1,0]
	v_cvt_pk_bf16_f32 v3, v70, v60
	v_bfe_u32 v7, v68, 16, 1
	v_add3_u32 v7, v68, v7, s45
	v_bfe_u32 v57, v56, 16, 1
	v_lshrrev_b32_e32 v7, 16, v7
	v_add3_u32 v56, v56, v57, s45
	v_and_or_b32 v7, v56, s44, v7
	v_and_b32_e32 v56, 0xffff0000, v8
	v_and_b32_e32 v57, 0xffff0000, v4
	v_mul_f32_e32 v4, v63, v56
	v_pk_fma_f32 v[58:59], v[62:63], v[56:57], v[4:5] op_sel:[0,1,0] op_sel_hi:[1,0,0] neg_lo:[0,0,1] neg_hi:[0,0,1]
	v_mul_f32_e32 v4, v63, v57
	v_pk_fma_f32 v[56:57], v[62:63], v[56:57], v[4:5] op_sel_hi:[1,1,0]
	v_cvt_pk_bf16_f32 v4, v71, v58
	v_bfe_u32 v8, v33, 16, 1
	v_add3_u32 v8, v33, v8, s45
	v_bfe_u32 v33, v56, 16, 1
	v_add3_u32 v33, v56, v33, s45
	v_and_b32_e32 v56, 0xffff0000, v9
	v_and_b32_e32 v57, 0xffff0000, v5
	v_mul_f32_e32 v58, v65, v56
	v_pk_fma_f32 v[58:59], v[64:65], v[56:57], v[58:59] op_sel:[0,1,0] op_sel_hi:[1,0,0] neg_lo:[0,0,1] neg_hi:[0,0,1]
	v_mul_f32_e32 v60, v65, v57
	v_pk_fma_f32 v[56:57], v[64:65], v[56:57], v[60:61] op_sel_hi:[1,1,0]
	v_cvt_pk_bf16_f32 v5, v72, v58
	v_bfe_u32 v9, v29, 16, 1
	v_add3_u32 v9, v29, v9, s45
	v_bfe_u32 v29, v56, 16, 1
	v_lshrrev_b32_e32 v9, 16, v9
	v_add3_u32 v29, v56, v29, s45
	v_mul_f32_e32 v56, v89, v96
	v_lshrrev_b32_e32 v8, 16, v8
	v_and_or_b32 v9, v29, s44, v9
	v_pk_fma_f32 v[56:57], v[88:89], v[96:97], v[56:57] op_sel:[0,1,0] op_sel_hi:[1,0,0] neg_lo:[0,0,1] neg_hi:[0,0,1]
	v_and_or_b32 v8, v33, s44, v8
	s_ashr_i32 s13, s12, 31
	v_mul_f32_e32 v58, v89, v97
	s_lshl_b64 s[8:9], s[12:13], 16
	v_pk_fma_f32 v[58:59], v[88:89], v[96:97], v[58:59] op_sel_hi:[1,1,0]
	v_cvt_pk_bf16_f32 v33, v125, v56
	v_bfe_u32 v29, v54, 16, 1
	v_lshl_add_u64 v[56:57], v[52:53], 0, s[8:9]
	v_add3_u32 v29, v54, v29, s45
	v_bfe_u32 v54, v58, 16, 1
	global_store_dwordx4 v[56:57], v[2:5], off
	global_store_dwordx4 v[56:57], v[14:17], off offset:1024
	global_store_dwordx4 v[56:57], v[6:9], off offset:2048
	global_store_dwordx4 v[56:57], v[10:13], off offset:3072
	v_add_co_u32_e32 v56, vcc, s42, v56
	v_lshrrev_b32_e32 v29, 16, v29
	v_add3_u32 v54, v58, v54, s45
	v_addc_co_u32_e32 v57, vcc, 0, v57, vcc
	v_and_or_b32 v29, v54, s44, v29
	global_store_dwordx4 v[56:57], v[22:25], off
	global_store_dwordx4 v[56:57], v[30:33], off offset:1024
	global_store_dwordx4 v[56:57], v[18:21], off offset:2048
	global_store_dwordx4 v[56:57], v[26:29], off offset:3072
	s_waitcnt lgkmcnt(0)
	s_barrier
	ds_read_b128 v[56:59], v123
	ds_read_b128 v[60:63], v123 offset:64
	ds_read_b128 v[64:67], v123 offset:8448
	ds_read_b128 v[68:71], v123 offset:8512
	ds_read_b128 v[72:75], v123 offset:16896
	ds_read_b128 v[76:79], v123 offset:16960
	ds_read_b128 v[80:83], v123 offset:25344
	ds_read_b128 v[84:87], v123 offset:25408
	ds_read_b128 v[88:91], v123 offset:33792
	ds_read_b128 v[92:95], v123 offset:33856
	ds_read_b128 v[96:99], v123 offset:42240
	ds_read_b128 v[100:103], v123 offset:42304
	ds_read_b128 v[104:107], v123 offset:50688
	ds_read_b128 v[108:111], v123 offset:50752
	ds_read_b128 v[112:115], v123 offset:59136
	ds_read_b128 v[116:119], v123 offset:59200
	s_waitcnt lgkmcnt(14)
	v_mfma_f32_16x16x32_bf16 v[56:59], v[56:59], v[2:5], 0
	s_lshl_b64 s[8:9], s[12:13], 15
	s_add_u32 s14, s36, s8
	s_addc_u32 s15, s37, s9
	s_waitcnt lgkmcnt(13)
	v_mfma_f32_16x16x32_bf16 v[64:67], v[64:67], v[2:5], 0
	s_waitcnt lgkmcnt(11)
	v_mfma_f32_16x16x32_bf16 v[72:75], v[72:75], v[2:5], 0
	s_waitcnt lgkmcnt(9)
	v_mfma_f32_16x16x32_bf16 v[80:83], v[80:83], v[2:5], 0
	s_waitcnt lgkmcnt(7)
	v_mfma_f32_16x16x32_bf16 v[88:91], v[88:91], v[2:5], 0
	s_waitcnt lgkmcnt(5)
	v_mfma_f32_16x16x32_bf16 v[96:99], v[96:99], v[2:5], 0
	s_waitcnt lgkmcnt(3)
	v_mfma_f32_16x16x32_bf16 v[104:107], v[104:107], v[2:5], 0
	s_waitcnt lgkmcnt(1)
	v_mfma_f32_16x16x32_bf16 v[2:5], v[112:115], v[2:5], 0
	v_mfma_f32_16x16x32_bf16 v[56:59], v[60:63], v[14:17], v[56:59]
	v_mfma_f32_16x16x32_bf16 v[60:63], v[68:71], v[14:17], v[64:67]
	v_mfma_f32_16x16x32_bf16 v[64:67], v[76:79], v[14:17], v[72:75]
	v_mfma_f32_16x16x32_bf16 v[68:71], v[84:87], v[14:17], v[80:83]
	v_mfma_f32_16x16x32_bf16 v[72:75], v[92:95], v[14:17], v[88:91]
	v_mfma_f32_16x16x32_bf16 v[76:79], v[100:103], v[14:17], v[96:99]
	v_mfma_f32_16x16x32_bf16 v[80:83], v[108:111], v[14:17], v[104:107]
	s_waitcnt lgkmcnt(0)
	v_mfma_f32_16x16x32_bf16 v[2:5], v[116:119], v[14:17], v[2:5]
	ds_read_b128 v[14:17], v123 offset:128
	ds_read_b128 v[84:87], v123 offset:192
	s_waitcnt lgkmcnt(1)
	v_mfma_f32_16x16x32_bf16 v[14:17], v[14:17], v[6:9], v[56:59]
	s_nop 2
	ds_read_b128 v[56:59], v123 offset:8576
	ds_read_b128 v[88:91], v123 offset:8640
	s_waitcnt lgkmcnt(1)
	v_mfma_f32_16x16x32_bf16 v[56:59], v[56:59], v[6:9], v[60:63]
	s_nop 2
	ds_read_b128 v[60:63], v123 offset:17024
	ds_read_b128 v[92:95], v123 offset:17088
	s_waitcnt lgkmcnt(1)
	v_mfma_f32_16x16x32_bf16 v[60:63], v[60:63], v[6:9], v[64:67]
	s_nop 2
	ds_read_b128 v[64:67], v123 offset:25472
	ds_read_b128 v[96:99], v123 offset:25536
	s_waitcnt lgkmcnt(1)
	v_mfma_f32_16x16x32_bf16 v[64:67], v[64:67], v[6:9], v[68:71]
	s_nop 2
	ds_read_b128 v[68:71], v123 offset:33920
	ds_read_b128 v[100:103], v123 offset:33984
	s_waitcnt lgkmcnt(1)
	v_mfma_f32_16x16x32_bf16 v[68:71], v[68:71], v[6:9], v[72:75]
	s_nop 2
	ds_read_b128 v[72:75], v123 offset:42368
	ds_read_b128 v[104:107], v123 offset:42432
	s_waitcnt lgkmcnt(1)
	v_mfma_f32_16x16x32_bf16 v[72:75], v[72:75], v[6:9], v[76:79]
	s_nop 2
	ds_read_b128 v[76:79], v123 offset:50816
	ds_read_b128 v[108:111], v123 offset:50880
	s_waitcnt lgkmcnt(1)
	v_mfma_f32_16x16x32_bf16 v[76:79], v[76:79], v[6:9], v[80:83]
	s_nop 2
	ds_read_b128 v[80:83], v123 offset:59264
	ds_read_b128 v[112:115], v123 offset:59328
	s_waitcnt lgkmcnt(1)
	v_mfma_f32_16x16x32_bf16 v[2:5], v[80:83], v[6:9], v[2:5]
	v_mfma_f32_16x16x32_bf16 v[6:9], v[84:87], v[10:13], v[14:17]
	v_mfma_f32_16x16x32_bf16 v[14:17], v[88:91], v[10:13], v[56:59]
	v_mfma_f32_16x16x32_bf16 v[56:59], v[92:95], v[10:13], v[60:63]
	v_mfma_f32_16x16x32_bf16 v[60:63], v[96:99], v[10:13], v[64:67]
	v_mfma_f32_16x16x32_bf16 v[64:67], v[100:103], v[10:13], v[68:71]
	v_mfma_f32_16x16x32_bf16 v[68:71], v[104:107], v[10:13], v[72:75]
	v_mfma_f32_16x16x32_bf16 v[72:75], v[108:111], v[10:13], v[76:79]
	s_waitcnt lgkmcnt(0)
	v_mfma_f32_16x16x32_bf16 v[2:5], v[112:115], v[10:13], v[2:5]
	ds_read_b128 v[10:13], v123 offset:256
	ds_read_b128 v[76:79], v123 offset:320
	s_waitcnt lgkmcnt(1)
	v_mfma_f32_16x16x32_bf16 v[6:9], v[10:13], v[22:25], v[6:9]
	ds_read_b128 v[10:13], v123 offset:8704
	ds_read_b128 v[80:83], v123 offset:8768
	s_waitcnt lgkmcnt(1)
	v_mfma_f32_16x16x32_bf16 v[10:13], v[10:13], v[22:25], v[14:17]
	s_nop 2
	ds_read_b128 v[14:17], v123 offset:17152
	ds_read_b128 v[84:87], v123 offset:17216
	s_waitcnt lgkmcnt(1)
	v_mfma_f32_16x16x32_bf16 v[14:17], v[14:17], v[22:25], v[56:59]
	s_nop 2
	ds_read_b128 v[56:59], v123 offset:25600
	ds_read_b128 v[88:91], v123 offset:25664
	s_waitcnt lgkmcnt(1)
	v_mfma_f32_16x16x32_bf16 v[56:59], v[56:59], v[22:25], v[60:63]
	s_nop 2
	ds_read_b128 v[60:63], v123 offset:34048
	ds_read_b128 v[92:95], v123 offset:34112
	s_waitcnt lgkmcnt(1)
	v_mfma_f32_16x16x32_bf16 v[60:63], v[60:63], v[22:25], v[64:67]
	s_nop 2
	ds_read_b128 v[64:67], v123 offset:42496
	ds_read_b128 v[96:99], v123 offset:42560
	s_waitcnt lgkmcnt(1)
	v_mfma_f32_16x16x32_bf16 v[64:67], v[64:67], v[22:25], v[68:71]
	s_nop 2
	ds_read_b128 v[68:71], v123 offset:50944
	ds_read_b128 v[100:103], v123 offset:51008
	s_waitcnt lgkmcnt(1)
	v_mfma_f32_16x16x32_bf16 v[68:71], v[68:71], v[22:25], v[72:75]
	s_nop 2
	ds_read_b128 v[72:75], v123 offset:59392
	ds_read_b128 v[104:107], v123 offset:59456
	s_waitcnt lgkmcnt(1)
	v_mfma_f32_16x16x32_bf16 v[2:5], v[72:75], v[22:25], v[2:5]
	v_mfma_f32_16x16x32_bf16 v[6:9], v[76:79], v[30:33], v[6:9]
	v_mfma_f32_16x16x32_bf16 v[10:13], v[80:83], v[30:33], v[10:13]
	v_mfma_f32_16x16x32_bf16 v[14:17], v[84:87], v[30:33], v[14:17]
	v_mfma_f32_16x16x32_bf16 v[22:25], v[88:91], v[30:33], v[56:59]
	v_mfma_f32_16x16x32_bf16 v[56:59], v[92:95], v[30:33], v[60:63]
	v_mfma_f32_16x16x32_bf16 v[60:63], v[96:99], v[30:33], v[64:67]
	v_mfma_f32_16x16x32_bf16 v[64:67], v[100:103], v[30:33], v[68:71]
	s_waitcnt lgkmcnt(0)
	v_mfma_f32_16x16x32_bf16 v[2:5], v[104:107], v[30:33], v[2:5]
	ds_read_b128 v[30:33], v123 offset:384
	ds_read_b128 v[68:71], v123 offset:448
	s_waitcnt lgkmcnt(1)
	v_mfma_f32_16x16x32_bf16 v[6:9], v[30:33], v[18:21], v[6:9]
	ds_read_b128 v[30:33], v123 offset:8832
	ds_read_b128 v[72:75], v123 offset:8896
	s_waitcnt lgkmcnt(1)
	v_mfma_f32_16x16x32_bf16 v[10:13], v[30:33], v[18:21], v[10:13]
	ds_read_b128 v[30:33], v123 offset:17280
	ds_read_b128 v[76:79], v123 offset:17344
	s_waitcnt lgkmcnt(1)
	v_mfma_f32_16x16x32_bf16 v[14:17], v[30:33], v[18:21], v[14:17]
	ds_read_b128 v[30:33], v123 offset:25728
	ds_read_b128 v[80:83], v123 offset:25792
	s_waitcnt lgkmcnt(1)
	v_mfma_f32_16x16x32_bf16 v[22:25], v[30:33], v[18:21], v[22:25]
	ds_read_b128 v[30:33], v123 offset:34176
	ds_read_b128 v[84:87], v123 offset:34240
	s_waitcnt lgkmcnt(1)
	v_mfma_f32_16x16x32_bf16 v[30:33], v[30:33], v[18:21], v[56:59]
	s_nop 2
	ds_read_b128 v[56:59], v123 offset:42624
	ds_read_b128 v[88:91], v123 offset:42688
	s_waitcnt lgkmcnt(1)
	v_mfma_f32_16x16x32_bf16 v[56:59], v[56:59], v[18:21], v[60:63]
	s_nop 2
	ds_read_b128 v[60:63], v123 offset:51072
	ds_read_b128 v[92:95], v123 offset:51136
	s_waitcnt lgkmcnt(1)
	v_mfma_f32_16x16x32_bf16 v[60:63], v[60:63], v[18:21], v[64:67]
	s_nop 2
	ds_read_b128 v[64:67], v123 offset:59520
	ds_read_b128 v[96:99], v123 offset:59584
	s_waitcnt lgkmcnt(1)
	v_mfma_f32_16x16x32_bf16 v[2:5], v[64:67], v[18:21], v[2:5]
	v_mfma_f32_16x16x32_bf16 v[6:9], v[68:71], v[26:29], v[6:9]
	v_mfma_f32_16x16x32_bf16 v[10:13], v[72:75], v[26:29], v[10:13]
	v_mfma_f32_16x16x32_bf16 v[14:17], v[76:79], v[26:29], v[14:17]
	v_mfma_f32_16x16x32_bf16 v[18:21], v[80:83], v[26:29], v[22:25]
	v_mfma_f32_16x16x32_bf16 v[22:25], v[84:87], v[26:29], v[30:33]
	v_mfma_f32_16x16x32_bf16 v[30:33], v[88:91], v[26:29], v[56:59]
	v_mfma_f32_16x16x32_bf16 v[56:59], v[92:95], v[26:29], v[60:63]
	s_waitcnt lgkmcnt(0)
	v_mfma_f32_16x16x32_bf16 v[2:5], v[96:99], v[26:29], v[2:5]
	v_bfe_u32 v26, v6, 16, 1
	v_add3_u32 v6, v6, v26, s45
	v_bfe_u32 v26, v7, 16, 1
	v_lshrrev_b32_e32 v6, 16, v6
	v_add3_u32 v7, v7, v26, s45
	v_and_or_b32 v6, v7, s44, v6
	v_bfe_u32 v7, v8, 16, 1
	v_add3_u32 v7, v8, v7, s45
	v_bfe_u32 v8, v9, 16, 1
	v_lshrrev_b32_e32 v7, 16, v7
	v_add3_u32 v8, v9, v8, s45
	v_and_or_b32 v7, v8, s44, v7
	v_lshl_add_u64 v[8:9], v[36:37], 1, s[14:15]
	global_store_dwordx2 v[8:9], v[6:7], off
	v_cvt_pk_bf16_f32 v6, v10, v11
	v_cvt_pk_bf16_f32 v7, v12, v13
	v_lshl_add_u64 v[8:9], v[38:39], 1, s[14:15]
	global_store_dwordx2 v[8:9], v[6:7], off
	v_cvt_pk_bf16_f32 v6, v14, v15
	v_cvt_pk_bf16_f32 v7, v16, v17
	v_lshl_add_u64 v[8:9], v[40:41], 1, s[14:15]
	global_store_dwordx2 v[8:9], v[6:7], off
	v_cvt_pk_bf16_f32 v6, v18, v19
	v_cvt_pk_bf16_f32 v7, v20, v21
	v_lshl_add_u64 v[8:9], v[42:43], 1, s[14:15]
	global_store_dwordx2 v[8:9], v[6:7], off
	v_cvt_pk_bf16_f32 v6, v22, v23
	v_cvt_pk_bf16_f32 v7, v24, v25
	v_lshl_add_u64 v[8:9], v[44:45], 1, s[14:15]
	global_store_dwordx2 v[8:9], v[6:7], off
	v_cvt_pk_bf16_f32 v6, v30, v31
	v_cvt_pk_bf16_f32 v7, v32, v33
	v_lshl_add_u64 v[8:9], v[46:47], 1, s[14:15]
	global_store_dwordx2 v[8:9], v[6:7], off
	v_cvt_pk_bf16_f32 v6, v56, v57
	v_cvt_pk_bf16_f32 v7, v58, v59
	v_lshl_add_u64 v[8:9], v[48:49], 1, s[14:15]
	global_store_dwordx2 v[8:9], v[6:7], off
	v_bfe_u32 v6, v2, 16, 1
	v_add3_u32 v2, v2, v6, s45
	v_bfe_u32 v6, v3, 16, 1
	v_lshrrev_b32_e32 v2, 16, v2
	v_add3_u32 v3, v3, v6, s45
	v_and_or_b32 v2, v3, s44, v2
	v_bfe_u32 v3, v4, 16, 1
	v_add3_u32 v3, v4, v3, s45
	v_bfe_u32 v4, v5, 16, 1
	v_lshrrev_b32_e32 v3, 16, v3
	v_add3_u32 v4, v5, v4, s45
	v_and_or_b32 v3, v4, s44, v3
	v_lshl_add_u64 v[4:5], v[50:51], 1, s[14:15]
	global_store_dwordx2 v[4:5], v[2:3], off
	s_and_saveexec_b64 s[14:15], s[6:7]
	s_cbranch_execz .LBB0_2362
	s_lshl_b64 s[8:9], s[8:9], 1
	s_add_u32 s8, s40, s8
	s_addc_u32 s9, s41, s9
	s_mov_b64 s[16:17], 0
	v_mov_b32_e32 v2, v170

.LBB0_2499:
	s_cmp_lt_i32 s92, 33
	s_cselect_b64 s[4:5], -1, 0
	s_cmp_gt_i32 s93, 32
	s_cselect_b64 s[6:7], -1, 0
	s_and_b64 s[4:5], s[4:5], s[6:7]
	s_andn2_b64 vcc, exec, s[4:5]
	s_cbranch_vccnz .LBB0_2587
	s_cmp_lt_u32 s88, 4
	s_cbranch_scc1 .Lmy_prio_skip32
	s_setprio 2
.Lmy_prio_skip32:
	s_mov_b32 s75, s89
	s_cmpk_gt_i32 s89, 0xff
	s_mov_b32 s6, 11
	s_mov_b32 s4, 12
	s_cbranch_scc1 .LBB0_2536
	s_lshr_b32 s3, s90, 7
	s_add_u32 s18, s26, 0x32d00000
	s_addc_u32 s19, s27, 0
	s_add_u32 s81, s26, 0x21d00000
	s_addc_u32 s82, s27, 0
	s_add_u32 s83, s26, 0x3d700000
	s_addc_u32 s84, s27, 0
	s_ashr_i32 s7, s6, 31
	s_lshl_b64 s[6:7], s[6:7], 3
	s_add_u32 s6, s0, s6
	s_addc_u32 s7, s1, s7
	s_ashr_i32 s5, s4, 31
	s_lshl_b64 s[4:5], s[4:5], 3
	s_add_u32 s4, s0, s4
	s_addc_u32 s5, s1, s5
	s_load_dwordx2 s[20:21], s[6:7], 0x0
	s_load_dwordx2 s[22:23], s[4:5], 0x0
	v_readlane_b32 s6, v255, 10
	v_and_b32_e32 v1, 15, v250
	s_lshl_b32 s5, s6, 12
	s_waitcnt vmcnt(0)
	v_lshl_or_b32 v65, s6, 4, v1
	v_add_u32_e32 v2, 0xffffff81, v65
	v_cvt_f32_i32_e32 v202, v2
	v_ashrrev_i32_e32 v2, 1, v250
	v_and_b32_e32 v203, -8, v2
	v_bfe_u32 v2, v250, 2, 2
	v_or_b32_e32 v2, v203, v2
	s_movk_i32 s6, 0x90
	v_lshlrev_b32_e32 v3, 3, v250
	v_mul_lo_u32 v2, v2, s6
	v_and_b32_e32 v3, 24, v3
	v_lshl_add_u32 v172, v250, 4, s5
	v_mov_b32_e32 v173, 0
	v_add3_u32 v204, 0, v2, v3
	v_ashrrev_i32_e32 v205, 3, v170
	v_lshlrev_b32_e32 v2, 4, v170
	v_add_u32_e32 v174, s5, v172
	v_mov_b32_e32 v175, v173
	v_mul_lo_u32 v7, v65, s6
	v_and_b32_e32 v8, 0x70, v2
	v_mul_lo_u32 v9, v205, s6
	v_lshl_add_u64 v[2:3], s[26:27], 0, v[172:173]
	s_mov_b64 s[6:7], 0x37100000
	v_lshl_add_u64 v[178:179], v[2:3], 0, s[6:7]
	v_lshl_add_u64 v[2:3], s[26:27], 0, v[174:175]
	s_mov_b64 s[6:7], 0x34f00000
	s_and_b32 s4, s90, 0xffffffc0
	v_cvt_f32_u32_e32 v201, v65
	v_lshl_add_u64 v[182:183], v[2:3], 0, s[6:7]
	v_lshlrev_b32_e32 v2, 3, v170
	s_add_i32 s4, s4, 0
	s_add_i32 s8, 0, 0x11400
	v_and_b32_e32 v2, 56, v2
	v_lshlrev_b32_e32 v4, 1, v203
	v_add_u32_e32 v5, s8, v203
	v_add_u32_e32 v6, s4, v203
	v_mul_u32_u24_e32 v1, 0x210, v1
	s_movk_i32 s4, 0x2100
	v_lshlrev_b32_e32 v3, 1, v2
	s_mov_b32 s41, 0
	v_sub_u32_e32 v171, 0x80, v65
	v_add_u32_e32 v200, 1, v65
	v_cmp_gt_i32_e64 s[4:5], s4, v170
	v_lshl_or_b32 v176, v205, 10, v8
	v_sub_u32_e32 v206, 0x7f, v205
	v_sub_u32_e32 v207, 63, v205
	v_add_u32_e32 v208, 64, v205
	v_mov_b32_e32 v177, v173
	v_lshl_add_u64 v[180:181], s[18:19], 0, v[174:175]
	v_add3_u32 v209, 0, v9, v8
	v_add3_u32 v210, s8, v9, v3
	v_add3_u32 v211, 0, v4, v1
	v_add_u32_e32 v212, 0xfffffe00, v170
	v_lshl_add_u32 v213, v170, 2, 0
	v_mov_b32_e32 v214, 0x42000000
	s_mov_b32 s85, 0xc2fc0000
	v_mov_b32_e32 v215, 0x42800000
	s_mov_b64 s[42:43], 0x1000
	s_mov_b32 s86, 0xffff0000
	s_movk_i32 s87, 0x7fff
	v_lshlrev_b32_e32 v172, 1, v2
	v_add_u32_e32 v216, v5, v7
	v_not_b32_e32 v217, 63
	v_mov_b32_e32 v218, 0xffff
	v_mov_b32_e32 v219, 0xffff0000
	v_add_u32_e32 v220, v6, v1
	s_mov_b32 s88, s75
	v_lshrrev_b32_e32 v2, 2, v170
	v_lshrrev_b32_e32 v3, 3, v170
	v_xor_b32_e32 v2, v2, v3
	v_and_b32_e32 v2, 1, v2
	v_bfe_u32 v3, v170, 4, 1
	v_lshlrev_b32_e32 v3, 5, v3
	v_sub_u32_e32 v3, 16, v3
	v_mul_lo_u32 v3, v3, v2
	v_add_u32_e32 v211, v211, v3
	v_bfe_u32 v3, v170, 5, 1
	v_lshlrev_b32_e32 v3, 5, v3
	v_sub_u32_e32 v3, 16, v3
	v_mul_lo_u32 v3, v3, v2
	v_add_u32_e32 v220, v220, v3
	s_branch .LBB0_2503

.LBB0_2587:
	s_setprio 0
	s_cmp_lt_i32 s92, 34
	s_cselect_b64 s[4:5], -1, 0
	s_cmp_gt_i32 s93, 33
	s_cselect_b64 s[6:7], -1, 0
	s_and_b64 s[4:5], s[4:5], s[6:7]
	s_andn2_b64 vcc, exec, s[4:5]
	s_cbranch_vccnz .LBB0_2641
	s_lshl_b32 s3, s89, 3
	s_add_i32 s3, s88, s3
	s_add_i32 s6, s3, 0x400
	s_cmpk_gt_i32 s6, 0x43ff
	s_mov_b32 s10, 13
	s_mov_b32 s4, 14
	s_cbranch_scc1 .LBB0_2591
	s_add_u32 s3, s26, 0x2a500000
	s_addc_u32 s15, s27, 0
	s_ashr_i32 s11, s10, 31
	s_lshl_b32 s8, s34, 3
	s_lshl_b64 s[10:11], s[10:11], 3
	s_add_u32 s12, s0, s10
	s_addc_u32 s13, s1, s11
	s_add_u32 s16, s26, 0x3d700000
	s_addc_u32 s17, s27, 0
	s_ashr_i32 s7, s6, 31
	s_lshl_b64 s[18:19], s[6:7], 12
	s_add_u32 s20, s16, s18
	s_addc_u32 s21, s17, s19
	s_add_u32 s22, s26, 0x41b00000
	s_waitcnt vmcnt(0)
	v_lshlrev_b32_e32 v2, 3, v250
	s_addc_u32 s23, s27, 0
	v_lshlrev_b32_e32 v1, 5, v250
	v_and_b32_e32 v2, 0x78, v2
	s_movk_i32 s5, 0xfe00
	s_add_u32 s28, s22, s18
	v_and_or_b32 v146, v1, s5, v2
	s_addc_u32 s29, s23, s19
	s_lshl_b64 s[10:11], s[6:7], 13
	v_ashrrev_i32_e32 v147, 31, v146
	s_add_u32 s10, s3, s10
	s_addc_u32 s11, s15, s11
	v_lshlrev_b64 v[2:3], 1, v[146:147]
	v_lshl_add_u64 v[4:5], s[10:11], 0, v[2:3]
	s_movk_i32 s7, 0x1000
	s_mov_b64 s[10:11], 0x1000
	v_lshl_add_u64 v[10:11], s[20:21], 0, v[2:3]
	v_add_co_u32_e32 v12, vcc, s7, v4
	v_lshl_add_u64 v[6:7], v[4:5], 0, s[10:11]
	v_lshl_add_u64 v[8:9], s[28:29], 0, v[2:3]
	global_load_dwordx4 v[34:37], v[4:5], off offset:768
	global_load_dwordx4 v[74:77], v[4:5], off offset:512
	global_load_dwordx4 v[78:81], v[6:7], off offset:512
	global_load_dwordx4 v[82:85], v[6:7], off offset:256
	global_load_dwordx4 v[106:109], v[8:9], off offset:512
	global_load_dwordx4 v[122:125], v[8:9], off offset:256
	global_load_dwordx4 v[118:121], v[10:11], off offset:512
	global_load_dwordx4 v[126:129], v[10:11], off offset:256
	v_addc_co_u32_e32 v13, vcc, 0, v5, vcc
	global_load_dwordx4 v[110:113], v[10:11], off offset:768
	global_load_dwordx4 v[94:97], v[12:13], off
	global_load_dwordx4 v[86:89], v[4:5], off offset:256
	global_load_dwordx4 v[90:93], v[4:5], off
	global_load_dwordx4 v[38:41], v[6:7], off offset:768
	global_load_dwordx4 v[130:133], v[8:9], off
	global_load_dwordx4 v[114:117], v[8:9], off offset:768
	global_load_dwordx4 v[134:137], v[10:11], off
	s_ashr_i32 s5, s4, 31
	s_lshl_b64 s[4:5], s[4:5], 3
	s_add_u32 s4, s0, s4
	s_addc_u32 s5, s1, s5
	s_load_dwordx2 s[12:13], s[12:13], 0x0
	s_nop 0
	s_load_dwordx2 s[4:5], s[4:5], 0x0
	v_lshlrev_b64 v[4:5], 2, v[146:147]
	v_lshl_add_u64 v[148:149], s[16:17], 0, v[2:3]
	v_lshl_add_u64 v[150:151], s[22:23], 0, v[2:3]
	s_waitcnt lgkmcnt(0)
	v_lshl_add_u64 v[6:7], s[12:13], 0, v[4:5]
	v_lshl_add_u64 v[4:5], s[4:5], 0, v[4:5]
	s_add_u32 s4, s26, s18
	s_addc_u32 s5, s27, s19
	s_mov_b64 s[12:13], 0x2000
	v_lshl_add_u64 v[2:3], s[4:5], 0, v[2:3]
	s_mov_b64 s[4:5], 0x45f00000
	s_ashr_i32 s9, s8, 31
	v_lshl_add_u64 v[152:153], v[6:7], 0, s[12:13]
	v_lshl_add_u64 v[154:155], v[4:5], 0, s[12:13]
	v_lshl_add_u64 v[156:157], v[2:3], 0, s[4:5]
	s_lshl_b64 s[12:13], s[8:9], 12
	s_mov_b32 s14, 0x3b000000
	v_mov_b32_e32 v1, 0x358637bd
	s_mov_b32 s9, 0xf800000
	v_mov_b32_e32 v171, 0x260
	v_lshlrev_b32_e32 v242, 4, v250
	s_lshl_b32 s98, s88, 14
	v_add_u32_e32 v242, s98, v242
	global_load_dwordx4 v[2:5], v[152:153], off
	global_load_dwordx4 v[6:9], v[152:153], off offset:16
	global_load_dwordx4 v[10:13], v[152:153], off offset:512
	global_load_dwordx4 v[14:17], v[152:153], off offset:528
	global_load_dwordx4 v[18:21], v[152:153], off offset:1024
	global_load_dwordx4 v[22:25], v[152:153], off offset:1040
	global_load_dwordx4 v[26:29], v[152:153], off offset:1536
	global_load_dwordx4 v[30:33], v[152:153], off offset:1552
	global_load_dwordx4 v[42:45], v[154:155], off
	global_load_dwordx4 v[46:49], v[154:155], off offset:16
	global_load_dwordx4 v[50:53], v[154:155], off offset:512
	global_load_dwordx4 v[54:57], v[154:155], off offset:528
	global_load_dwordx4 v[58:61], v[154:155], off offset:1024
	global_load_dwordx4 v[62:65], v[154:155], off offset:1040
	global_load_dwordx4 v[66:69], v[154:155], off offset:1536
	global_load_dwordx4 v[70:73], v[154:155], off offset:1552
	s_waitcnt vmcnt(0)
	ds_write_b128 v242, v[2:5]
	ds_write_b128 v242, v[6:9] offset:1024
	ds_write_b128 v242, v[10:13] offset:2048
	ds_write_b128 v242, v[14:17] offset:3072
	ds_write_b128 v242, v[18:21] offset:4096
	ds_write_b128 v242, v[22:25] offset:5120
	ds_write_b128 v242, v[26:29] offset:6144
	ds_write_b128 v242, v[30:33] offset:7168
	ds_write_b128 v242, v[42:45] offset:8192
	ds_write_b128 v242, v[46:49] offset:9216
	ds_write_b128 v242, v[50:53] offset:10240
	ds_write_b128 v242, v[54:57] offset:11264
	ds_write_b128 v242, v[58:61] offset:12288
	ds_write_b128 v242, v[62:65] offset:13312
	ds_write_b128 v242, v[66:69] offset:14336
	ds_write_b128 v242, v[70:73] offset:15360
	s_waitcnt lgkmcnt(0)

.LBB0_2722:
	global_load_dwordx2 v[60:61], v[50:51], off offset:1536
	global_load_dwordx2 v[62:63], v[50:51], off
	global_load_dwordx2 v[64:65], v[50:51], off offset:512
	global_load_dwordx2 v[66:67], v[50:51], off offset:1024
	s_add_i32 s8, s40, 0x400
	s_lshr_b32 s9, s40, 12
	s_mulk_i32 s9, 0x1800
	s_cmpk_gt_i32 s8, 0x3ff
	s_cselect_b32 s42, s9, 0x6000
	s_lshl_b64 s[8:9], s[42:43], 2
	v_lshl_add_u64 v[86:87], v[32:33], 0, s[8:9]
	v_lshl_add_u64 v[88:89], v[30:31], 0, s[8:9]
	s_waitcnt lgkmcnt(6)
	global_load_dwordx4 v[18:21], v[86:87], off
	s_waitcnt lgkmcnt(4)
	global_load_dwordx4 v[22:25], v[86:87], off offset:1024
	s_waitcnt lgkmcnt(2)
	global_load_dwordx4 v[26:29], v[86:87], off offset:2048
	s_waitcnt lgkmcnt(0)
	global_load_dwordx4 v[52:55], v[88:89], off
	global_load_dwordx4 v[56:59], v[88:89], off offset:1024
	global_load_dwordx4 v[74:77], v[88:89], off offset:2048
	global_load_dwordx4 v[78:81], v[88:89], off offset:3072
	global_load_dwordx4 v[82:85], v[86:87], off offset:3072
	s_waitcnt vmcnt(11)
	v_lshlrev_b32_e32 v87, 16, v60
	s_waitcnt vmcnt(10)
	v_lshlrev_b32_e32 v90, 16, v62
	v_and_b32_e32 v91, 0xffff0000, v62
	v_lshlrev_b32_e32 v62, 16, v63
	v_and_b32_e32 v63, 0xffff0000, v63
	v_and_b32_e32 v89, 0xffff0000, v60
	s_waitcnt vmcnt(9)
	v_lshlrev_b32_e32 v93, 16, v65
	v_lshlrev_b32_e32 v92, 16, v64
	v_and_b32_e32 v65, 0xffff0000, v65
	v_and_b32_e32 v64, 0xffff0000, v64
	s_waitcnt vmcnt(8)
	v_and_b32_e32 v95, 0xffff0000, v66
	v_mul_f32_e32 v86, v63, v63
	v_mul_f32_e32 v88, v91, v91
	v_lshlrev_b32_e32 v94, 16, v66
	v_lshlrev_b32_e32 v66, 16, v67
	v_and_b32_e32 v67, 0xffff0000, v67
	v_pk_mul_f32 v[96:97], v[64:65], v[64:65]
	v_mov_b32_e32 v99, v87
	v_mul_f32_e32 v98, v95, v95
	v_pk_fma_f32 v[102:103], v[62:63], v[62:63], v[86:87] op_sel_hi:[1,1,0]
	v_pk_fma_f32 v[104:105], v[90:91], v[90:91], v[88:89] op_sel_hi:[1,1,0]
	v_lshlrev_b32_e32 v60, 16, v61
	v_and_b32_e32 v61, 0xffff0000, v61
	v_mul_f32_e32 v100, v67, v67
	v_pk_fma_f32 v[96:97], v[92:93], v[92:93], v[96:97]
	v_pk_fma_f32 v[106:107], v[94:95], v[94:95], v[98:99] op_sel_hi:[1,1,0]
	v_mov_b32_e32 v86, v104
	v_mov_b32_e32 v98, v102
	v_mul_f32_e32 v73, v89, v89
	v_mul_f32_e32 v108, v60, v60
	v_mul_f32_e32 v109, v61, v61
	v_pk_fma_f32 v[100:101], v[66:67], v[66:67], v[100:101] op_sel_hi:[1,1,0]
	v_pk_add_f32 v[102:103], v[104:105], v[102:103]
	v_pk_add_f32 v[96:97], v[96:97], v[96:97] op_sel:[0,1] op_sel_hi:[1,0]
	v_pk_mul_f32 v[98:99], v[86:87], v[98:99]
	v_mov_b32_e32 v107, v108
	v_mov_b32_e32 v101, v109
	v_mov_b32_e32 v97, v73
	v_mov_b32_e32 v103, v99
	v_pk_add_f32 v[100:101], v[106:107], v[100:101]
	v_pk_add_f32 v[96:97], v[102:103], v[96:97]
	v_mov_b32_e32 v88, v87
	v_pk_add_f32 v[96:97], v[96:97], v[100:101]
	s_waitcnt vmcnt(7)
	v_pk_add_f32 v[18:19], v[18:19], 1.0 op_sel_hi:[1,0]
	v_add_f32_e32 v73, v96, v97
	v_mov_b32_e32 v97, v65
	v_mov_b32_e32 v96, v93
	v_add_f32_dpp v73, v73, v73 row_ror:8 row_mask:0xf bank_mask:0xf bound_ctrl:1
	v_mov_b32_e32 v93, v64
	s_waitcnt vmcnt(6)
	v_pk_add_f32 v[22:23], v[22:23], 1.0 op_sel_hi:[1,0]
	v_add_f32_dpp v73, v73, v73 row_ror:4 row_mask:0xf bank_mask:0xf bound_ctrl:1
	v_pk_add_f32 v[20:21], v[20:21], 1.0 op_sel_hi:[1,0]
	v_pk_add_f32 v[24:25], v[24:25], 1.0 op_sel_hi:[1,0]
	v_add_f32_dpp v73, v73, v73 row_ror:2 row_mask:0xf bank_mask:0xf bound_ctrl:1
	s_waitcnt vmcnt(5)
	v_pk_add_f32 v[26:27], v[26:27], 1.0 op_sel_hi:[1,0]
	v_pk_add_f32 v[28:29], v[28:29], 1.0 op_sel_hi:[1,0]
	v_add_f32_dpp v73, v73, v73 row_ror:1 row_mask:0xf bank_mask:0xf bound_ctrl:1
	ds_bpermute_b32 v86, v1, v73
	s_waitcnt vmcnt(0)
	v_pk_add_f32 v[84:85], v[84:85], 1.0 op_sel_hi:[1,0]
	s_waitcnt lgkmcnt(0)
	v_add_f32_e32 v65, v73, v86
	ds_bpermute_b32 v73, v68, v65
	s_waitcnt lgkmcnt(0)
	v_add_f32_e32 v64, v65, v73
	v_fmamk_f32 v64, v64, 0x3a800000, v70
	v_mul_f32_e32 v65, 0x4f800000, v64
	v_cmp_gt_f32_e32 vcc, s33, v64
	s_nop 1
	v_cndmask_b32_e32 v64, v64, v65, vcc
	v_sqrt_f32_e32 v65, v64
	s_nop 0
	v_add_u32_e32 v73, -1, v65
	v_add_u32_e32 v86, 1, v65
	v_fma_f32 v87, -v73, v65, v64
	v_fma_f32 v98, -v86, v65, v64
	v_cmp_ge_f32_e64 s[8:9], 0, v87
	s_nop 1
	v_cndmask_b32_e64 v65, v65, v73, s[8:9]
	v_cmp_lt_f32_e64 s[8:9], 0, v98
	s_nop 1
	v_cndmask_b32_e64 v65, v65, v86, s[8:9]
	v_mul_f32_e32 v73, 0x37800000, v65
	v_cndmask_b32_e32 v65, v65, v73, vcc
	v_cmp_class_f32_e32 vcc, v64, v71
	s_nop 1
	v_cndmask_b32_e32 v64, v65, v64, vcc
	v_div_scale_f32 v65, s[8:9], v64, v64, 1.0
	v_rcp_f32_e32 v73, v65
	v_div_scale_f32 v86, vcc, 1.0, v64, 1.0
	v_fma_f32 v87, -v65, v73, 1.0
	v_fmac_f32_e32 v73, v87, v73
	v_mul_f32_e32 v87, v86, v73
	v_fma_f32 v98, -v65, v87, v86
	v_fmac_f32_e32 v87, v98, v73
	v_fma_f32 v65, -v65, v87, v86
	v_div_fmas_f32 v65, v65, v73, v87
	v_div_fixup_f32 v64, v65, v64, 1.0
	v_pk_mul_f32 v[86:87], v[90:91], v[64:65] op_sel_hi:[1,0]
	v_pk_mul_f32 v[62:63], v[62:63], v[64:65] op_sel_hi:[1,0]
	v_pk_mul_f32 v[90:91], v[96:97], v[64:65] op_sel_hi:[1,0]
	v_pk_mul_f32 v[92:93], v[92:93], v[64:65] op_sel_hi:[1,0]
	v_pk_mul_f32 v[66:67], v[66:67], v[64:65] op_sel_hi:[1,0]
	v_pk_mul_f32 v[94:95], v[94:95], v[64:65] op_sel_hi:[1,0]
	v_pk_mul_f32 v[60:61], v[60:61], v[64:65] op_sel_hi:[1,0]
	v_pk_mul_f32 v[64:65], v[88:89], v[64:65] op_sel_hi:[1,0]
	v_pk_mul_f32 v[86:87], v[10:11], v[86:87]
	v_pk_mul_f32 v[88:89], v[2:3], v[92:93]
	v_pk_mul_f32 v[92:93], v[6:7], v[94:95]
	v_pk_mul_f32 v[94:95], v[8:9], v[66:67]
	v_pk_mul_f32 v[96:97], v[14:15], v[64:65]
	v_pk_fma_f32 v[66:67], v[18:19], v[86:87], v[52:53]
	v_pk_add_f32 v[18:19], v[82:83], 1.0 op_sel_hi:[1,0]
	v_pk_fma_f32 v[64:65], v[22:23], v[88:89], v[56:57]
	v_pk_fma_f32 v[56:57], v[18:19], v[96:97], v[78:79]
	v_pk_mul_f32 v[62:63], v[12:13], v[62:63]
	v_pk_fma_f32 v[62:63], v[20:21], v[62:63], v[54:55]
	v_cvt_pk_bf16_f32 v18, v66, v67
	v_cvt_pk_bf16_f32 v19, v62, v63
	v_add_co_u32_e32 v20, vcc, s37, v50
	v_pk_mul_f32 v[90:91], v[4:5], v[90:91]
	s_nop 0
	v_addc_co_u32_e32 v21, vcc, 0, v51, vcc
	global_store_dwordx2 v[20:21], v[18:19], off
	v_pk_mul_f32 v[98:99], v[16:17], v[60:61]
	v_pk_fma_f32 v[60:61], v[24:25], v[90:91], v[58:59]
	v_cvt_pk_bf16_f32 v18, v64, v65
	v_pk_fma_f32 v[58:59], v[26:27], v[92:93], v[74:75]
	v_cvt_pk_bf16_f32 v19, v60, v61
	global_store_dwordx2 v[20:21], v[18:19], off offset:512
	v_pk_fma_f32 v[54:55], v[28:29], v[94:95], v[76:77]
	v_cvt_pk_bf16_f32 v18, v58, v59
	v_cvt_pk_bf16_f32 v19, v54, v55
	global_store_dwordx2 v[20:21], v[18:19], off offset:1024
	v_pk_fma_f32 v[52:53], v[84:85], v[98:99], v[80:81]
	v_cvt_pk_bf16_f32 v18, v56, v57
	v_cvt_pk_bf16_f32 v19, v52, v53
	global_store_dwordx2 v[20:21], v[18:19], off offset:1536
	global_load_dwordx4 v[18:21], v[34:35], off
	s_nop 0
	global_load_dwordx4 v[74:77], v[34:35], off offset:16
	global_load_dwordx4 v[22:25], v[34:35], off offset:32
	global_load_dwordx4 v[78:81], v[34:35], off offset:48
	global_load_dwordx4 v[26:29], v[36:37], off
	global_load_dwordx4 v[82:85], v[36:37], off offset:16
	global_load_dwordx4 v[86:89], v[36:37], off offset:32
	global_load_dwordx4 v[90:93], v[36:37], off offset:48
	global_load_dwordx4 v[94:97], v[38:39], off
	global_load_dwordx4 v[98:101], v[38:39], off offset:16
	global_load_dwordx4 v[102:105], v[38:39], off offset:32
	global_load_dwordx4 v[106:109], v[38:39], off offset:48
	global_load_dwordx4 v[110:113], v[40:41], off
	global_load_dwordx4 v[114:117], v[40:41], off offset:16
	global_load_dwordx4 v[118:121], v[40:41], off offset:32
	global_load_dwordx4 v[122:125], v[40:41], off offset:48
	global_load_dwordx4 v[126:129], v[42:43], off
	global_load_dwordx4 v[130:133], v[42:43], off offset:16
	global_load_dwordx4 v[134:137], v[42:43], off offset:32
	global_load_dwordx4 v[138:141], v[42:43], off offset:48
	global_load_dwordx4 v[142:145], v[44:45], off offset:16
	global_load_dwordx4 v[146:149], v[44:45], off
	global_load_dwordx4 v[150:153], v[44:45], off offset:48
	global_load_dwordx4 v[154:157], v[44:45], off offset:32
	s_waitcnt vmcnt(23)
	v_pk_fma_f32 v[18:19], v[18:19], v[66:67], 0 op_sel_hi:[1,0,0]
	s_waitcnt vmcnt(22)
	v_fma_f32 v180, v74, v66, 0
	v_fma_f32 v181, v75, v66, 0
	v_fma_f32 v182, v76, v66, 0
	v_fma_f32 v183, v77, v66, 0
	global_load_dwordx4 v[74:77], v[46:47], off offset:16
	global_load_dwordx4 v[158:161], v[46:47], off
	s_waitcnt vmcnt(22)
	v_fmac_f32_e32 v180, v78, v67
	v_fmac_f32_e32 v181, v79, v67
	v_fmac_f32_e32 v182, v80, v67
	v_fmac_f32_e32 v183, v81, v67
	global_load_dwordx4 v[78:81], v[46:47], off offset:48
	global_load_dwordx4 v[162:165], v[46:47], off offset:32
	global_load_dwordx4 v[166:169], v[48:49], off offset:16
	global_load_dwordx4 v[172:175], v[48:49], off
	s_waitcnt vmcnt(24)
	v_fmac_f32_e32 v180, v62, v82
	v_fmac_f32_e32 v181, v62, v83
	v_fmac_f32_e32 v182, v62, v84
	v_fmac_f32_e32 v183, v62, v85
	global_load_dwordx4 v[82:85], v[48:49], off offset:48
	global_load_dwordx4 v[176:179], v[48:49], off offset:32
	v_pk_fma_f32 v[18:19], v[22:23], v[66:67], v[18:19] op_sel:[0,1,0]
	v_fma_f32 v73, v20, v66, 0
	v_pk_fma_f32 v[18:19], v[62:63], v[26:27], v[18:19] op_sel_hi:[0,1,1]
	s_waitcnt vmcnt(25)
	v_pk_fma_f32 v[18:19], v[62:63], v[86:87], v[18:19] op_sel:[1,0,0]
	v_fma_f32 v171, v21, v66, 0
	s_waitcnt vmcnt(23)
	v_pk_fma_f32 v[18:19], v[64:65], v[94:95], v[18:19] op_sel_hi:[0,1,1]
	v_fmac_f32_e32 v73, v24, v67
	v_fmac_f32_e32 v171, v25, v67
	s_waitcnt vmcnt(21)
	v_pk_fma_f32 v[18:19], v[64:65], v[102:103], v[18:19] op_sel:[1,0,0]
	v_fmac_f32_e32 v73, v62, v28
	v_fmac_f32_e32 v171, v62, v29
	s_waitcnt vmcnt(19)
	v_pk_fma_f32 v[18:19], v[60:61], v[110:111], v[18:19] op_sel_hi:[0,1,1]
	v_fmac_f32_e32 v73, v63, v88
	v_fmac_f32_e32 v171, v63, v89
	v_fmac_f32_e32 v180, v63, v90
	v_fmac_f32_e32 v181, v63, v91
	v_fmac_f32_e32 v182, v63, v92
	v_fmac_f32_e32 v183, v63, v93
	s_waitcnt vmcnt(17)
	v_pk_fma_f32 v[18:19], v[60:61], v[118:119], v[18:19] op_sel:[1,0,0]
	v_fmac_f32_e32 v73, v64, v96
	v_fmac_f32_e32 v171, v64, v97
	v_fmac_f32_e32 v180, v64, v98
	v_fmac_f32_e32 v181, v64, v99
	v_fmac_f32_e32 v182, v64, v100
	v_fmac_f32_e32 v183, v64, v101
	s_waitcnt vmcnt(15)
	v_pk_fma_f32 v[18:19], v[58:59], v[126:127], v[18:19] op_sel_hi:[0,1,1]
	v_fmac_f32_e32 v73, v65, v104
	v_fmac_f32_e32 v171, v65, v105
	v_fmac_f32_e32 v180, v65, v106
	v_fmac_f32_e32 v181, v65, v107
	v_fmac_f32_e32 v182, v65, v108
	v_fmac_f32_e32 v183, v65, v109
	s_waitcnt vmcnt(13)
	v_pk_fma_f32 v[18:19], v[58:59], v[134:135], v[18:19] op_sel:[1,0,0]
	v_fmac_f32_e32 v73, v60, v112
	v_fmac_f32_e32 v171, v60, v113
	v_fmac_f32_e32 v180, v60, v114
	v_fmac_f32_e32 v181, v60, v115
	v_fmac_f32_e32 v182, v60, v116
	v_fmac_f32_e32 v183, v60, v117
	s_waitcnt vmcnt(10)
	v_pk_fma_f32 v[18:19], v[54:55], v[146:147], v[18:19] op_sel_hi:[0,1,1]
	v_fmac_f32_e32 v73, v61, v120
	v_fmac_f32_e32 v171, v61, v121
	v_fmac_f32_e32 v180, v61, v122
	v_fmac_f32_e32 v181, v61, v123
	v_fmac_f32_e32 v182, v61, v124
	v_fmac_f32_e32 v183, v61, v125
	s_waitcnt vmcnt(8)
	v_pk_fma_f32 v[18:19], v[54:55], v[154:155], v[18:19] op_sel:[1,0,0]
	v_fmac_f32_e32 v73, v58, v128
	v_fmac_f32_e32 v171, v58, v129
	v_fmac_f32_e32 v180, v58, v130
	v_fmac_f32_e32 v181, v58, v131
	v_fmac_f32_e32 v182, v58, v132
	v_fmac_f32_e32 v183, v58, v133
	v_fmac_f32_e32 v73, v59, v136
	v_fmac_f32_e32 v171, v59, v137
	v_fmac_f32_e32 v180, v59, v138
	v_fmac_f32_e32 v181, v59, v139
	v_fmac_f32_e32 v182, v59, v140
	v_fmac_f32_e32 v183, v59, v141
	v_fmac_f32_e32 v73, v54, v148
	v_fmac_f32_e32 v171, v54, v149
	v_fmac_f32_e32 v180, v54, v142
	v_fmac_f32_e32 v181, v54, v143
	v_fmac_f32_e32 v182, v54, v144
	v_fmac_f32_e32 v183, v54, v145
	v_fmac_f32_e32 v73, v55, v156
	v_fmac_f32_e32 v171, v55, v157
	v_fmac_f32_e32 v180, v55, v150
	s_waitcnt vmcnt(6)
	v_pk_fma_f32 v[18:19], v[56:57], v[158:159], v[18:19] op_sel_hi:[0,1,1]
	v_fmac_f32_e32 v181, v55, v151
	v_fmac_f32_e32 v182, v55, v152
	v_fmac_f32_e32 v183, v55, v153
	v_mov_b32_e32 v20, 0
	s_waitcnt vmcnt(4)
	v_pk_fma_f32 v[18:19], v[56:57], v[162:163], v[18:19] op_sel:[1,0,0]
	v_mov_b32_e32 v21, 0
	s_waitcnt vmcnt(2)
	v_pk_fma_f32 v[18:19], v[52:53], v[172:173], v[18:19] op_sel_hi:[0,1,1]
	v_fmac_f32_e32 v73, v56, v160
	v_fmac_f32_e32 v171, v56, v161
	v_fmac_f32_e32 v180, v56, v74
	s_waitcnt vmcnt(0)
	v_pk_fma_f32 v[18:19], v[52:53], v[176:177], v[18:19] op_sel:[1,0,0]
	v_fmac_f32_e32 v181, v56, v75
	v_fmac_f32_e32 v182, v56, v76
	v_fmac_f32_e32 v183, v56, v77
	v_mov_b32_dpp v20, v18 row_ror:8 row_mask:0xf bank_mask:0xf
	v_mov_b32_dpp v21, v19 row_ror:8 row_mask:0xf bank_mask:0xf
	v_fmac_f32_e32 v73, v57, v164
	v_fmac_f32_e32 v171, v57, v165
	v_fmac_f32_e32 v180, v57, v78
	v_fmac_f32_e32 v181, v57, v79
	v_fmac_f32_e32 v182, v57, v80
	v_fmac_f32_e32 v183, v57, v81
	v_pk_add_f32 v[18:19], v[18:19], v[20:21]
	v_mov_b32_e32 v20, 0
	v_mov_b32_e32 v21, 0
	v_fmac_f32_e32 v73, v52, v174
	v_fmac_f32_e32 v171, v52, v175
	v_fmac_f32_e32 v180, v52, v166
	v_fmac_f32_e32 v181, v52, v167
	v_fmac_f32_e32 v182, v52, v168
	v_fmac_f32_e32 v183, v52, v169
	v_mov_b32_dpp v20, v18 row_ror:4 row_mask:0xf bank_mask:0xf
	v_mov_b32_dpp v21, v19 row_ror:4 row_mask:0xf bank_mask:0xf
	v_fmac_f32_e32 v73, v53, v178
	v_fmac_f32_e32 v171, v53, v179
	v_pk_add_f32 v[18:19], v[18:19], v[20:21]
	v_mov_b32_e32 v20, 0
	v_mov_b32_e32 v21, 0
	v_fmac_f32_e32 v180, v53, v82
	v_fmac_f32_e32 v181, v53, v83
	v_fmac_f32_e32 v182, v53, v84
	v_fmac_f32_e32 v183, v53, v85
	v_mov_b32_dpp v20, v18 row_ror:2 row_mask:0xf bank_mask:0xf
	v_mov_b32_dpp v21, v19 row_ror:2 row_mask:0xf bank_mask:0xf
	v_add_f32_dpp v22, v73, v73 row_ror:8 row_mask:0xf bank_mask:0xf bound_ctrl:1
	v_add_f32_dpp v24, v171, v171 row_ror:8 row_mask:0xf bank_mask:0xf bound_ctrl:1
	v_add_f32_dpp v26, v180, v180 row_ror:8 row_mask:0xf bank_mask:0xf bound_ctrl:1
	v_add_f32_dpp v28, v181, v181 row_ror:8 row_mask:0xf bank_mask:0xf bound_ctrl:1
	v_add_f32_dpp v52, v182, v182 row_ror:8 row_mask:0xf bank_mask:0xf bound_ctrl:1
	v_add_f32_dpp v54, v183, v183 row_ror:8 row_mask:0xf bank_mask:0xf bound_ctrl:1
	v_pk_add_f32 v[18:19], v[18:19], v[20:21]
	v_mov_b32_e32 v20, 0
	v_mov_b32_e32 v21, 0
	v_add_f32_dpp v22, v22, v22 row_ror:4 row_mask:0xf bank_mask:0xf bound_ctrl:1
	v_add_f32_dpp v24, v24, v24 row_ror:4 row_mask:0xf bank_mask:0xf bound_ctrl:1
	v_add_f32_dpp v26, v26, v26 row_ror:4 row_mask:0xf bank_mask:0xf bound_ctrl:1
	v_add_f32_dpp v28, v28, v28 row_ror:4 row_mask:0xf bank_mask:0xf bound_ctrl:1
	v_add_f32_dpp v52, v52, v52 row_ror:4 row_mask:0xf bank_mask:0xf bound_ctrl:1
	v_add_f32_dpp v54, v54, v54 row_ror:4 row_mask:0xf bank_mask:0xf bound_ctrl:1
	v_mov_b32_dpp v20, v18 row_ror:1 row_mask:0xf bank_mask:0xf
	v_mov_b32_dpp v21, v19 row_ror:1 row_mask:0xf bank_mask:0xf
	v_add_f32_dpp v22, v22, v22 row_ror:2 row_mask:0xf bank_mask:0xf bound_ctrl:1
	v_add_f32_dpp v24, v24, v24 row_ror:2 row_mask:0xf bank_mask:0xf bound_ctrl:1
	v_add_f32_dpp v26, v26, v26 row_ror:2 row_mask:0xf bank_mask:0xf bound_ctrl:1
	v_add_f32_dpp v28, v28, v28 row_ror:2 row_mask:0xf bank_mask:0xf bound_ctrl:1
	v_add_f32_dpp v52, v52, v52 row_ror:2 row_mask:0xf bank_mask:0xf bound_ctrl:1
	v_add_f32_dpp v54, v54, v54 row_ror:2 row_mask:0xf bank_mask:0xf bound_ctrl:1
	v_pk_add_f32 v[18:19], v[18:19], v[20:21]
	v_add_f32_dpp v22, v22, v22 row_ror:1 row_mask:0xf bank_mask:0xf bound_ctrl:1
	v_add_f32_dpp v24, v24, v24 row_ror:1 row_mask:0xf bank_mask:0xf bound_ctrl:1
	v_add_f32_dpp v26, v26, v26 row_ror:1 row_mask:0xf bank_mask:0xf bound_ctrl:1
	v_add_f32_dpp v28, v28, v28 row_ror:1 row_mask:0xf bank_mask:0xf bound_ctrl:1
	v_add_f32_dpp v52, v52, v52 row_ror:1 row_mask:0xf bank_mask:0xf bound_ctrl:1
	v_add_f32_dpp v54, v54, v54 row_ror:1 row_mask:0xf bank_mask:0xf bound_ctrl:1
	ds_bpermute_b32 v20, v1, v18
	ds_bpermute_b32 v21, v1, v19
	ds_bpermute_b32 v23, v1, v22
	ds_bpermute_b32 v25, v1, v24
	ds_bpermute_b32 v27, v1, v26
	ds_bpermute_b32 v29, v1, v28
	ds_bpermute_b32 v53, v1, v52
	ds_bpermute_b32 v55, v1, v54
	s_waitcnt lgkmcnt(6)
	v_pk_add_f32 v[18:19], v[18:19], v[20:21]
	s_waitcnt lgkmcnt(5)
	v_add_f32_e32 v22, v22, v23
	s_waitcnt lgkmcnt(4)
	v_add_f32_e32 v24, v24, v25
	s_waitcnt lgkmcnt(3)
	v_add_f32_e32 v26, v26, v27
	s_waitcnt lgkmcnt(2)
	v_add_f32_e32 v28, v28, v29
	s_waitcnt lgkmcnt(1)
	v_add_f32_e32 v52, v52, v53
	s_waitcnt lgkmcnt(0)
	v_add_f32_e32 v54, v54, v55
	ds_bpermute_b32 v20, v68, v18
	ds_bpermute_b32 v21, v68, v19
	ds_bpermute_b32 v23, v68, v22
	ds_bpermute_b32 v25, v68, v24
	ds_bpermute_b32 v27, v68, v26
	ds_bpermute_b32 v29, v68, v28
	ds_bpermute_b32 v53, v68, v52
	ds_bpermute_b32 v55, v68, v54
	s_and_saveexec_b64 s[50:51], s[6:7]
	s_cbranch_execz .LBB0_2721
	s_waitcnt lgkmcnt(6)
	v_pk_add_f32 v[18:19], v[18:19], v[20:21]
	s_waitcnt lgkmcnt(5)
	v_add_f32_e32 v22, v22, v23
	v_cmp_gt_f32_e32 vcc, v19, v18
	s_waitcnt lgkmcnt(4)
	v_add_f32_e32 v24, v24, v25
	s_waitcnt lgkmcnt(3)
	v_add_f32_e32 v26, v26, v27
	v_cndmask_b32_e32 v20, v18, v19, vcc
	v_cmp_gt_f32_e64 s[8:9], v22, v20
	s_waitcnt lgkmcnt(2)
	v_add_f32_e32 v28, v28, v29
	v_cndmask_b32_e64 v21, 0, 1, vcc
	v_cndmask_b32_e64 v20, v20, v22, s[8:9]
	v_cmp_gt_f32_e64 s[10:11], v24, v20
	v_cndmask_b32_e64 v21, v21, 2, s[8:9]
	s_waitcnt lgkmcnt(1)
	v_add_f32_e32 v52, v52, v53
	v_cndmask_b32_e64 v20, v20, v24, s[10:11]
	v_cmp_gt_f32_e64 s[12:13], v26, v20
	v_cndmask_b32_e64 v21, v21, 3, s[10:11]
	s_waitcnt lgkmcnt(0)
	v_add_f32_e32 v54, v54, v55
	v_cndmask_b32_e64 v20, v20, v26, s[12:13]
	v_cmp_gt_f32_e64 s[14:15], v28, v20
	v_cndmask_b32_e64 v21, v21, 4, s[12:13]
	v_cmp_nlt_f32_e64 s[20:21], s41, v18
	v_cndmask_b32_e64 v20, v20, v28, s[14:15]
	v_cmp_gt_f32_e64 s[16:17], v52, v20
	v_cndmask_b32_e64 v21, v21, 5, s[14:15]
	s_nop 0
	v_cndmask_b32_e64 v20, v20, v52, s[16:17]
	v_cndmask_b32_e64 v21, v21, 6, s[16:17]
	v_cmp_ngt_f32_e32 vcc, v54, v20
	s_and_b64 s[22:23], s[16:17], vcc
	s_nop 0
	v_cndmask_b32_e32 v21, 7, v21, vcc
	v_cmp_eq_u32_e64 s[18:19], 0, v21
	s_or_b64 s[18:19], s[18:19], s[20:21]
	v_cmp_ne_u32_e64 s[16:17], 1, v21
	v_cndmask_b32_e64 v18, v18, v72, s[18:19]
	v_cmp_gt_f32_e64 s[20:21], v19, v18
	s_and_b64 s[16:17], s[16:17], s[20:21]
	v_cndmask_b32_e64 v18, v18, v19, s[16:17]
	v_cmp_ne_u32_e64 s[14:15], 2, v21
	v_cmp_gt_f32_e64 s[20:21], v22, v18
	s_and_b64 s[14:15], s[14:15], s[20:21]
	v_cndmask_b32_e64 v18, v18, v22, s[14:15]
	v_cmp_ne_u32_e64 s[12:13], 3, v21
	v_cmp_gt_f32_e64 s[20:21], v24, v18
	s_and_b64 s[12:13], s[12:13], s[20:21]
	v_cndmask_b32_e64 v18, v18, v24, s[12:13]
	v_cmp_ne_u32_e64 s[10:11], 4, v21
	v_cmp_gt_f32_e64 s[20:21], v26, v18
	s_and_b64 s[10:11], s[10:11], s[20:21]
	v_cndmask_b32_e64 v18, v18, v26, s[10:11]
	v_cmp_ne_u32_e64 s[8:9], 5, v21
	v_cmp_gt_f32_e64 s[20:21], v28, v18
	s_and_b64 s[8:9], s[8:9], s[20:21]
	v_cndmask_b32_e64 v18, v18, v28, s[8:9]
	v_cmp_ngt_f32_e64 s[20:21], v52, v18
	s_or_b64 s[20:21], s[22:23], s[20:21]
	v_cndmask_b32_e32 v20, v54, v20, vcc
	v_cndmask_b32_e64 v18, v52, v18, s[20:21]
	v_cmp_gt_f32_e64 s[22:23], v54, v18
	s_and_b64 s[22:23], vcc, s[22:23]
	v_cndmask_b32_e64 v19, 0, -1, s[18:19]
	v_cndmask_b32_e64 v18, v18, v54, s[22:23]
	v_sub_f32_e32 v18, v18, v20
	v_mul_f32_e32 v18, 0x3fb8aa3b, v18
	v_exp_f32_e32 v18, v18
	v_cndmask_b32_e64 v19, v19, 1, s[16:17]
	v_cndmask_b32_e64 v19, v19, 2, s[14:15]
	v_cndmask_b32_e64 v19, v19, 3, s[12:13]
	v_add_f32_e32 v20, 1.0, v18
	v_cndmask_b32_e64 v19, v19, 4, s[10:11]
	v_div_scale_f32 v22, s[10:11], v20, v20, 1.0
	v_rcp_f32_e32 v23, v22
	v_lshl_add_u32 v25, v21, 2, s3
	ds_read_b32 v26, v25
	v_cndmask_b32_e64 v19, v19, 5, s[8:9]
	v_fma_f32 v24, -v22, v23, 1.0
	v_fmac_f32_e32 v23, v24, v23
	v_div_scale_f32 v24, vcc, 1.0, v20, 1.0
	v_mul_f32_e32 v27, v24, v23
	v_fma_f32 v28, -v22, v27, v24
	v_cndmask_b32_e64 v19, 6, v19, s[20:21]
	v_fmac_f32_e32 v27, v28, v23
	v_cndmask_b32_e64 v19, v19, 7, s[22:23]
	v_fma_f32 v22, -v22, v27, v24
	s_waitcnt lgkmcnt(0)
	v_add_u32_e32 v24, 1, v26
	ds_write_b32 v25, v24
	v_lshl_add_u32 v24, v19, 2, s3
	ds_read_b32 v25, v24
	s_add_i32 s8, s46, -1
	s_ashr_i32 s9, s8, 31
	s_lshl_b64 s[8:9], s[8:9], 2
	v_div_fmas_f32 v22, v22, v23, v27
	s_add_u32 s10, s78, s8
	v_readlane_b32 s13, v255, 7
	v_div_fixup_f32 v20, v22, v20, 1.0
	s_waitcnt lgkmcnt(0)
	v_add_u32_e32 v22, 1, v25
	s_addc_u32 s11, s13, s9
	s_ashr_i32 s47, s46, 31
	ds_write_b32 v24, v22
	global_store_dword v69, v21, s[10:11]
	s_lshl_b64 s[10:11], s[46:47], 2
	s_add_u32 s12, s78, s10
	s_addc_u32 s13, s13, s11
	global_store_dword v69, v19, s[12:13]
	s_add_u32 s12, s35, s8
	s_addc_u32 s13, s74, s9
	global_store_dword v69, v20, s[12:13]
	s_add_u32 s12, s35, s10
	v_mul_f32_e32 v18, v18, v20
	s_addc_u32 s13, s74, s11
	global_store_dword v69, v18, s[12:13]
	v_readlane_b32 s12, v255, 8
	s_add_u32 s8, s12, s8
	v_readlane_b32 s13, v255, 9
	s_addc_u32 s9, s13, s9
	global_store_dword v69, v26, s[8:9]
	s_add_u32 s8, s12, s10
	s_addc_u32 s9, s13, s11
	global_store_dword v69, v25, s[8:9]
	s_branch .LBB0_2721
